# v9: v6 + removed the no-op s_setprio 0/1 pairs between the two 16-MFMA clusters of every GEMM super-phase
# baseline (speedup 1.0000x reference)
; #define PG8_STAGE(bufoff, gbase, voff) do { _Pragma("unroll") for (int _i = 0; _i < 2; ++_i) \
;         __builtin_amdgcn_global_load_lds((const unsigned*)((const char*)(gbase) + (voff)[_i]), (PG8_LAS unsigned*)(lds + (bufoff) + ldsw + _i * 8192), 16, 0, 0); } while (0)
; #define PG8_LDA(dst, b, h) do { _Pragma("unroll") for (int m = 0; m < 4; ++m) _Pragma("unroll") for (int k = 0; k < 2; ++k) dst[m][k] = *(const PG8_LAS bf16x8*)(lds + PG8_SA(b, h) + aoff + m * 2048 + k * 1024); } while (0)
; #define PG8_LDB(dst, b, h) do { _Pragma("unroll") for (int n = 0; n < 2; ++n) _Pragma("unroll") for (int k = 0; k < 2; ++k) dst[n][k] = *(const PG8_LAS bf16x8*)(lds + PG8_SB(b, h) + boff + n * 2048 + k * 1024); } while (0)
; #define PG8_MMA(ai, bj, At, Bt) do { __builtin_amdgcn_s_setprio(1); _Pragma("unroll") for (int m = 0; m < 4; ++m) _Pragma("unroll") for (int n = 0; n < 2; ++n) _Pragma("unroll") for (int k = 0; k < 2; ++k) \
;         acc[ai][bj][m][n] = __builtin_amdgcn_mfma_f32_16x16x32_bf16(Bt[n][k], At[m][k], acc[ai][bj][m][n], 0, 0, 0); __builtin_amdgcn_s_setprio(0); } while (0)
; #define PG8_WAIT_V(n) asm volatile("s_waitcnt vmcnt(" #n ")" ::: "memory")
; #define PG8_WAIT_L(n) asm volatile("s_waitcnt lgkmcnt(" #n ")" ::: "memory")
; #define PG8_BAR __builtin_amdgcn_s_barrier()
; #define PG8_SCHED __builtin_amdgcn_sched_barrier(0)
; template <class Epi, class Sched, bool ALIGN_EPI = false, bool SP2 = false>
; __device__ __forceinline__ void gemm_phase(PG8_LAS unsigned char* lds, const Gemm g, const Sched& S, const Epi& E) {
;     ...
;             PG8_LDB(B0, 0, 0); PG8_LDB(B1, 0, 1); PG8_SCHED; PG8_LDA(At, 0, 0); PG8_STAGE(PG8_SA(1, 1), a1 + hstep, voffA);
;             PG8_WAIT_V(8); PG8_WAIT_L(0); PG8_BAR; PG8_MMA(0, 0, At, B0); PG8_MMA(0, 1, At, B1); PG8_BAR; PG8_SCHED;
;             PG8_LDA(At, 0, 1); PG8_STAGE(PG8_SB(0, 0), b2, voffB); PG8_STAGE(PG8_SB(0, 1), b2 + hstep, voffB); PG8_STAGE(PG8_SA(0, 0), a2, voffA);
;             PG8_WAIT_V(8); PG8_WAIT_L(0); PG8_BAR; PG8_MMA(1, 0, At, B0); PG8_MMA(1, 1, At, B1); PG8_BAR; PG8_SCHED;
.LBB0_230:
	ds_read_b128 v[152:155], v149
	ds_read_b128 v[156:159], v149 offset:1024
	ds_read_b128 v[160:163], v149 offset:2048
	ds_read_b128 v[164:167], v149 offset:3072
	ds_read_b128 v[168:171], v150
	ds_read_b128 v[172:175], v150 offset:1024
	ds_read_b128 v[176:179], v150 offset:2048
	ds_read_b128 v[180:183], v150 offset:3072
	s_add_u32 s28, s26, 0xfff80080
	s_addc_u32 s29, s27, -1
	s_cmp_eq_u32 s78, 28
	s_cselect_b32 s35, s15, s29
	s_cselect_b32 s34, s60, s28
	s_cselect_b32 s29, s13, s63
	s_cselect_b32 s28, s61, s62
	v_lshl_add_u64 v[216:217], s[26:27], 0, v[138:139]
	s_add_i32 m0, s3, 0xc000
	ds_read_b128 v[184:187], v151
	ds_read_b128 v[188:191], v151 offset:1024
	ds_read_b128 v[192:195], v151 offset:2048
	ds_read_b128 v[196:199], v151 offset:3072
	ds_read_b128 v[200:203], v151 offset:4096
	ds_read_b128 v[204:207], v151 offset:5120
	ds_read_b128 v[208:211], v151 offset:6144
	ds_read_b128 v[212:215], v151 offset:7168
	global_load_lds_dwordx4 v[216:217], off
	v_lshl_add_u64 v[216:217], s[26:27], 0, v[140:141]
	s_add_i32 m0, s3, 0xe000
	s_nop 0
	global_load_lds_dwordx4 v[216:217], off
	s_waitcnt vmcnt(8)
	s_waitcnt lgkmcnt(0)
	s_barrier
	s_setprio 1
	s_waitcnt lgkmcnt(0)
	v_mfma_f32_16x16x32_bf16 v[126:129], v[152:155], v[184:187], v[126:129]
	v_mfma_f32_16x16x32_bf16 v[122:125], v[160:163], v[184:187], v[122:125]
	v_mfma_f32_16x16x32_bf16 v[118:121], v[152:155], v[192:195], v[118:121]
	v_mfma_f32_16x16x32_bf16 v[114:117], v[160:163], v[192:195], v[114:117]
	v_mfma_f32_16x16x32_bf16 v[102:105], v[152:155], v[200:203], v[102:105]
	v_mfma_f32_16x16x32_bf16 v[98:101], v[160:163], v[200:203], v[98:101]
	v_mfma_f32_16x16x32_bf16 v[86:89], v[152:155], v[208:211], v[86:89]
	v_mfma_f32_16x16x32_bf16 v[82:85], v[160:163], v[208:211], v[82:85]
	v_mfma_f32_16x16x32_bf16 v[126:129], v[156:159], v[188:191], v[126:129]
	v_mfma_f32_16x16x32_bf16 v[122:125], v[164:167], v[188:191], v[122:125]
	v_mfma_f32_16x16x32_bf16 v[118:121], v[156:159], v[196:199], v[118:121]
	v_mfma_f32_16x16x32_bf16 v[114:117], v[164:167], v[196:199], v[114:117]
	v_mfma_f32_16x16x32_bf16 v[102:105], v[156:159], v[204:207], v[102:105]
	v_mfma_f32_16x16x32_bf16 v[98:101], v[164:167], v[204:207], v[98:101]
	v_mfma_f32_16x16x32_bf16 v[86:89], v[156:159], v[212:215], v[86:89]
	v_mfma_f32_16x16x32_bf16 v[82:85], v[164:167], v[212:215], v[82:85]
	v_mfma_f32_16x16x32_bf16 v[110:113], v[168:171], v[184:187], v[110:113]
	v_mfma_f32_16x16x32_bf16 v[106:109], v[176:179], v[184:187], v[106:109]
	v_mfma_f32_16x16x32_bf16 v[94:97], v[168:171], v[192:195], v[94:97]
	v_mfma_f32_16x16x32_bf16 v[90:93], v[176:179], v[192:195], v[90:93]
	v_mfma_f32_16x16x32_bf16 v[78:81], v[168:171], v[200:203], v[78:81]
	v_mfma_f32_16x16x32_bf16 v[74:77], v[176:179], v[200:203], v[74:77]
	v_mfma_f32_16x16x32_bf16 v[70:73], v[168:171], v[208:211], v[70:73]
	v_mfma_f32_16x16x32_bf16 v[66:69], v[176:179], v[208:211], v[66:69]
	v_mfma_f32_16x16x32_bf16 v[110:113], v[172:175], v[188:191], v[110:113]
	v_mfma_f32_16x16x32_bf16 v[106:109], v[180:183], v[188:191], v[106:109]
	v_mfma_f32_16x16x32_bf16 v[94:97], v[172:175], v[196:199], v[94:97]
	v_mfma_f32_16x16x32_bf16 v[90:93], v[180:183], v[196:199], v[90:93]
	v_mfma_f32_16x16x32_bf16 v[78:81], v[172:175], v[204:207], v[78:81]
	v_mfma_f32_16x16x32_bf16 v[74:77], v[180:183], v[204:207], v[74:77]
	v_mfma_f32_16x16x32_bf16 v[70:73], v[172:175], v[212:215], v[70:73]
	v_mfma_f32_16x16x32_bf16 v[66:69], v[180:183], v[212:215], v[66:69]
	s_setprio 0
	s_barrier
	s_add_i32 s79, s56, s2
	v_lshl_add_u64 v[216:217], s[28:29], 0, v[134:135]
	s_mov_b32 m0, s79
	ds_read_b128 v[184:187], v151 offset:16384
	ds_read_b128 v[188:191], v151 offset:17408
	ds_read_b128 v[192:195], v151 offset:18432
	ds_read_b128 v[196:199], v151 offset:19456
	ds_read_b128 v[200:203], v151 offset:20480
	ds_read_b128 v[204:207], v151 offset:21504
	ds_read_b128 v[208:211], v151 offset:22528
	ds_read_b128 v[212:215], v151 offset:23552
	global_load_lds_dwordx4 v[216:217], off
	s_add_i32 m0, s79, 0x2000
	s_add_u32 s96, s28, 0x80000
	v_lshl_add_u64 v[218:219], s[28:29], 0, v[130:131]
	s_addc_u32 s97, s29, 0
	s_add_i32 s79, s57, s2
	global_load_lds_dwordx4 v[218:219], off
	v_lshl_add_u64 v[220:221], s[96:97], 0, v[134:135]
	s_mov_b32 m0, s79
	v_lshl_add_u64 v[222:223], s[34:35], 0, v[132:133]
	global_load_lds_dwordx4 v[220:221], off
	v_lshl_add_u64 v[220:221], s[96:97], 0, v[130:131]
	s_add_i32 m0, s79, 0x2000
	s_nop 0
	global_load_lds_dwordx4 v[220:221], off
	v_lshl_add_u64 v[220:221], s[34:35], 0, v[136:137]
	s_mov_b32 m0, s3
	s_nop 0
	global_load_lds_dwordx4 v[220:221], off
	s_mov_b32 m0, s11
	s_nop 0
	global_load_lds_dwordx4 v[222:223], off
	s_waitcnt vmcnt(8)
	s_waitcnt lgkmcnt(0)
	s_barrier
; #define PG8_STAGE(bufoff, gbase, voff) do { _Pragma("unroll") for (int _i = 0; _i < 2; ++_i) \
;         __builtin_amdgcn_global_load_lds((const unsigned*)((const char*)(gbase) + (voff)[_i]), (PG8_LAS unsigned*)(lds + (bufoff) + ldsw + _i * 8192), 16, 0, 0); } while (0)
; #define PG8_LDA(dst, b, h) do { _Pragma("unroll") for (int m = 0; m < 4; ++m) _Pragma("unroll") for (int k = 0; k < 2; ++k) dst[m][k] = *(const PG8_LAS bf16x8*)(lds + PG8_SA(b, h) + aoff + m * 2048 + k * 1024); } while (0)
; #define PG8_LDB(dst, b, h) do { _Pragma("unroll") for (int n = 0; n < 2; ++n) _Pragma("unroll") for (int k = 0; k < 2; ++k) dst[n][k] = *(const PG8_LAS bf16x8*)(lds + PG8_SB(b, h) + boff + n * 2048 + k * 1024); } while (0)
; #define PG8_MMA(ai, bj, At, Bt) do { __builtin_amdgcn_s_setprio(1); _Pragma("unroll") for (int m = 0; m < 4; ++m) _Pragma("unroll") for (int n = 0; n < 2; ++n) _Pragma("unroll") for (int k = 0; k < 2; ++k) \
;         acc[ai][bj][m][n] = __builtin_amdgcn_mfma_f32_16x16x32_bf16(Bt[n][k], At[m][k], acc[ai][bj][m][n], 0, 0, 0); __builtin_amdgcn_s_setprio(0); } while (0)
; #define PG8_WAIT_V(n) asm volatile("s_waitcnt vmcnt(" #n ")" ::: "memory")
; #define PG8_WAIT_L(n) asm volatile("s_waitcnt lgkmcnt(" #n ")" ::: "memory")
; #define PG8_BAR __builtin_amdgcn_s_barrier()
; #define PG8_SCHED __builtin_amdgcn_sched_barrier(0)
; template <class Epi, class Sched, bool ALIGN_EPI = false, bool SP2 = false>
; __device__ __forceinline__ void gemm_phase(PG8_LAS unsigned char* lds, const Gemm g, const Sched& S, const Epi& E) {
;     ...
;             PG8_WAIT_V(8); PG8_WAIT_L(0); PG8_BAR; PG8_MMA(1, 0, At, B0); PG8_MMA(1, 1, At, B1); PG8_BAR; PG8_SCHED;
;             PG8_LDB(B0, 1, 0); PG8_LDB(B1, 1, 1); PG8_SCHED; PG8_LDA(At, 1, 0); PG8_STAGE(PG8_SA(0, 1), a2 + hstep, voffA);
;             PG8_WAIT_V(8); PG8_WAIT_L(0); PG8_BAR; PG8_MMA(0, 0, At, B0); PG8_MMA(0, 1, At, B1); PG8_BAR; PG8_SCHED;
;             PG8_LDA(At, 1, 1); PG8_STAGE(PG8_SB(1, 0), b3, voffB); PG8_STAGE(PG8_SB(1, 1), b3 + hstep, voffB); PG8_STAGE(PG8_SA(1, 0), a3, voffA);
	s_setprio 1
	s_waitcnt lgkmcnt(0)
	v_mfma_f32_16x16x32_bf16 v[62:65], v[152:155], v[184:187], v[62:65]
	v_mfma_f32_16x16x32_bf16 v[58:61], v[160:163], v[184:187], v[58:61]
	v_mfma_f32_16x16x32_bf16 v[54:57], v[152:155], v[192:195], v[54:57]
	v_mfma_f32_16x16x32_bf16 v[50:53], v[160:163], v[192:195], v[50:53]
	v_mfma_f32_16x16x32_bf16 v[38:41], v[152:155], v[200:203], v[38:41]
	v_mfma_f32_16x16x32_bf16 v[34:37], v[160:163], v[200:203], v[34:37]
	v_mfma_f32_16x16x32_bf16 v[22:25], v[152:155], v[208:211], v[22:25]
	v_mfma_f32_16x16x32_bf16 v[18:21], v[160:163], v[208:211], v[18:21]
	v_mfma_f32_16x16x32_bf16 v[62:65], v[156:159], v[188:191], v[62:65]
	v_mfma_f32_16x16x32_bf16 v[58:61], v[164:167], v[188:191], v[58:61]
	v_mfma_f32_16x16x32_bf16 v[54:57], v[156:159], v[196:199], v[54:57]
	v_mfma_f32_16x16x32_bf16 v[50:53], v[164:167], v[196:199], v[50:53]
	v_mfma_f32_16x16x32_bf16 v[38:41], v[156:159], v[204:207], v[38:41]
	v_mfma_f32_16x16x32_bf16 v[34:37], v[164:167], v[204:207], v[34:37]
	v_mfma_f32_16x16x32_bf16 v[22:25], v[156:159], v[212:215], v[22:25]
	v_mfma_f32_16x16x32_bf16 v[18:21], v[164:167], v[212:215], v[18:21]
	v_mfma_f32_16x16x32_bf16 v[46:49], v[168:171], v[184:187], v[46:49]
	v_mfma_f32_16x16x32_bf16 v[42:45], v[176:179], v[184:187], v[42:45]
	v_mfma_f32_16x16x32_bf16 v[30:33], v[168:171], v[192:195], v[30:33]
	v_mfma_f32_16x16x32_bf16 v[26:29], v[176:179], v[192:195], v[26:29]
	v_mfma_f32_16x16x32_bf16 v[14:17], v[168:171], v[200:203], v[14:17]
	v_mfma_f32_16x16x32_bf16 v[10:13], v[176:179], v[200:203], v[10:13]
	v_mfma_f32_16x16x32_bf16 v[6:9], v[168:171], v[208:211], v[6:9]
	v_mfma_f32_16x16x32_bf16 v[2:5], v[176:179], v[208:211], v[2:5]
	v_mfma_f32_16x16x32_bf16 v[46:49], v[172:175], v[188:191], v[46:49]
	v_mfma_f32_16x16x32_bf16 v[42:45], v[180:183], v[188:191], v[42:45]
	v_mfma_f32_16x16x32_bf16 v[30:33], v[172:175], v[196:199], v[30:33]
	v_mfma_f32_16x16x32_bf16 v[26:29], v[180:183], v[196:199], v[26:29]
	v_mfma_f32_16x16x32_bf16 v[14:17], v[172:175], v[204:207], v[14:17]
	v_mfma_f32_16x16x32_bf16 v[10:13], v[180:183], v[204:207], v[10:13]
	v_mfma_f32_16x16x32_bf16 v[6:9], v[172:175], v[212:215], v[6:9]
	v_mfma_f32_16x16x32_bf16 v[2:5], v[180:183], v[212:215], v[2:5]
	s_setprio 0
	s_barrier
	s_add_i32 s79, 0, 0x18000
	s_add_i32 s96, 0, 0x1c000
	v_add_u32_e32 v164, s79, v147
	v_add_u32_e32 v180, s96, v147
	ds_read_b128 v[152:155], v164
	ds_read_b128 v[156:159], v164 offset:1024
	ds_read_b128 v[160:163], v164 offset:2048
	ds_read_b128 v[164:167], v164 offset:3072
	ds_read_b128 v[168:171], v180
	ds_read_b128 v[172:175], v180 offset:1024
	ds_read_b128 v[176:179], v180 offset:2048
	ds_read_b128 v[180:183], v180 offset:3072
	s_add_u32 s34, s34, 0x80000
	s_addc_u32 s35, s35, 0
	s_mov_b32 m0, s33
	v_lshl_add_u64 v[224:225], s[34:35], 0, v[136:137]
	ds_read_b128 v[184:187], v151 offset:32768
	ds_read_b128 v[188:191], v151 offset:33792
	ds_read_b128 v[192:195], v151 offset:34816
	ds_read_b128 v[196:199], v151 offset:35840
	ds_read_b128 v[200:203], v151 offset:36864
	ds_read_b128 v[204:207], v151 offset:37888
	ds_read_b128 v[208:211], v151 offset:38912
	ds_read_b128 v[212:215], v151 offset:39936
	global_load_lds_dwordx4 v[224:225], off
	v_lshl_add_u64 v[224:225], s[34:35], 0, v[132:133]
	s_mov_b32 m0, s36
	s_nop 0
	global_load_lds_dwordx4 v[224:225], off
	s_waitcnt vmcnt(8)
	s_waitcnt lgkmcnt(0)
	s_barrier
	s_setprio 1
	s_waitcnt lgkmcnt(0)
	v_mfma_f32_16x16x32_bf16 v[126:129], v[152:155], v[184:187], v[126:129]
	v_mfma_f32_16x16x32_bf16 v[122:125], v[160:163], v[184:187], v[122:125]
	v_mfma_f32_16x16x32_bf16 v[118:121], v[152:155], v[192:195], v[118:121]
	v_mfma_f32_16x16x32_bf16 v[114:117], v[160:163], v[192:195], v[114:117]
	v_mfma_f32_16x16x32_bf16 v[102:105], v[152:155], v[200:203], v[102:105]
	v_mfma_f32_16x16x32_bf16 v[98:101], v[160:163], v[200:203], v[98:101]
	v_mfma_f32_16x16x32_bf16 v[86:89], v[152:155], v[208:211], v[86:89]
	v_mfma_f32_16x16x32_bf16 v[82:85], v[160:163], v[208:211], v[82:85]
	v_mfma_f32_16x16x32_bf16 v[126:129], v[156:159], v[188:191], v[126:129]
	v_mfma_f32_16x16x32_bf16 v[122:125], v[164:167], v[188:191], v[122:125]
	v_mfma_f32_16x16x32_bf16 v[118:121], v[156:159], v[196:199], v[118:121]
	v_mfma_f32_16x16x32_bf16 v[114:117], v[164:167], v[196:199], v[114:117]
	v_mfma_f32_16x16x32_bf16 v[102:105], v[156:159], v[204:207], v[102:105]
	v_mfma_f32_16x16x32_bf16 v[98:101], v[164:167], v[204:207], v[98:101]
	v_mfma_f32_16x16x32_bf16 v[86:89], v[156:159], v[212:215], v[86:89]
	v_mfma_f32_16x16x32_bf16 v[82:85], v[164:167], v[212:215], v[82:85]
	v_mfma_f32_16x16x32_bf16 v[110:113], v[168:171], v[184:187], v[110:113]
	v_mfma_f32_16x16x32_bf16 v[106:109], v[176:179], v[184:187], v[106:109]
	v_mfma_f32_16x16x32_bf16 v[94:97], v[168:171], v[192:195], v[94:97]
	v_mfma_f32_16x16x32_bf16 v[90:93], v[176:179], v[192:195], v[90:93]
	v_mfma_f32_16x16x32_bf16 v[78:81], v[168:171], v[200:203], v[78:81]
	v_mfma_f32_16x16x32_bf16 v[74:77], v[176:179], v[200:203], v[74:77]
	v_mfma_f32_16x16x32_bf16 v[70:73], v[168:171], v[208:211], v[70:73]
	v_mfma_f32_16x16x32_bf16 v[66:69], v[176:179], v[208:211], v[66:69]
	v_mfma_f32_16x16x32_bf16 v[110:113], v[172:175], v[188:191], v[110:113]
	v_mfma_f32_16x16x32_bf16 v[106:109], v[180:183], v[188:191], v[106:109]
	v_mfma_f32_16x16x32_bf16 v[94:97], v[172:175], v[196:199], v[94:97]
	v_mfma_f32_16x16x32_bf16 v[90:93], v[180:183], v[196:199], v[90:93]
	v_mfma_f32_16x16x32_bf16 v[78:81], v[172:175], v[204:207], v[78:81]
	v_mfma_f32_16x16x32_bf16 v[74:77], v[180:183], v[204:207], v[74:77]
	v_mfma_f32_16x16x32_bf16 v[70:73], v[172:175], v[212:215], v[70:73]
	v_mfma_f32_16x16x32_bf16 v[66:69], v[180:183], v[212:215], v[66:69]
	s_setprio 0
	s_barrier
; #define PG8_STAGE(bufoff, gbase, voff) do { _Pragma("unroll") for (int _i = 0; _i < 2; ++_i) \
;         __builtin_amdgcn_global_load_lds((const unsigned*)((const char*)(gbase) + (voff)[_i]), (PG8_LAS unsigned*)(lds + (bufoff) + ldsw + _i * 8192), 16, 0, 0); } while (0)
; #define PG8_LDA(dst, b, h) do { _Pragma("unroll") for (int m = 0; m < 4; ++m) _Pragma("unroll") for (int k = 0; k < 2; ++k) dst[m][k] = *(const PG8_LAS bf16x8*)(lds + PG8_SA(b, h) + aoff + m * 2048 + k * 1024); } while (0)
; #define PG8_MMA(ai, bj, At, Bt) do { __builtin_amdgcn_s_setprio(1); _Pragma("unroll") for (int m = 0; m < 4; ++m) _Pragma("unroll") for (int n = 0; n < 2; ++n) _Pragma("unroll") for (int k = 0; k < 2; ++k) \
;         acc[ai][bj][m][n] = __builtin_amdgcn_mfma_f32_16x16x32_bf16(Bt[n][k], At[m][k], acc[ai][bj][m][n], 0, 0, 0); __builtin_amdgcn_s_setprio(0); } while (0)
; #define PG8_WAIT_V(n) asm volatile("s_waitcnt vmcnt(" #n ")" ::: "memory")
; #define PG8_WAIT_L(n) asm volatile("s_waitcnt lgkmcnt(" #n ")" ::: "memory")
; #define PG8_BAR __builtin_amdgcn_s_barrier()
; #define PG8_SCHED __builtin_amdgcn_sched_barrier(0)
; template <class Epi, class Sched, bool ALIGN_EPI = false, bool SP2 = false>
; __device__ __forceinline__ void gemm_phase(PG8_LAS unsigned char* lds, const Gemm g, const Sched& S, const Epi& E) {
;     ...
;             PG8_LDA(At, 1, 1); PG8_STAGE(PG8_SB(1, 0), b3, voffB); PG8_STAGE(PG8_SB(1, 1), b3 + hstep, voffB); PG8_STAGE(PG8_SA(1, 0), a3, voffA);
;             PG8_WAIT_V(8); PG8_WAIT_L(0); PG8_BAR; PG8_MMA(1, 0, At, B0); PG8_MMA(1, 1, At, B1); PG8_BAR; PG8_SCHED;
	s_add_i32 s34, s79, s2
	v_lshl_add_u64 v[216:217], v[216:217], 0, s[6:7]
	s_mov_b32 m0, s34
	ds_read_b128 v[184:187], v151 offset:49152
	ds_read_b128 v[188:191], v151 offset:50176
	ds_read_b128 v[192:195], v151 offset:51200
	ds_read_b128 v[196:199], v151 offset:52224
	ds_read_b128 v[200:203], v151 offset:53248
	ds_read_b128 v[204:207], v151 offset:54272
	ds_read_b128 v[208:211], v151 offset:55296
	ds_read_b128 v[212:215], v151 offset:56320
	global_load_lds_dwordx4 v[216:217], off
	s_add_i32 m0, s34, 0x2000
	s_add_u32 s28, s28, 0x80080
	v_lshl_add_u64 v[216:217], v[218:219], 0, s[6:7]
	s_addc_u32 s29, s29, 0
	s_add_i32 s34, s96, s2
	global_load_lds_dwordx4 v[216:217], off
	v_lshl_add_u64 v[216:217], s[28:29], 0, v[134:135]
	s_mov_b32 m0, s34
	s_nop 0
	global_load_lds_dwordx4 v[216:217], off
	v_lshl_add_u64 v[216:217], s[28:29], 0, v[130:131]
	s_add_i32 m0, s34, 0x2000
	s_nop 0
	global_load_lds_dwordx4 v[216:217], off
	v_lshl_add_u64 v[216:217], v[220:221], 0, s[6:7]
	s_mov_b32 m0, s38
	s_nop 0
	global_load_lds_dwordx4 v[216:217], off
	v_lshl_add_u64 v[216:217], v[222:223], 0, s[6:7]
	s_mov_b32 m0, s39
	s_nop 0
	global_load_lds_dwordx4 v[216:217], off
	s_waitcnt vmcnt(8)
	s_waitcnt lgkmcnt(0)
	s_barrier
	s_setprio 1
	s_waitcnt lgkmcnt(0)
	v_mfma_f32_16x16x32_bf16 v[62:65], v[152:155], v[184:187], v[62:65]
	v_mfma_f32_16x16x32_bf16 v[58:61], v[160:163], v[184:187], v[58:61]
	v_mfma_f32_16x16x32_bf16 v[54:57], v[152:155], v[192:195], v[54:57]
	v_mfma_f32_16x16x32_bf16 v[50:53], v[160:163], v[192:195], v[50:53]
	v_mfma_f32_16x16x32_bf16 v[38:41], v[152:155], v[200:203], v[38:41]
	v_mfma_f32_16x16x32_bf16 v[34:37], v[160:163], v[200:203], v[34:37]
	v_mfma_f32_16x16x32_bf16 v[22:25], v[152:155], v[208:211], v[22:25]
	v_mfma_f32_16x16x32_bf16 v[18:21], v[160:163], v[208:211], v[18:21]
	v_mfma_f32_16x16x32_bf16 v[62:65], v[156:159], v[188:191], v[62:65]
	v_mfma_f32_16x16x32_bf16 v[58:61], v[164:167], v[188:191], v[58:61]
	v_mfma_f32_16x16x32_bf16 v[54:57], v[156:159], v[196:199], v[54:57]
	v_mfma_f32_16x16x32_bf16 v[50:53], v[164:167], v[196:199], v[50:53]
	v_mfma_f32_16x16x32_bf16 v[38:41], v[156:159], v[204:207], v[38:41]
	v_mfma_f32_16x16x32_bf16 v[34:37], v[164:167], v[204:207], v[34:37]
	v_mfma_f32_16x16x32_bf16 v[22:25], v[156:159], v[212:215], v[22:25]
	v_mfma_f32_16x16x32_bf16 v[18:21], v[164:167], v[212:215], v[18:21]
	v_mfma_f32_16x16x32_bf16 v[46:49], v[168:171], v[184:187], v[46:49]
	v_mfma_f32_16x16x32_bf16 v[42:45], v[176:179], v[184:187], v[42:45]
	v_mfma_f32_16x16x32_bf16 v[30:33], v[168:171], v[192:195], v[30:33]
	v_mfma_f32_16x16x32_bf16 v[26:29], v[176:179], v[192:195], v[26:29]
	v_mfma_f32_16x16x32_bf16 v[14:17], v[168:171], v[200:203], v[14:17]
	v_mfma_f32_16x16x32_bf16 v[10:13], v[176:179], v[200:203], v[10:13]
	v_mfma_f32_16x16x32_bf16 v[6:9], v[168:171], v[208:211], v[6:9]
	v_mfma_f32_16x16x32_bf16 v[2:5], v[176:179], v[208:211], v[2:5]
	v_mfma_f32_16x16x32_bf16 v[46:49], v[172:175], v[188:191], v[46:49]
	v_mfma_f32_16x16x32_bf16 v[42:45], v[180:183], v[188:191], v[42:45]
	v_mfma_f32_16x16x32_bf16 v[30:33], v[172:175], v[196:199], v[30:33]
	v_mfma_f32_16x16x32_bf16 v[26:29], v[180:183], v[196:199], v[26:29]
	v_mfma_f32_16x16x32_bf16 v[14:17], v[172:175], v[204:207], v[14:17]
	v_mfma_f32_16x16x32_bf16 v[10:13], v[180:183], v[204:207], v[10:13]
	v_mfma_f32_16x16x32_bf16 v[6:9], v[172:175], v[212:215], v[6:9]
	v_mfma_f32_16x16x32_bf16 v[2:5], v[180:183], v[212:215], v[2:5]
	s_setprio 0
	s_barrier
	s_add_i32 s78, s78, 2
	s_add_u32 s26, s26, 0x100
	s_addc_u32 s27, s27, 0
	s_add_u32 s62, s62, 0x100
	s_addc_u32 s63, s63, 0
	s_cmp_gt_u32 s78, 29
	s_cbranch_scc0 .LBB0_230
	s_and_b64 vcc, exec, s[8:9]
	s_mov_b32 s88, s4
	s_cbranch_vccz .LBB0_233
	s_barrier

; #define PG8_STAGE(bufoff, gbase, voff) do { _Pragma("unroll") for (int _i = 0; _i < 2; ++_i) \
;         __builtin_amdgcn_global_load_lds((const unsigned*)((const char*)(gbase) + (voff)[_i]), (PG8_LAS unsigned*)(lds + (bufoff) + ldsw + _i * 8192), 16, 0, 0); } while (0)
; #define PG8_LDA(dst, b, h) do { _Pragma("unroll") for (int m = 0; m < 4; ++m) _Pragma("unroll") for (int k = 0; k < 2; ++k) dst[m][k] = *(const PG8_LAS bf16x8*)(lds + PG8_SA(b, h) + aoff + m * 2048 + k * 1024); } while (0)
; #define PG8_LDB(dst, b, h) do { _Pragma("unroll") for (int n = 0; n < 2; ++n) _Pragma("unroll") for (int k = 0; k < 2; ++k) dst[n][k] = *(const PG8_LAS bf16x8*)(lds + PG8_SB(b, h) + boff + n * 2048 + k * 1024); } while (0)
; #define PG8_MMA(ai, bj, At, Bt) do { __builtin_amdgcn_s_setprio(1); _Pragma("unroll") for (int m = 0; m < 4; ++m) _Pragma("unroll") for (int n = 0; n < 2; ++n) _Pragma("unroll") for (int k = 0; k < 2; ++k) \
;         acc[ai][bj][m][n] = __builtin_amdgcn_mfma_f32_16x16x32_bf16(Bt[n][k], At[m][k], acc[ai][bj][m][n], 0, 0, 0); __builtin_amdgcn_s_setprio(0); } while (0)
; #define PG8_WAIT_V(n) asm volatile("s_waitcnt vmcnt(" #n ")" ::: "memory")
; #define PG8_WAIT_L(n) asm volatile("s_waitcnt lgkmcnt(" #n ")" ::: "memory")
; #define PG8_BAR __builtin_amdgcn_s_barrier()
; #define PG8_SCHED __builtin_amdgcn_sched_barrier(0)
; template <class Epi, class Sched, bool ALIGN_EPI = false, bool SP2 = false>
; __device__ __forceinline__ void gemm_phase(PG8_LAS unsigned char* lds, const Gemm g, const Sched& S, const Epi& E) {
;     ...
;             PG8_LDB(B0, 0, 0); PG8_LDB(B1, 0, 1); PG8_SCHED; PG8_LDA(At, 0, 0); PG8_STAGE(PG8_SA(1, 1), a1 + hstep, voffA);
;             PG8_WAIT_V(8); PG8_WAIT_L(0); PG8_BAR; PG8_MMA(0, 0, At, B0); PG8_MMA(0, 1, At, B1); PG8_BAR; PG8_SCHED;
;             PG8_LDA(At, 0, 1); PG8_STAGE(PG8_SB(0, 0), b2, voffB); PG8_STAGE(PG8_SB(0, 1), b2 + hstep, voffB); PG8_STAGE(PG8_SA(0, 0), a2, voffA);
;             PG8_WAIT_V(8); PG8_WAIT_L(0); PG8_BAR; PG8_MMA(1, 0, At, B0); PG8_MMA(1, 1, At, B1); PG8_BAR; PG8_SCHED;
.LBB0_892:
	ds_read_b128 v[144:147], v155
	ds_read_b128 v[148:151], v155 offset:1024
	ds_read_b128 v[166:169], v155 offset:2048
	ds_read_b128 v[170:173], v155 offset:3072
	ds_read_b128 v[174:177], v156
	ds_read_b128 v[178:181], v156 offset:1024
	ds_read_b128 v[182:185], v156 offset:2048
	ds_read_b128 v[190:193], v156 offset:3072
	s_add_u32 s28, s26, 0x100
	s_addc_u32 s29, s27, 0
	s_cmp_eq_u32 s45, 28
	s_cselect_b32 s35, s7, s29
	s_cselect_b32 s34, s19, s28
	s_cselect_b32 s31, s17, s44
	s_cselect_b32 s30, s42, s43
	v_lshl_add_u64 v[160:161], s[26:27], 0, v[136:137]
	s_add_i32 m0, s3, 0xc000
	ds_read_b128 v[194:197], v157
	ds_read_b128 v[198:201], v157 offset:1024
	ds_read_b128 v[202:205], v157 offset:2048
	ds_read_b128 v[206:209], v157 offset:3072
	ds_read_b128 v[210:213], v157 offset:4096
	ds_read_b128 v[214:217], v157 offset:5120
	ds_read_b128 v[218:221], v157 offset:6144
	ds_read_b128 v[222:225], v157 offset:7168
	global_load_lds_dwordx4 v[160:161], off
	v_lshl_add_u64 v[160:161], s[26:27], 0, v[138:139]
	s_add_i32 m0, s3, 0xe000
	s_nop 0
	global_load_lds_dwordx4 v[160:161], off
	s_waitcnt vmcnt(8)
	s_waitcnt lgkmcnt(0)
	s_barrier
	s_setprio 1
	s_waitcnt lgkmcnt(0)
	v_mfma_f32_16x16x32_bf16 v[126:129], v[144:147], v[194:197], v[126:129]
	v_mfma_f32_16x16x32_bf16 v[122:125], v[166:169], v[194:197], v[122:125]
	v_mfma_f32_16x16x32_bf16 v[110:113], v[144:147], v[202:205], v[110:113]
	v_mfma_f32_16x16x32_bf16 v[106:109], v[166:169], v[202:205], v[106:109]
	v_mfma_f32_16x16x32_bf16 v[94:97], v[144:147], v[210:213], v[94:97]
	v_mfma_f32_16x16x32_bf16 v[90:93], v[166:169], v[210:213], v[90:93]
	v_mfma_f32_16x16x32_bf16 v[78:81], v[144:147], v[218:221], v[78:81]
	v_mfma_f32_16x16x32_bf16 v[74:77], v[166:169], v[218:221], v[74:77]
	v_mfma_f32_16x16x32_bf16 v[126:129], v[148:151], v[198:201], v[126:129]
	v_mfma_f32_16x16x32_bf16 v[122:125], v[170:173], v[198:201], v[122:125]
	v_mfma_f32_16x16x32_bf16 v[110:113], v[148:151], v[206:209], v[110:113]
	v_mfma_f32_16x16x32_bf16 v[106:109], v[170:173], v[206:209], v[106:109]
	v_mfma_f32_16x16x32_bf16 v[94:97], v[148:151], v[214:217], v[94:97]
	v_mfma_f32_16x16x32_bf16 v[90:93], v[170:173], v[214:217], v[90:93]
	v_mfma_f32_16x16x32_bf16 v[78:81], v[148:151], v[222:225], v[78:81]
	v_mfma_f32_16x16x32_bf16 v[74:77], v[170:173], v[222:225], v[74:77]
	v_mfma_f32_16x16x32_bf16 v[118:121], v[174:177], v[194:197], v[118:121]
	v_mfma_f32_16x16x32_bf16 v[114:117], v[182:185], v[194:197], v[114:117]
	v_mfma_f32_16x16x32_bf16 v[102:105], v[174:177], v[202:205], v[102:105]
	v_mfma_f32_16x16x32_bf16 v[98:101], v[182:185], v[202:205], v[98:101]
	v_mfma_f32_16x16x32_bf16 v[86:89], v[174:177], v[210:213], v[86:89]
	v_mfma_f32_16x16x32_bf16 v[82:85], v[182:185], v[210:213], v[82:85]
	v_mfma_f32_16x16x32_bf16 v[70:73], v[174:177], v[218:221], v[70:73]
	v_mfma_f32_16x16x32_bf16 v[66:69], v[182:185], v[218:221], v[66:69]
	v_mfma_f32_16x16x32_bf16 v[118:121], v[178:181], v[198:201], v[118:121]
	v_mfma_f32_16x16x32_bf16 v[114:117], v[190:193], v[198:201], v[114:117]
	v_mfma_f32_16x16x32_bf16 v[102:105], v[178:181], v[206:209], v[102:105]
	v_mfma_f32_16x16x32_bf16 v[98:101], v[190:193], v[206:209], v[98:101]
	v_mfma_f32_16x16x32_bf16 v[86:89], v[178:181], v[214:217], v[86:89]
	v_mfma_f32_16x16x32_bf16 v[82:85], v[190:193], v[214:217], v[82:85]
	v_mfma_f32_16x16x32_bf16 v[70:73], v[178:181], v[222:225], v[70:73]
	v_mfma_f32_16x16x32_bf16 v[66:69], v[190:193], v[222:225], v[66:69]
	s_setprio 0
	s_barrier
	s_add_i32 s26, s39, s2
	v_lshl_add_u64 v[160:161], s[30:31], 0, v[130:131]
	s_mov_b32 m0, s26
	ds_read_b128 v[194:197], v157 offset:16384
	ds_read_b128 v[198:201], v157 offset:17408
	ds_read_b128 v[202:205], v157 offset:18432
	ds_read_b128 v[206:209], v157 offset:19456
	ds_read_b128 v[210:213], v157 offset:20480
	ds_read_b128 v[214:217], v157 offset:21504
	ds_read_b128 v[218:221], v157 offset:22528
	ds_read_b128 v[222:225], v157 offset:23552
	global_load_lds_dwordx4 v[160:161], off
	s_add_i32 m0, s26, 0x2000
	s_add_u32 s26, s30, 0x80000
	v_lshl_add_u64 v[186:187], s[30:31], 0, v[132:133]
	s_addc_u32 s27, s31, 0
	s_add_i32 s46, s40, s2
	global_load_lds_dwordx4 v[186:187], off
	v_lshl_add_u64 v[226:227], s[26:27], 0, v[130:131]
	s_mov_b32 m0, s46
	v_lshl_add_u64 v[228:229], s[34:35], 0, v[132:133]
	global_load_lds_dwordx4 v[226:227], off
	v_lshl_add_u64 v[226:227], s[26:27], 0, v[132:133]
	s_add_i32 m0, s46, 0x2000
	s_nop 0
	global_load_lds_dwordx4 v[226:227], off
	v_lshl_add_u64 v[226:227], s[34:35], 0, v[130:131]
	s_mov_b32 m0, s3
	s_nop 0
	global_load_lds_dwordx4 v[226:227], off
	s_mov_b32 m0, s4
	s_nop 0
	global_load_lds_dwordx4 v[228:229], off
	s_waitcnt vmcnt(8)
	s_waitcnt lgkmcnt(0)
	s_barrier
; #define PG8_STAGE(bufoff, gbase, voff) do { _Pragma("unroll") for (int _i = 0; _i < 2; ++_i) \
;         __builtin_amdgcn_global_load_lds((const unsigned*)((const char*)(gbase) + (voff)[_i]), (PG8_LAS unsigned*)(lds + (bufoff) + ldsw + _i * 8192), 16, 0, 0); } while (0)
; #define PG8_LDA(dst, b, h) do { _Pragma("unroll") for (int m = 0; m < 4; ++m) _Pragma("unroll") for (int k = 0; k < 2; ++k) dst[m][k] = *(const PG8_LAS bf16x8*)(lds + PG8_SA(b, h) + aoff + m * 2048 + k * 1024); } while (0)
; #define PG8_LDB(dst, b, h) do { _Pragma("unroll") for (int n = 0; n < 2; ++n) _Pragma("unroll") for (int k = 0; k < 2; ++k) dst[n][k] = *(const PG8_LAS bf16x8*)(lds + PG8_SB(b, h) + boff + n * 2048 + k * 1024); } while (0)
; #define PG8_MMA(ai, bj, At, Bt) do { __builtin_amdgcn_s_setprio(1); _Pragma("unroll") for (int m = 0; m < 4; ++m) _Pragma("unroll") for (int n = 0; n < 2; ++n) _Pragma("unroll") for (int k = 0; k < 2; ++k) \
;         acc[ai][bj][m][n] = __builtin_amdgcn_mfma_f32_16x16x32_bf16(Bt[n][k], At[m][k], acc[ai][bj][m][n], 0, 0, 0); __builtin_amdgcn_s_setprio(0); } while (0)
; #define PG8_WAIT_V(n) asm volatile("s_waitcnt vmcnt(" #n ")" ::: "memory")
; #define PG8_WAIT_L(n) asm volatile("s_waitcnt lgkmcnt(" #n ")" ::: "memory")
; #define PG8_BAR __builtin_amdgcn_s_barrier()
; #define PG8_SCHED __builtin_amdgcn_sched_barrier(0)
; template <class Epi, class Sched, bool ALIGN_EPI = false, bool SP2 = false>
; __device__ __forceinline__ void gemm_phase(PG8_LAS unsigned char* lds, const Gemm g, const Sched& S, const Epi& E) {
;     ...
;             PG8_WAIT_V(8); PG8_WAIT_L(0); PG8_BAR; PG8_MMA(1, 0, At, B0); PG8_MMA(1, 1, At, B1); PG8_BAR; PG8_SCHED;
;             PG8_LDB(B0, 1, 0); PG8_LDB(B1, 1, 1); PG8_SCHED; PG8_LDA(At, 1, 0); PG8_STAGE(PG8_SA(0, 1), a2 + hstep, voffA);
;             PG8_WAIT_V(8); PG8_WAIT_L(0); PG8_BAR; PG8_MMA(0, 0, At, B0); PG8_MMA(0, 1, At, B1); PG8_BAR; PG8_SCHED;
;             PG8_LDA(At, 1, 1); PG8_STAGE(PG8_SB(1, 0), b3, voffB); PG8_STAGE(PG8_SB(1, 1), b3 + hstep, voffB); PG8_STAGE(PG8_SA(1, 0), a3, voffA);
	s_setprio 1
	s_waitcnt lgkmcnt(0)
	v_mfma_f32_16x16x32_bf16 v[62:65], v[144:147], v[194:197], v[62:65]
	v_mfma_f32_16x16x32_bf16 v[58:61], v[166:169], v[194:197], v[58:61]
	v_mfma_f32_16x16x32_bf16 v[46:49], v[144:147], v[202:205], v[46:49]
	v_mfma_f32_16x16x32_bf16 v[42:45], v[166:169], v[202:205], v[42:45]
	v_mfma_f32_16x16x32_bf16 v[30:33], v[144:147], v[210:213], v[30:33]
	v_mfma_f32_16x16x32_bf16 v[26:29], v[166:169], v[210:213], v[26:29]
	v_mfma_f32_16x16x32_bf16 v[14:17], v[144:147], v[218:221], v[14:17]
	v_mfma_f32_16x16x32_bf16 v[10:13], v[166:169], v[218:221], v[10:13]
	v_mfma_f32_16x16x32_bf16 v[62:65], v[148:151], v[198:201], v[62:65]
	v_mfma_f32_16x16x32_bf16 v[58:61], v[170:173], v[198:201], v[58:61]
	v_mfma_f32_16x16x32_bf16 v[46:49], v[148:151], v[206:209], v[46:49]
	v_mfma_f32_16x16x32_bf16 v[42:45], v[170:173], v[206:209], v[42:45]
	v_mfma_f32_16x16x32_bf16 v[30:33], v[148:151], v[214:217], v[30:33]
	v_mfma_f32_16x16x32_bf16 v[26:29], v[170:173], v[214:217], v[26:29]
	v_mfma_f32_16x16x32_bf16 v[14:17], v[148:151], v[222:225], v[14:17]
	v_mfma_f32_16x16x32_bf16 v[10:13], v[170:173], v[222:225], v[10:13]
	v_mfma_f32_16x16x32_bf16 v[54:57], v[174:177], v[194:197], v[54:57]
	v_mfma_f32_16x16x32_bf16 v[50:53], v[182:185], v[194:197], v[50:53]
	v_mfma_f32_16x16x32_bf16 v[38:41], v[174:177], v[202:205], v[38:41]
	v_mfma_f32_16x16x32_bf16 v[34:37], v[182:185], v[202:205], v[34:37]
	v_mfma_f32_16x16x32_bf16 v[22:25], v[174:177], v[210:213], v[22:25]
	v_mfma_f32_16x16x32_bf16 v[18:21], v[182:185], v[210:213], v[18:21]
	v_mfma_f32_16x16x32_bf16 v[6:9], v[174:177], v[218:221], v[6:9]
	v_mfma_f32_16x16x32_bf16 v[2:5], v[182:185], v[218:221], v[2:5]
	v_mfma_f32_16x16x32_bf16 v[54:57], v[178:181], v[198:201], v[54:57]
	v_mfma_f32_16x16x32_bf16 v[50:53], v[190:193], v[198:201], v[50:53]
	v_mfma_f32_16x16x32_bf16 v[38:41], v[178:181], v[206:209], v[38:41]
	v_mfma_f32_16x16x32_bf16 v[34:37], v[190:193], v[206:209], v[34:37]
	v_mfma_f32_16x16x32_bf16 v[22:25], v[178:181], v[214:217], v[22:25]
	v_mfma_f32_16x16x32_bf16 v[18:21], v[190:193], v[214:217], v[18:21]
	v_mfma_f32_16x16x32_bf16 v[6:9], v[178:181], v[222:225], v[6:9]
	v_mfma_f32_16x16x32_bf16 v[2:5], v[190:193], v[222:225], v[2:5]
	s_setprio 0
	s_barrier
	s_add_i32 s46, 0, 0x18000
	v_add_u32_e32 v134, s46, v153
	s_add_i32 s47, 0, 0x1c000
	ds_read_b128 v[144:147], v134
	ds_read_b128 v[148:151], v134 offset:1024
	ds_read_b128 v[166:169], v134 offset:2048
	ds_read_b128 v[170:173], v134 offset:3072
	v_add_u32_e32 v134, s47, v153
	ds_read_b128 v[174:177], v134
	ds_read_b128 v[178:181], v134 offset:1024
	ds_read_b128 v[182:185], v134 offset:2048
	ds_read_b128 v[190:193], v134 offset:3072
	s_add_u32 s26, s34, 0x80000
	s_addc_u32 s27, s35, 0
	s_mov_b32 m0, s5
	v_lshl_add_u64 v[230:231], s[26:27], 0, v[130:131]
	ds_read_b128 v[194:197], v157 offset:32768
	ds_read_b128 v[198:201], v157 offset:33792
	ds_read_b128 v[202:205], v157 offset:34816
	ds_read_b128 v[206:209], v157 offset:35840
	ds_read_b128 v[210:213], v157 offset:36864
	ds_read_b128 v[214:217], v157 offset:37888
	ds_read_b128 v[218:221], v157 offset:38912
	ds_read_b128 v[222:225], v157 offset:39936
	global_load_lds_dwordx4 v[230:231], off
	v_lshl_add_u64 v[230:231], s[26:27], 0, v[132:133]
	s_mov_b32 m0, s25
	s_nop 0
	global_load_lds_dwordx4 v[230:231], off
	s_waitcnt vmcnt(8)
	s_waitcnt lgkmcnt(0)
	s_barrier
	s_setprio 1
	s_waitcnt lgkmcnt(0)
	v_mfma_f32_16x16x32_bf16 v[126:129], v[144:147], v[194:197], v[126:129]
	v_mfma_f32_16x16x32_bf16 v[122:125], v[166:169], v[194:197], v[122:125]
	v_mfma_f32_16x16x32_bf16 v[110:113], v[144:147], v[202:205], v[110:113]
	v_mfma_f32_16x16x32_bf16 v[106:109], v[166:169], v[202:205], v[106:109]
	v_mfma_f32_16x16x32_bf16 v[94:97], v[144:147], v[210:213], v[94:97]
	v_mfma_f32_16x16x32_bf16 v[90:93], v[166:169], v[210:213], v[90:93]
	v_mfma_f32_16x16x32_bf16 v[78:81], v[144:147], v[218:221], v[78:81]
	v_mfma_f32_16x16x32_bf16 v[74:77], v[166:169], v[218:221], v[74:77]
	v_mfma_f32_16x16x32_bf16 v[126:129], v[148:151], v[198:201], v[126:129]
	v_mfma_f32_16x16x32_bf16 v[122:125], v[170:173], v[198:201], v[122:125]
	v_mfma_f32_16x16x32_bf16 v[110:113], v[148:151], v[206:209], v[110:113]
	v_mfma_f32_16x16x32_bf16 v[106:109], v[170:173], v[206:209], v[106:109]
	v_mfma_f32_16x16x32_bf16 v[94:97], v[148:151], v[214:217], v[94:97]
	v_mfma_f32_16x16x32_bf16 v[90:93], v[170:173], v[214:217], v[90:93]
	v_mfma_f32_16x16x32_bf16 v[78:81], v[148:151], v[222:225], v[78:81]
	v_mfma_f32_16x16x32_bf16 v[74:77], v[170:173], v[222:225], v[74:77]
	v_mfma_f32_16x16x32_bf16 v[118:121], v[174:177], v[194:197], v[118:121]
	v_mfma_f32_16x16x32_bf16 v[114:117], v[182:185], v[194:197], v[114:117]
	v_mfma_f32_16x16x32_bf16 v[102:105], v[174:177], v[202:205], v[102:105]
	v_mfma_f32_16x16x32_bf16 v[98:101], v[182:185], v[202:205], v[98:101]
	v_mfma_f32_16x16x32_bf16 v[86:89], v[174:177], v[210:213], v[86:89]
	v_mfma_f32_16x16x32_bf16 v[82:85], v[182:185], v[210:213], v[82:85]
	v_mfma_f32_16x16x32_bf16 v[70:73], v[174:177], v[218:221], v[70:73]
	v_mfma_f32_16x16x32_bf16 v[66:69], v[182:185], v[218:221], v[66:69]
	v_mfma_f32_16x16x32_bf16 v[118:121], v[178:181], v[198:201], v[118:121]
	v_mfma_f32_16x16x32_bf16 v[114:117], v[190:193], v[198:201], v[114:117]
	v_mfma_f32_16x16x32_bf16 v[102:105], v[178:181], v[206:209], v[102:105]
	v_mfma_f32_16x16x32_bf16 v[98:101], v[190:193], v[206:209], v[98:101]
	v_mfma_f32_16x16x32_bf16 v[86:89], v[178:181], v[214:217], v[86:89]
	v_mfma_f32_16x16x32_bf16 v[82:85], v[190:193], v[214:217], v[82:85]
	v_mfma_f32_16x16x32_bf16 v[70:73], v[178:181], v[222:225], v[70:73]
	v_mfma_f32_16x16x32_bf16 v[66:69], v[190:193], v[222:225], v[66:69]
	s_setprio 0
	s_barrier
; #define PG8_STAGE(bufoff, gbase, voff) do { _Pragma("unroll") for (int _i = 0; _i < 2; ++_i) \
;         __builtin_amdgcn_global_load_lds((const unsigned*)((const char*)(gbase) + (voff)[_i]), (PG8_LAS unsigned*)(lds + (bufoff) + ldsw + _i * 8192), 16, 0, 0); } while (0)
; #define PG8_LDA(dst, b, h) do { _Pragma("unroll") for (int m = 0; m < 4; ++m) _Pragma("unroll") for (int k = 0; k < 2; ++k) dst[m][k] = *(const PG8_LAS bf16x8*)(lds + PG8_SA(b, h) + aoff + m * 2048 + k * 1024); } while (0)
; #define PG8_MMA(ai, bj, At, Bt) do { __builtin_amdgcn_s_setprio(1); _Pragma("unroll") for (int m = 0; m < 4; ++m) _Pragma("unroll") for (int n = 0; n < 2; ++n) _Pragma("unroll") for (int k = 0; k < 2; ++k) \
;         acc[ai][bj][m][n] = __builtin_amdgcn_mfma_f32_16x16x32_bf16(Bt[n][k], At[m][k], acc[ai][bj][m][n], 0, 0, 0); __builtin_amdgcn_s_setprio(0); } while (0)
; #define PG8_WAIT_V(n) asm volatile("s_waitcnt vmcnt(" #n ")" ::: "memory")
; #define PG8_WAIT_L(n) asm volatile("s_waitcnt lgkmcnt(" #n ")" ::: "memory")
; #define PG8_BAR __builtin_amdgcn_s_barrier()
; #define PG8_SCHED __builtin_amdgcn_sched_barrier(0)
; template <class Epi, class Sched, bool ALIGN_EPI = false, bool SP2 = false>
; __device__ __forceinline__ void gemm_phase(PG8_LAS unsigned char* lds, const Gemm g, const Sched& S, const Epi& E) {
;     ...
;             PG8_LDA(At, 1, 1); PG8_STAGE(PG8_SB(1, 0), b3, voffB); PG8_STAGE(PG8_SB(1, 1), b3 + hstep, voffB); PG8_STAGE(PG8_SA(1, 0), a3, voffA);
;             PG8_WAIT_V(8); PG8_WAIT_L(0); PG8_BAR; PG8_MMA(1, 0, At, B0); PG8_MMA(1, 1, At, B1); PG8_BAR; PG8_SCHED;
	s_add_i32 s26, s46, s2
	v_lshl_add_u64 v[160:161], v[160:161], 0, s[12:13]
	s_mov_b32 m0, s26
	ds_read_b128 v[194:197], v157 offset:49152
	ds_read_b128 v[198:201], v157 offset:50176
	ds_read_b128 v[202:205], v157 offset:51200
	ds_read_b128 v[206:209], v157 offset:52224
	ds_read_b128 v[210:213], v157 offset:53248
	ds_read_b128 v[214:217], v157 offset:54272
	ds_read_b128 v[218:221], v157 offset:55296
	ds_read_b128 v[222:225], v157 offset:56320
	global_load_lds_dwordx4 v[160:161], off
	s_add_i32 m0, s26, 0x2000
	s_add_u32 s26, s30, 0x80080
	v_lshl_add_u64 v[160:161], v[186:187], 0, s[12:13]
	s_addc_u32 s27, s31, 0
	s_add_i32 s30, s47, s2
	global_load_lds_dwordx4 v[160:161], off
	v_lshl_add_u64 v[160:161], s[26:27], 0, v[130:131]
	s_mov_b32 m0, s30
	s_nop 0
	global_load_lds_dwordx4 v[160:161], off
	v_lshl_add_u64 v[160:161], s[26:27], 0, v[132:133]
	s_add_i32 m0, s30, 0x2000
	s_nop 0
	global_load_lds_dwordx4 v[160:161], off
	v_lshl_add_u64 v[160:161], v[226:227], 0, s[12:13]
	s_mov_b32 m0, s37
	s_nop 0
	global_load_lds_dwordx4 v[160:161], off
	v_lshl_add_u64 v[160:161], v[228:229], 0, s[12:13]
	s_mov_b32 m0, s38
	s_nop 0
	global_load_lds_dwordx4 v[160:161], off
	s_waitcnt vmcnt(8)
	s_waitcnt lgkmcnt(0)
	s_barrier
	s_setprio 1
	s_waitcnt lgkmcnt(0)
	v_mfma_f32_16x16x32_bf16 v[62:65], v[144:147], v[194:197], v[62:65]
	v_mfma_f32_16x16x32_bf16 v[58:61], v[166:169], v[194:197], v[58:61]
	v_mfma_f32_16x16x32_bf16 v[46:49], v[144:147], v[202:205], v[46:49]
	v_mfma_f32_16x16x32_bf16 v[42:45], v[166:169], v[202:205], v[42:45]
	v_mfma_f32_16x16x32_bf16 v[30:33], v[144:147], v[210:213], v[30:33]
	v_mfma_f32_16x16x32_bf16 v[26:29], v[166:169], v[210:213], v[26:29]
	v_mfma_f32_16x16x32_bf16 v[14:17], v[144:147], v[218:221], v[14:17]
	v_mfma_f32_16x16x32_bf16 v[10:13], v[166:169], v[218:221], v[10:13]
	v_mfma_f32_16x16x32_bf16 v[62:65], v[148:151], v[198:201], v[62:65]
	v_mfma_f32_16x16x32_bf16 v[58:61], v[170:173], v[198:201], v[58:61]
	v_mfma_f32_16x16x32_bf16 v[46:49], v[148:151], v[206:209], v[46:49]
	v_mfma_f32_16x16x32_bf16 v[42:45], v[170:173], v[206:209], v[42:45]
	v_mfma_f32_16x16x32_bf16 v[30:33], v[148:151], v[214:217], v[30:33]
	v_mfma_f32_16x16x32_bf16 v[26:29], v[170:173], v[214:217], v[26:29]
	v_mfma_f32_16x16x32_bf16 v[14:17], v[148:151], v[222:225], v[14:17]
	v_mfma_f32_16x16x32_bf16 v[10:13], v[170:173], v[222:225], v[10:13]
	v_mfma_f32_16x16x32_bf16 v[54:57], v[174:177], v[194:197], v[54:57]
	v_mfma_f32_16x16x32_bf16 v[50:53], v[182:185], v[194:197], v[50:53]
	v_mfma_f32_16x16x32_bf16 v[38:41], v[174:177], v[202:205], v[38:41]
	v_mfma_f32_16x16x32_bf16 v[34:37], v[182:185], v[202:205], v[34:37]
	v_mfma_f32_16x16x32_bf16 v[22:25], v[174:177], v[210:213], v[22:25]
	v_mfma_f32_16x16x32_bf16 v[18:21], v[182:185], v[210:213], v[18:21]
	v_mfma_f32_16x16x32_bf16 v[6:9], v[174:177], v[218:221], v[6:9]
	v_mfma_f32_16x16x32_bf16 v[2:5], v[182:185], v[218:221], v[2:5]
	v_mfma_f32_16x16x32_bf16 v[54:57], v[178:181], v[198:201], v[54:57]
	v_mfma_f32_16x16x32_bf16 v[50:53], v[190:193], v[198:201], v[50:53]
	v_mfma_f32_16x16x32_bf16 v[38:41], v[178:181], v[206:209], v[38:41]
	v_mfma_f32_16x16x32_bf16 v[34:37], v[190:193], v[206:209], v[34:37]
	v_mfma_f32_16x16x32_bf16 v[22:25], v[178:181], v[214:217], v[22:25]
	v_mfma_f32_16x16x32_bf16 v[18:21], v[190:193], v[214:217], v[18:21]
	v_mfma_f32_16x16x32_bf16 v[6:9], v[178:181], v[222:225], v[6:9]
	v_mfma_f32_16x16x32_bf16 v[2:5], v[190:193], v[222:225], v[2:5]
	s_setprio 0
	s_barrier
	s_add_i32 s45, s45, 2
	s_add_u32 s43, s43, 0x100
	s_addc_u32 s44, s44, 0
	s_cmp_gt_u32 s45, 29
	s_mov_b64 s[26:27], s[28:29]
	s_cbranch_scc0 .LBB0_892
	s_and_b64 vcc, exec, s[14:15]
	s_cbranch_vccz .LBB0_895
	s_barrier

; #define PG8_STAGE(bufoff, gbase, voff) do { _Pragma("unroll") for (int _i = 0; _i < 2; ++_i) \
;         __builtin_amdgcn_global_load_lds((const unsigned*)((const char*)(gbase) + (voff)[_i]), (PG8_LAS unsigned*)(lds + (bufoff) + ldsw + _i * 8192), 16, 0, 0); } while (0)
; #define PG8_LDA(dst, b, h) do { _Pragma("unroll") for (int m = 0; m < 4; ++m) _Pragma("unroll") for (int k = 0; k < 2; ++k) dst[m][k] = *(const PG8_LAS bf16x8*)(lds + PG8_SA(b, h) + aoff + m * 2048 + k * 1024); } while (0)
; #define PG8_LDB(dst, b, h) do { _Pragma("unroll") for (int n = 0; n < 2; ++n) _Pragma("unroll") for (int k = 0; k < 2; ++k) dst[n][k] = *(const PG8_LAS bf16x8*)(lds + PG8_SB(b, h) + boff + n * 2048 + k * 1024); } while (0)
; #define PG8_WAIT_V(n) asm volatile("s_waitcnt vmcnt(" #n ")" ::: "memory")
; #define PG8_WAIT_L(n) asm volatile("s_waitcnt lgkmcnt(" #n ")" ::: "memory")
; #define PG8_BAR __builtin_amdgcn_s_barrier()
; #define PG8_SCHED __builtin_amdgcn_sched_barrier(0)
; template <class Epi, class Sched, bool ALIGN_EPI = false, bool SP2 = false>
; __device__ __forceinline__ void gemm_phase(PG8_LAS unsigned char* lds, const Gemm g, const Sched& S, const Epi& E) {
;     ...
;         const char* nA = has_next ? (const char*)g.A + (size_t)nxt.pm * tstep + (size_t)nxt.k0 * 2 : cA; const char* nB = has_next ? (const char*)g.Bt + (size_t)nxt.pn * tstep + (size_t)nxt.k0 * 2 : cB;
;         for (int t = 0; t < nt; t += 2) {
;             const bool last = (t == nt - 2);
;             const char* a1 = cA + (size_t)(t + 1) * kstep;
;             const char* a2 = last ? nA : cA + (size_t)(t + 2) * kstep; const char* b2 = last ? nB : cB + (size_t)(t + 2) * kstep;
;             const char* a3 = a2 + kstep; const char* b3 = b2 + kstep;
;             if (last && has_next) S.a_ready(nxt);
;             if constexpr (SP2) {
;             PG8_LDB(B0, 0, 0); PG8_LDB(B1, 0, 1); PG8_SCHED; PG8_LDA(At, 0, 0); PG8_STAGE(PG8_SA(1, 1), a1 + hstep, voffA);
;             PG8_WAIT_V(8); PG8_WAIT_L(0); PG8_BAR; PG8_MMA(0, 0, At, B0); PG8_MMA(0, 1, At, B1); PG8_BAR; PG8_SCHED;
;             PG8_LDA(At, 0, 1); PG8_STAGE(PG8_SB(0, 0), b2, voffB); PG8_STAGE(PG8_SB(0, 1), b2 + hstep, voffB); PG8_STAGE(PG8_SA(0, 0), a2, voffA);
;             PG8_WAIT_V(8); PG8_WAIT_L(0); PG8_BAR; PG8_MMA(1, 0, At, B0); PG8_MMA(1, 1, At, B1); PG8_BAR; PG8_SCHED;
.LBB0_944:
	s_add_u32 s25, s16, s23
	s_addc_u32 s27, s17, 0
	s_add_u32 s38, s25, 0x100
	s_addc_u32 s39, s27, 0
	s_and_b64 s[36:37], s[34:35], exec
	s_cselect_b32 s39, s7, s39
	s_cselect_b32 s38, s6, s38
	s_add_u32 s23, s14, s23
	s_addc_u32 s36, s15, 0
	s_add_u32 s23, s23, 0x100
	s_addc_u32 s36, s36, 0
	s_and_b64 s[34:35], s[34:35], exec
	s_cselect_b32 s41, s29, s36
	s_cselect_b32 s40, s28, s23
	s_add_u32 s44, s25, 0x80080
	s_addc_u32 s45, s27, 0
	s_add_i32 s59, s49, s2
	ds_read_b128 v[144:147], v141
	ds_read_b128 v[148:151], v141 offset:1024
	ds_read_b128 v[152:155], v141 offset:2048
	ds_read_b128 v[156:159], v141 offset:3072
	ds_read_b128 v[166:169], v142
	ds_read_b128 v[170:173], v142 offset:1024
	ds_read_b128 v[174:177], v142 offset:2048
	ds_read_b128 v[178:181], v142 offset:3072
	s_add_i32 m0, s3, 0xc000
	s_add_i32 s60, s3, 0xe000
	s_add_i32 s56, s59, 0x2000
	s_add_u32 s42, s40, 0x80000
	s_addc_u32 s43, s41, 0
	s_add_i32 s58, s50, s2
	s_add_i32 s57, s58, 0x2000
	s_add_i32 s55, 0, 0x18000
	s_add_i32 s54, 0, 0x1c000
	s_add_u32 s36, s38, 0x80000
	s_addc_u32 s37, s39, 0
	s_add_i32 s53, s55, s2
	s_add_i32 s25, s53, 0x2000
	s_add_u32 s34, s40, 0x80080
	s_addc_u32 s35, s41, 0
	s_add_i32 s27, s54, s2
	s_add_i32 s23, s27, 0x2000
	v_lshl_add_u64 v[160:161], s[44:45], 0, v[132:133]
	ds_read_b128 v[182:185], v143
	ds_read_b128 v[190:193], v143 offset:1024
	ds_read_b128 v[194:197], v143 offset:2048
	ds_read_b128 v[198:201], v143 offset:3072
	ds_read_b128 v[202:205], v143 offset:4096
	ds_read_b128 v[206:209], v143 offset:5120
	ds_read_b128 v[210:213], v143 offset:6144
	ds_read_b128 v[214:217], v143 offset:7168
	global_load_lds_dwordx4 v[160:161], off
	v_lshl_add_u64 v[160:161], s[44:45], 0, v[130:131]
	s_mov_b32 m0, s60
	s_nop 0
	global_load_lds_dwordx4 v[160:161], off
	s_waitcnt vmcnt(8)
	s_waitcnt lgkmcnt(0)
	s_barrier
	s_setprio 1
	s_waitcnt lgkmcnt(0)
	v_mfma_f32_16x16x32_bf16 v[126:129], v[144:147], v[182:185], v[126:129]
	v_mfma_f32_16x16x32_bf16 v[122:125], v[152:155], v[182:185], v[122:125]
	v_mfma_f32_16x16x32_bf16 v[118:121], v[144:147], v[194:197], v[118:121]
	v_mfma_f32_16x16x32_bf16 v[114:117], v[152:155], v[194:197], v[114:117]
	v_mfma_f32_16x16x32_bf16 v[106:109], v[144:147], v[202:205], v[106:109]
	v_mfma_f32_16x16x32_bf16 v[98:101], v[152:155], v[202:205], v[98:101]
	v_mfma_f32_16x16x32_bf16 v[90:93], v[144:147], v[210:213], v[90:93]
	v_mfma_f32_16x16x32_bf16 v[82:85], v[152:155], v[210:213], v[82:85]
	v_mfma_f32_16x16x32_bf16 v[126:129], v[148:151], v[190:193], v[126:129]
	v_mfma_f32_16x16x32_bf16 v[122:125], v[156:159], v[190:193], v[122:125]
	v_mfma_f32_16x16x32_bf16 v[118:121], v[148:151], v[198:201], v[118:121]
	v_mfma_f32_16x16x32_bf16 v[114:117], v[156:159], v[198:201], v[114:117]
	v_mfma_f32_16x16x32_bf16 v[106:109], v[148:151], v[206:209], v[106:109]
	v_mfma_f32_16x16x32_bf16 v[98:101], v[156:159], v[206:209], v[98:101]
	v_mfma_f32_16x16x32_bf16 v[90:93], v[148:151], v[214:217], v[90:93]
	v_mfma_f32_16x16x32_bf16 v[82:85], v[156:159], v[214:217], v[82:85]
	v_mfma_f32_16x16x32_bf16 v[110:113], v[166:169], v[182:185], v[110:113]
	v_mfma_f32_16x16x32_bf16 v[102:105], v[174:177], v[182:185], v[102:105]
	v_mfma_f32_16x16x32_bf16 v[94:97], v[166:169], v[194:197], v[94:97]
	v_mfma_f32_16x16x32_bf16 v[86:89], v[174:177], v[194:197], v[86:89]
	v_mfma_f32_16x16x32_bf16 v[78:81], v[166:169], v[202:205], v[78:81]
	v_mfma_f32_16x16x32_bf16 v[74:77], v[174:177], v[202:205], v[74:77]
	v_mfma_f32_16x16x32_bf16 v[70:73], v[166:169], v[210:213], v[70:73]
	v_mfma_f32_16x16x32_bf16 v[66:69], v[174:177], v[210:213], v[66:69]
	v_mfma_f32_16x16x32_bf16 v[110:113], v[170:173], v[190:193], v[110:113]
	v_mfma_f32_16x16x32_bf16 v[102:105], v[178:181], v[190:193], v[102:105]
	v_mfma_f32_16x16x32_bf16 v[94:97], v[170:173], v[198:201], v[94:97]
	v_mfma_f32_16x16x32_bf16 v[86:89], v[178:181], v[198:201], v[86:89]
	v_mfma_f32_16x16x32_bf16 v[78:81], v[170:173], v[206:209], v[78:81]
	v_mfma_f32_16x16x32_bf16 v[74:77], v[178:181], v[206:209], v[74:77]
	v_mfma_f32_16x16x32_bf16 v[70:73], v[170:173], v[214:217], v[70:73]
	v_mfma_f32_16x16x32_bf16 v[66:69], v[178:181], v[214:217], v[66:69]
	s_setprio 0
	s_barrier
	s_mov_b32 m0, s59
	v_lshl_add_u64 v[160:161], s[40:41], 0, v[132:133]
	ds_read_b128 v[182:185], v143 offset:16384
	ds_read_b128 v[190:193], v143 offset:17408
	ds_read_b128 v[194:197], v143 offset:18432
	ds_read_b128 v[198:201], v143 offset:19456
	ds_read_b128 v[202:205], v143 offset:20480
	ds_read_b128 v[206:209], v143 offset:21504
	ds_read_b128 v[210:213], v143 offset:22528
	ds_read_b128 v[214:217], v143 offset:23552
	global_load_lds_dwordx4 v[160:161], off
	v_lshl_add_u64 v[186:187], s[40:41], 0, v[130:131]
	s_mov_b32 m0, s56
	v_lshl_add_u64 v[218:219], s[42:43], 0, v[132:133]
	global_load_lds_dwordx4 v[186:187], off
	s_mov_b32 m0, s58
	v_lshl_add_u64 v[220:221], s[38:39], 0, v[130:131]
	global_load_lds_dwordx4 v[218:219], off
	v_lshl_add_u64 v[218:219], s[42:43], 0, v[130:131]
	s_mov_b32 m0, s57
	s_nop 0
	global_load_lds_dwordx4 v[218:219], off
	v_lshl_add_u64 v[218:219], s[38:39], 0, v[132:133]
	s_mov_b32 m0, s3
	s_nop 0
	global_load_lds_dwordx4 v[218:219], off
	s_mov_b32 m0, s4
	s_nop 0
	global_load_lds_dwordx4 v[220:221], off
	s_waitcnt vmcnt(8)
	s_waitcnt lgkmcnt(0)
	s_barrier
; #define PG8_STAGE(bufoff, gbase, voff) do { _Pragma("unroll") for (int _i = 0; _i < 2; ++_i) \
;         __builtin_amdgcn_global_load_lds((const unsigned*)((const char*)(gbase) + (voff)[_i]), (PG8_LAS unsigned*)(lds + (bufoff) + ldsw + _i * 8192), 16, 0, 0); } while (0)
; #define PG8_LDA(dst, b, h) do { _Pragma("unroll") for (int m = 0; m < 4; ++m) _Pragma("unroll") for (int k = 0; k < 2; ++k) dst[m][k] = *(const PG8_LAS bf16x8*)(lds + PG8_SA(b, h) + aoff + m * 2048 + k * 1024); } while (0)
; #define PG8_LDB(dst, b, h) do { _Pragma("unroll") for (int n = 0; n < 2; ++n) _Pragma("unroll") for (int k = 0; k < 2; ++k) dst[n][k] = *(const PG8_LAS bf16x8*)(lds + PG8_SB(b, h) + boff + n * 2048 + k * 1024); } while (0)
; #define PG8_MMA(ai, bj, At, Bt) do { __builtin_amdgcn_s_setprio(1); _Pragma("unroll") for (int m = 0; m < 4; ++m) _Pragma("unroll") for (int n = 0; n < 2; ++n) _Pragma("unroll") for (int k = 0; k < 2; ++k) \
;         acc[ai][bj][m][n] = __builtin_amdgcn_mfma_f32_16x16x32_bf16(Bt[n][k], At[m][k], acc[ai][bj][m][n], 0, 0, 0); __builtin_amdgcn_s_setprio(0); } while (0)
; #define PG8_WAIT_V(n) asm volatile("s_waitcnt vmcnt(" #n ")" ::: "memory")
; #define PG8_WAIT_L(n) asm volatile("s_waitcnt lgkmcnt(" #n ")" ::: "memory")
; #define PG8_BAR __builtin_amdgcn_s_barrier()
; #define PG8_SCHED __builtin_amdgcn_sched_barrier(0)
; template <class Epi, class Sched, bool ALIGN_EPI = false, bool SP2 = false>
; __device__ __forceinline__ void gemm_phase(PG8_LAS unsigned char* lds, const Gemm g, const Sched& S, const Epi& E) {
;     ...
;             PG8_WAIT_V(8); PG8_WAIT_L(0); PG8_BAR; PG8_MMA(0, 0, At, B0); PG8_MMA(0, 1, At, B1); PG8_BAR; PG8_SCHED;
;             PG8_LDA(At, 0, 1); PG8_STAGE(PG8_SB(0, 0), b2, voffB); PG8_STAGE(PG8_SB(0, 1), b2 + hstep, voffB); PG8_STAGE(PG8_SA(0, 0), a2, voffA);
;             PG8_WAIT_V(8); PG8_WAIT_L(0); PG8_BAR; PG8_MMA(1, 0, At, B0); PG8_MMA(1, 1, At, B1); PG8_BAR; PG8_SCHED;
;             PG8_LDB(B0, 1, 0); PG8_LDB(B1, 1, 1); PG8_SCHED; PG8_LDA(At, 1, 0); PG8_STAGE(PG8_SA(0, 1), a2 + hstep, voffA);
;             PG8_WAIT_V(8); PG8_WAIT_L(0); PG8_BAR; PG8_MMA(0, 0, At, B0); PG8_MMA(0, 1, At, B1); PG8_BAR; PG8_SCHED;
	s_setprio 1
	s_waitcnt lgkmcnt(0)
	v_mfma_f32_16x16x32_bf16 v[62:65], v[144:147], v[182:185], v[62:65]
	v_mfma_f32_16x16x32_bf16 v[58:61], v[152:155], v[182:185], v[58:61]
	v_mfma_f32_16x16x32_bf16 v[54:57], v[144:147], v[194:197], v[54:57]
	v_mfma_f32_16x16x32_bf16 v[50:53], v[152:155], v[194:197], v[50:53]
	v_mfma_f32_16x16x32_bf16 v[38:41], v[144:147], v[202:205], v[38:41]
	v_mfma_f32_16x16x32_bf16 v[34:37], v[152:155], v[202:205], v[34:37]
	v_mfma_f32_16x16x32_bf16 v[22:25], v[144:147], v[210:213], v[22:25]
	v_mfma_f32_16x16x32_bf16 v[18:21], v[152:155], v[210:213], v[18:21]
	v_mfma_f32_16x16x32_bf16 v[62:65], v[148:151], v[190:193], v[62:65]
	v_mfma_f32_16x16x32_bf16 v[58:61], v[156:159], v[190:193], v[58:61]
	v_mfma_f32_16x16x32_bf16 v[54:57], v[148:151], v[198:201], v[54:57]
	v_mfma_f32_16x16x32_bf16 v[50:53], v[156:159], v[198:201], v[50:53]
	v_mfma_f32_16x16x32_bf16 v[38:41], v[148:151], v[206:209], v[38:41]
	v_mfma_f32_16x16x32_bf16 v[34:37], v[156:159], v[206:209], v[34:37]
	v_mfma_f32_16x16x32_bf16 v[22:25], v[148:151], v[214:217], v[22:25]
	v_mfma_f32_16x16x32_bf16 v[18:21], v[156:159], v[214:217], v[18:21]
	v_mfma_f32_16x16x32_bf16 v[46:49], v[166:169], v[182:185], v[46:49]
	v_mfma_f32_16x16x32_bf16 v[42:45], v[174:177], v[182:185], v[42:45]
	v_mfma_f32_16x16x32_bf16 v[30:33], v[166:169], v[194:197], v[30:33]
	v_mfma_f32_16x16x32_bf16 v[26:29], v[174:177], v[194:197], v[26:29]
	v_mfma_f32_16x16x32_bf16 v[14:17], v[166:169], v[202:205], v[14:17]
	v_mfma_f32_16x16x32_bf16 v[10:13], v[174:177], v[202:205], v[10:13]
	v_mfma_f32_16x16x32_bf16 v[6:9], v[166:169], v[210:213], v[6:9]
	v_mfma_f32_16x16x32_bf16 v[2:5], v[174:177], v[210:213], v[2:5]
	v_mfma_f32_16x16x32_bf16 v[46:49], v[170:173], v[190:193], v[46:49]
	v_mfma_f32_16x16x32_bf16 v[42:45], v[178:181], v[190:193], v[42:45]
	v_mfma_f32_16x16x32_bf16 v[30:33], v[170:173], v[198:201], v[30:33]
	v_mfma_f32_16x16x32_bf16 v[26:29], v[178:181], v[198:201], v[26:29]
	v_mfma_f32_16x16x32_bf16 v[14:17], v[170:173], v[206:209], v[14:17]
	v_mfma_f32_16x16x32_bf16 v[10:13], v[178:181], v[206:209], v[10:13]
	v_mfma_f32_16x16x32_bf16 v[6:9], v[170:173], v[214:217], v[6:9]
	v_mfma_f32_16x16x32_bf16 v[2:5], v[178:181], v[214:217], v[2:5]
	s_setprio 0
	s_barrier
	v_add_u32_e32 v156, s55, v138
	v_add_u32_e32 v162, s54, v138
	ds_read_b128 v[144:147], v156
	ds_read_b128 v[148:151], v156 offset:1024
	ds_read_b128 v[152:155], v156 offset:2048
	ds_read_b128 v[156:159], v156 offset:3072
	ds_read_b128 v[166:169], v162
	ds_read_b128 v[170:173], v162 offset:1024
	ds_read_b128 v[174:177], v162 offset:2048
	ds_read_b128 v[178:181], v162 offset:3072
	s_mov_b32 m0, s5
	v_lshl_add_u64 v[222:223], s[36:37], 0, v[132:133]
	ds_read_b128 v[182:185], v143 offset:32768
	ds_read_b128 v[190:193], v143 offset:33792
	ds_read_b128 v[194:197], v143 offset:34816
	ds_read_b128 v[198:201], v143 offset:35840
	ds_read_b128 v[202:205], v143 offset:36864
	ds_read_b128 v[206:209], v143 offset:37888
	ds_read_b128 v[210:213], v143 offset:38912
	ds_read_b128 v[214:217], v143 offset:39936
	global_load_lds_dwordx4 v[222:223], off
	v_lshl_add_u64 v[222:223], s[36:37], 0, v[130:131]
	s_mov_b32 m0, s11
	s_nop 0
	global_load_lds_dwordx4 v[222:223], off
	s_waitcnt vmcnt(8)
	s_waitcnt lgkmcnt(0)
	s_barrier
	s_setprio 1
	s_waitcnt lgkmcnt(0)
	v_mfma_f32_16x16x32_bf16 v[126:129], v[144:147], v[182:185], v[126:129]
	v_mfma_f32_16x16x32_bf16 v[122:125], v[152:155], v[182:185], v[122:125]
	v_mfma_f32_16x16x32_bf16 v[118:121], v[144:147], v[194:197], v[118:121]
	v_mfma_f32_16x16x32_bf16 v[114:117], v[152:155], v[194:197], v[114:117]
	v_mfma_f32_16x16x32_bf16 v[106:109], v[144:147], v[202:205], v[106:109]
	v_mfma_f32_16x16x32_bf16 v[98:101], v[152:155], v[202:205], v[98:101]
	v_mfma_f32_16x16x32_bf16 v[90:93], v[144:147], v[210:213], v[90:93]
	v_mfma_f32_16x16x32_bf16 v[82:85], v[152:155], v[210:213], v[82:85]
	v_mfma_f32_16x16x32_bf16 v[126:129], v[148:151], v[190:193], v[126:129]
	v_mfma_f32_16x16x32_bf16 v[122:125], v[156:159], v[190:193], v[122:125]
	v_mfma_f32_16x16x32_bf16 v[118:121], v[148:151], v[198:201], v[118:121]
	v_mfma_f32_16x16x32_bf16 v[114:117], v[156:159], v[198:201], v[114:117]
	v_mfma_f32_16x16x32_bf16 v[106:109], v[148:151], v[206:209], v[106:109]
	v_mfma_f32_16x16x32_bf16 v[98:101], v[156:159], v[206:209], v[98:101]
	v_mfma_f32_16x16x32_bf16 v[90:93], v[148:151], v[214:217], v[90:93]
	v_mfma_f32_16x16x32_bf16 v[82:85], v[156:159], v[214:217], v[82:85]
	v_mfma_f32_16x16x32_bf16 v[110:113], v[166:169], v[182:185], v[110:113]
	v_mfma_f32_16x16x32_bf16 v[102:105], v[174:177], v[182:185], v[102:105]
	v_mfma_f32_16x16x32_bf16 v[94:97], v[166:169], v[194:197], v[94:97]
	v_mfma_f32_16x16x32_bf16 v[86:89], v[174:177], v[194:197], v[86:89]
	v_mfma_f32_16x16x32_bf16 v[78:81], v[166:169], v[202:205], v[78:81]
	v_mfma_f32_16x16x32_bf16 v[74:77], v[174:177], v[202:205], v[74:77]
	v_mfma_f32_16x16x32_bf16 v[70:73], v[166:169], v[210:213], v[70:73]
	v_mfma_f32_16x16x32_bf16 v[66:69], v[174:177], v[210:213], v[66:69]
	v_mfma_f32_16x16x32_bf16 v[110:113], v[170:173], v[190:193], v[110:113]
	v_mfma_f32_16x16x32_bf16 v[102:105], v[178:181], v[190:193], v[102:105]
	v_mfma_f32_16x16x32_bf16 v[94:97], v[170:173], v[198:201], v[94:97]
	v_mfma_f32_16x16x32_bf16 v[86:89], v[178:181], v[198:201], v[86:89]
	v_mfma_f32_16x16x32_bf16 v[78:81], v[170:173], v[206:209], v[78:81]
	v_mfma_f32_16x16x32_bf16 v[74:77], v[178:181], v[206:209], v[74:77]
	v_mfma_f32_16x16x32_bf16 v[70:73], v[170:173], v[214:217], v[70:73]
	v_mfma_f32_16x16x32_bf16 v[66:69], v[178:181], v[214:217], v[66:69]
	s_setprio 0
	s_barrier
; #define PG8_STAGE(bufoff, gbase, voff) do { _Pragma("unroll") for (int _i = 0; _i < 2; ++_i) \
;         __builtin_amdgcn_global_load_lds((const unsigned*)((const char*)(gbase) + (voff)[_i]), (PG8_LAS unsigned*)(lds + (bufoff) + ldsw + _i * 8192), 16, 0, 0); } while (0)
; #define PG8_LDA(dst, b, h) do { _Pragma("unroll") for (int m = 0; m < 4; ++m) _Pragma("unroll") for (int k = 0; k < 2; ++k) dst[m][k] = *(const PG8_LAS bf16x8*)(lds + PG8_SA(b, h) + aoff + m * 2048 + k * 1024); } while (0)
; #define PG8_WAIT_V(n) asm volatile("s_waitcnt vmcnt(" #n ")" ::: "memory")
; template <class Epi, class Sched, bool ALIGN_EPI = false, bool SP2 = false>
; __device__ __forceinline__ void gemm_phase(PG8_LAS unsigned char* lds, const Gemm g, const Sched& S, const Epi& E) {
;     ...
;             PG8_LDA(At, 1, 1); PG8_STAGE(PG8_SB(1, 0), b3, voffB); PG8_STAGE(PG8_SB(1, 1), b3 + hstep, voffB); PG8_STAGE(PG8_SA(1, 0), a3, voffA);
;             PG8_WAIT_V(8); PG8_WAIT_L(0); PG8_BAR; PG8_MMA(1, 0, At, B0); PG8_MMA(1, 1, At, B1); PG8_BAR; PG8_SCHED;
;             } else {
;             PG8_LDB(B0, 0, 0); PG8_SCHED; PG8_LDA(At, 0, 0); PG8_STAGE(PG8_SA(1, 1), a1 + hstep, voffA);
;             PG8_WAIT_L(8); PG8_BAR; PG8_WAIT_L(0); PG8_MMA(0, 0, At, B0); PG8_BAR; PG8_SCHED;
;             PG8_LDB(B1, 0, 1); PG8_STAGE(PG8_SB(0, 0), b2, voffB);
;             PG8_BAR; PG8_WAIT_L(0); PG8_MMA(0, 1, At, B1); PG8_BAR;
;             PG8_LDA(At, 0, 1); PG8_STAGE(PG8_SA(0, 0), a2, voffA);
;             PG8_BAR; PG8_WAIT_L(0); PG8_MMA(1, 0, At, B0); PG8_BAR; PG8_SCHED;
;             PG8_STAGE(PG8_SB(0, 1), b2 + hstep, voffB);
;             PG8_WAIT_V(6); PG8_BAR; PG8_MMA(1, 1, At, B1); PG8_BAR;
;             PG8_LDB(B0, 1, 0); PG8_SCHED; PG8_LDA(At, 1, 0); PG8_STAGE(PG8_SA(0, 1), a2 + hstep, voffA);
;             PG8_WAIT_L(8); PG8_BAR; PG8_WAIT_L(0); PG8_MMA(0, 0, At, B0); PG8_BAR; PG8_SCHED;
;             PG8_LDB(B1, 1, 1); PG8_STAGE(PG8_SB(1, 0), b3, voffB);
;             PG8_BAR; PG8_WAIT_L(0); PG8_MMA(0, 1, At, B1); PG8_BAR;
;             PG8_LDA(At, 1, 1); PG8_STAGE(PG8_SA(1, 0), a3, voffA);
;             PG8_BAR; PG8_WAIT_L(0); PG8_MMA(1, 0, At, B0); PG8_BAR; PG8_SCHED;
;             PG8_STAGE(PG8_SB(1, 1), b3 + hstep, voffB);
;             PG8_WAIT_V(6); PG8_BAR; PG8_MMA(1, 1, At, B1); PG8_BAR;
;             }
;         }
;         if constexpr (ALIGN_EPI) { if (wr == 0) PG8_BAR; }
	s_mov_b32 m0, s53
	v_lshl_add_u64 v[160:161], v[160:161], 0, s[18:19]
	ds_read_b128 v[182:185], v143 offset:49152
	ds_read_b128 v[190:193], v143 offset:50176
	ds_read_b128 v[194:197], v143 offset:51200
	ds_read_b128 v[198:201], v143 offset:52224
	ds_read_b128 v[202:205], v143 offset:53248
	ds_read_b128 v[206:209], v143 offset:54272
	ds_read_b128 v[210:213], v143 offset:55296
	ds_read_b128 v[214:217], v143 offset:56320
	global_load_lds_dwordx4 v[160:161], off
	v_lshl_add_u64 v[160:161], v[186:187], 0, s[18:19]
	s_mov_b32 m0, s25
	s_nop 0
	global_load_lds_dwordx4 v[160:161], off
	v_lshl_add_u64 v[160:161], s[34:35], 0, v[132:133]
	s_mov_b32 m0, s27
	s_nop 0
	global_load_lds_dwordx4 v[160:161], off
	v_lshl_add_u64 v[160:161], s[34:35], 0, v[130:131]
	s_mov_b32 m0, s23
	s_nop 0
	global_load_lds_dwordx4 v[160:161], off
	v_lshl_add_u64 v[160:161], v[218:219], 0, s[18:19]
	s_mov_b32 m0, s33
	s_nop 0
	global_load_lds_dwordx4 v[160:161], off
	v_lshl_add_u64 v[160:161], v[220:221], 0, s[18:19]
	s_mov_b32 m0, s48
	s_nop 0
	global_load_lds_dwordx4 v[160:161], off
	s_waitcnt vmcnt(8)
	s_waitcnt lgkmcnt(0)
	s_barrier
	s_setprio 1
	s_waitcnt lgkmcnt(0)
	v_mfma_f32_16x16x32_bf16 v[62:65], v[144:147], v[182:185], v[62:65]
	v_mfma_f32_16x16x32_bf16 v[58:61], v[152:155], v[182:185], v[58:61]
	v_mfma_f32_16x16x32_bf16 v[54:57], v[144:147], v[194:197], v[54:57]
	v_mfma_f32_16x16x32_bf16 v[50:53], v[152:155], v[194:197], v[50:53]
	v_mfma_f32_16x16x32_bf16 v[38:41], v[144:147], v[202:205], v[38:41]
	v_mfma_f32_16x16x32_bf16 v[34:37], v[152:155], v[202:205], v[34:37]
	v_mfma_f32_16x16x32_bf16 v[22:25], v[144:147], v[210:213], v[22:25]
	v_mfma_f32_16x16x32_bf16 v[18:21], v[152:155], v[210:213], v[18:21]
	v_mfma_f32_16x16x32_bf16 v[62:65], v[148:151], v[190:193], v[62:65]
	v_mfma_f32_16x16x32_bf16 v[58:61], v[156:159], v[190:193], v[58:61]
	v_mfma_f32_16x16x32_bf16 v[54:57], v[148:151], v[198:201], v[54:57]
	v_mfma_f32_16x16x32_bf16 v[50:53], v[156:159], v[198:201], v[50:53]
	v_mfma_f32_16x16x32_bf16 v[38:41], v[148:151], v[206:209], v[38:41]
	v_mfma_f32_16x16x32_bf16 v[34:37], v[156:159], v[206:209], v[34:37]
	v_mfma_f32_16x16x32_bf16 v[22:25], v[148:151], v[214:217], v[22:25]
	v_mfma_f32_16x16x32_bf16 v[18:21], v[156:159], v[214:217], v[18:21]
	v_mfma_f32_16x16x32_bf16 v[46:49], v[166:169], v[182:185], v[46:49]
	v_mfma_f32_16x16x32_bf16 v[42:45], v[174:177], v[182:185], v[42:45]
	v_mfma_f32_16x16x32_bf16 v[30:33], v[166:169], v[194:197], v[30:33]
	v_mfma_f32_16x16x32_bf16 v[26:29], v[174:177], v[194:197], v[26:29]
	v_mfma_f32_16x16x32_bf16 v[14:17], v[166:169], v[202:205], v[14:17]
	v_mfma_f32_16x16x32_bf16 v[10:13], v[174:177], v[202:205], v[10:13]
	v_mfma_f32_16x16x32_bf16 v[6:9], v[166:169], v[210:213], v[6:9]
	v_mfma_f32_16x16x32_bf16 v[2:5], v[174:177], v[210:213], v[2:5]
	v_mfma_f32_16x16x32_bf16 v[46:49], v[170:173], v[190:193], v[46:49]
	v_mfma_f32_16x16x32_bf16 v[42:45], v[178:181], v[190:193], v[42:45]
	v_mfma_f32_16x16x32_bf16 v[30:33], v[170:173], v[198:201], v[30:33]
	v_mfma_f32_16x16x32_bf16 v[26:29], v[178:181], v[198:201], v[26:29]
	v_mfma_f32_16x16x32_bf16 v[14:17], v[170:173], v[206:209], v[14:17]
	v_mfma_f32_16x16x32_bf16 v[10:13], v[178:181], v[206:209], v[10:13]
	v_mfma_f32_16x16x32_bf16 v[6:9], v[170:173], v[214:217], v[6:9]
	v_mfma_f32_16x16x32_bf16 v[2:5], v[178:181], v[214:217], v[2:5]
	s_setprio 0
	s_barrier
	s_movk_i32 s23, 0x100
	s_andn2_b64 vcc, exec, s[30:31]
	s_mov_b64 s[34:35], -1
	s_mov_b64 s[30:31], 0
	s_cbranch_vccz .LBB0_944
	s_and_b64 vcc, exec, s[20:21]
	s_cbranch_vccz .LBB0_947
	s_barrier

; #define PG8_STAGE(bufoff, gbase, voff) do { _Pragma("unroll") for (int _i = 0; _i < 2; ++_i) \
;         __builtin_amdgcn_global_load_lds((const unsigned*)((const char*)(gbase) + (voff)[_i]), (PG8_LAS unsigned*)(lds + (bufoff) + ldsw + _i * 8192), 16, 0, 0); } while (0)
; #define PG8_LDA(dst, b, h) do { _Pragma("unroll") for (int m = 0; m < 4; ++m) _Pragma("unroll") for (int k = 0; k < 2; ++k) dst[m][k] = *(const PG8_LAS bf16x8*)(lds + PG8_SA(b, h) + aoff + m * 2048 + k * 1024); } while (0)
; #define PG8_LDB(dst, b, h) do { _Pragma("unroll") for (int n = 0; n < 2; ++n) _Pragma("unroll") for (int k = 0; k < 2; ++k) dst[n][k] = *(const PG8_LAS bf16x8*)(lds + PG8_SB(b, h) + boff + n * 2048 + k * 1024); } while (0)
; #define PG8_WAIT_V(n) asm volatile("s_waitcnt vmcnt(" #n ")" ::: "memory")
; #define PG8_WAIT_L(n) asm volatile("s_waitcnt lgkmcnt(" #n ")" ::: "memory")
; #define PG8_BAR __builtin_amdgcn_s_barrier()
; #define PG8_SCHED __builtin_amdgcn_sched_barrier(0)
; template <class Epi, class Sched, bool ALIGN_EPI = false, bool SP2 = false>
; __device__ __forceinline__ void gemm_phase(PG8_LAS unsigned char* lds, const Gemm g, const Sched& S, const Epi& E) {
;     ...
;         const char* nA = has_next ? (const char*)g.A + (size_t)nxt.pm * tstep + (size_t)nxt.k0 * 2 : cA; const char* nB = has_next ? (const char*)g.Bt + (size_t)nxt.pn * tstep + (size_t)nxt.k0 * 2 : cB;
;         for (int t = 0; t < nt; t += 2) {
;             const bool last = (t == nt - 2);
;             const char* a1 = cA + (size_t)(t + 1) * kstep;
;             const char* a2 = last ? nA : cA + (size_t)(t + 2) * kstep; const char* b2 = last ? nB : cB + (size_t)(t + 2) * kstep;
;             const char* a3 = a2 + kstep; const char* b3 = b2 + kstep;
;             if (last && has_next) S.a_ready(nxt);
;             if constexpr (SP2) {
;             PG8_LDB(B0, 0, 0); PG8_LDB(B1, 0, 1); PG8_SCHED; PG8_LDA(At, 0, 0); PG8_STAGE(PG8_SA(1, 1), a1 + hstep, voffA);
;             PG8_WAIT_V(8); PG8_WAIT_L(0); PG8_BAR; PG8_MMA(0, 0, At, B0); PG8_MMA(0, 1, At, B1); PG8_BAR; PG8_SCHED;
;             PG8_LDA(At, 0, 1); PG8_STAGE(PG8_SB(0, 0), b2, voffB); PG8_STAGE(PG8_SB(0, 1), b2 + hstep, voffB); PG8_STAGE(PG8_SA(0, 0), a2, voffA);
;             PG8_WAIT_V(8); PG8_WAIT_L(0); PG8_BAR; PG8_MMA(1, 0, At, B0); PG8_MMA(1, 1, At, B1); PG8_BAR; PG8_SCHED;
.LBB0_1086:
	ds_read_b128 v[146:149], v153
	ds_read_b128 v[156:159], v153 offset:1024
	ds_read_b128 v[166:169], v153 offset:2048
	ds_read_b128 v[170:173], v153 offset:3072
	ds_read_b128 v[174:177], v154
	ds_read_b128 v[178:181], v154 offset:1024
	ds_read_b128 v[182:185], v154 offset:2048
	ds_read_b128 v[190:193], v154 offset:3072
	s_add_u32 s28, s26, 0xfff80080
	s_addc_u32 s29, s27, -1
	s_cmp_eq_u32 s44, 28
	s_cselect_b32 s31, s19, s29
	s_cselect_b32 s30, s40, s28
	s_cselect_b32 s29, s17, s43
	s_cselect_b32 s28, s41, s42
	v_lshl_add_u64 v[160:161], s[26:27], 0, v[138:139]
	s_add_i32 m0, s4, 0xc000
	ds_read_b128 v[194:197], v155
	ds_read_b128 v[198:201], v155 offset:1024
	ds_read_b128 v[202:205], v155 offset:2048
	ds_read_b128 v[206:209], v155 offset:3072
	ds_read_b128 v[210:213], v155 offset:4096
	ds_read_b128 v[214:217], v155 offset:5120
	ds_read_b128 v[218:221], v155 offset:6144
	ds_read_b128 v[222:225], v155 offset:7168
	global_load_lds_dwordx4 v[160:161], off
	v_lshl_add_u64 v[160:161], s[26:27], 0, v[140:141]
	s_add_i32 m0, s4, 0xe000
	s_nop 0
	global_load_lds_dwordx4 v[160:161], off
	s_waitcnt vmcnt(8)
	s_waitcnt lgkmcnt(0)
	s_barrier
	s_setprio 1
	s_waitcnt lgkmcnt(0)
	v_mfma_f32_16x16x32_bf16 v[126:129], v[146:149], v[194:197], v[126:129]
	v_mfma_f32_16x16x32_bf16 v[118:121], v[166:169], v[194:197], v[118:121]
	v_mfma_f32_16x16x32_bf16 v[110:113], v[146:149], v[202:205], v[110:113]
	v_mfma_f32_16x16x32_bf16 v[102:105], v[166:169], v[202:205], v[102:105]
	v_mfma_f32_16x16x32_bf16 v[94:97], v[146:149], v[210:213], v[94:97]
	v_mfma_f32_16x16x32_bf16 v[86:89], v[166:169], v[210:213], v[86:89]
	v_mfma_f32_16x16x32_bf16 v[78:81], v[146:149], v[218:221], v[78:81]
	v_mfma_f32_16x16x32_bf16 v[70:73], v[166:169], v[218:221], v[70:73]
	v_mfma_f32_16x16x32_bf16 v[126:129], v[156:159], v[198:201], v[126:129]
	v_mfma_f32_16x16x32_bf16 v[118:121], v[170:173], v[198:201], v[118:121]
	v_mfma_f32_16x16x32_bf16 v[110:113], v[156:159], v[206:209], v[110:113]
	v_mfma_f32_16x16x32_bf16 v[102:105], v[170:173], v[206:209], v[102:105]
	v_mfma_f32_16x16x32_bf16 v[94:97], v[156:159], v[214:217], v[94:97]
	v_mfma_f32_16x16x32_bf16 v[86:89], v[170:173], v[214:217], v[86:89]
	v_mfma_f32_16x16x32_bf16 v[78:81], v[156:159], v[222:225], v[78:81]
	v_mfma_f32_16x16x32_bf16 v[70:73], v[170:173], v[222:225], v[70:73]
	v_mfma_f32_16x16x32_bf16 v[122:125], v[174:177], v[194:197], v[122:125]
	v_mfma_f32_16x16x32_bf16 v[114:117], v[182:185], v[194:197], v[114:117]
	v_mfma_f32_16x16x32_bf16 v[106:109], v[174:177], v[202:205], v[106:109]
	v_mfma_f32_16x16x32_bf16 v[98:101], v[182:185], v[202:205], v[98:101]
	v_mfma_f32_16x16x32_bf16 v[90:93], v[174:177], v[210:213], v[90:93]
	v_mfma_f32_16x16x32_bf16 v[82:85], v[182:185], v[210:213], v[82:85]
	v_mfma_f32_16x16x32_bf16 v[74:77], v[174:177], v[218:221], v[74:77]
	v_mfma_f32_16x16x32_bf16 v[66:69], v[182:185], v[218:221], v[66:69]
	v_mfma_f32_16x16x32_bf16 v[122:125], v[178:181], v[198:201], v[122:125]
	v_mfma_f32_16x16x32_bf16 v[114:117], v[190:193], v[198:201], v[114:117]
	v_mfma_f32_16x16x32_bf16 v[106:109], v[178:181], v[206:209], v[106:109]
	v_mfma_f32_16x16x32_bf16 v[98:101], v[190:193], v[206:209], v[98:101]
	v_mfma_f32_16x16x32_bf16 v[90:93], v[178:181], v[214:217], v[90:93]
	v_mfma_f32_16x16x32_bf16 v[82:85], v[190:193], v[214:217], v[82:85]
	v_mfma_f32_16x16x32_bf16 v[74:77], v[178:181], v[222:225], v[74:77]
	v_mfma_f32_16x16x32_bf16 v[66:69], v[190:193], v[222:225], v[66:69]
	s_setprio 0
	s_barrier
	s_add_i32 s45, s37, s2
	v_lshl_add_u64 v[160:161], s[28:29], 0, v[134:135]
	s_mov_b32 m0, s45
	ds_read_b128 v[194:197], v155 offset:16384
	ds_read_b128 v[198:201], v155 offset:17408
	ds_read_b128 v[202:205], v155 offset:18432
	ds_read_b128 v[206:209], v155 offset:19456
	ds_read_b128 v[210:213], v155 offset:20480
	ds_read_b128 v[214:217], v155 offset:21504
	ds_read_b128 v[218:221], v155 offset:22528
	ds_read_b128 v[222:225], v155 offset:23552
	global_load_lds_dwordx4 v[160:161], off
	s_add_i32 m0, s45, 0x2000
	s_add_u32 s48, s28, 0x80000
	v_lshl_add_u64 v[186:187], s[28:29], 0, v[130:131]
	s_addc_u32 s49, s29, 0
	s_add_i32 s45, s38, s2
	global_load_lds_dwordx4 v[186:187], off
	v_lshl_add_u64 v[226:227], s[48:49], 0, v[134:135]
	s_mov_b32 m0, s45
	v_lshl_add_u64 v[228:229], s[30:31], 0, v[132:133]
	global_load_lds_dwordx4 v[226:227], off
	v_lshl_add_u64 v[226:227], s[48:49], 0, v[130:131]
	s_add_i32 m0, s45, 0x2000
	s_nop 0
	global_load_lds_dwordx4 v[226:227], off
	v_lshl_add_u64 v[226:227], s[30:31], 0, v[136:137]
	s_mov_b32 m0, s4
	s_nop 0
	global_load_lds_dwordx4 v[226:227], off
	s_mov_b32 m0, s5
	s_nop 0
	global_load_lds_dwordx4 v[228:229], off
	s_waitcnt vmcnt(8)
	s_waitcnt lgkmcnt(0)
	s_barrier
; #define PG8_STAGE(bufoff, gbase, voff) do { _Pragma("unroll") for (int _i = 0; _i < 2; ++_i) \
;         __builtin_amdgcn_global_load_lds((const unsigned*)((const char*)(gbase) + (voff)[_i]), (PG8_LAS unsigned*)(lds + (bufoff) + ldsw + _i * 8192), 16, 0, 0); } while (0)
; #define PG8_LDA(dst, b, h) do { _Pragma("unroll") for (int m = 0; m < 4; ++m) _Pragma("unroll") for (int k = 0; k < 2; ++k) dst[m][k] = *(const PG8_LAS bf16x8*)(lds + PG8_SA(b, h) + aoff + m * 2048 + k * 1024); } while (0)
; #define PG8_LDB(dst, b, h) do { _Pragma("unroll") for (int n = 0; n < 2; ++n) _Pragma("unroll") for (int k = 0; k < 2; ++k) dst[n][k] = *(const PG8_LAS bf16x8*)(lds + PG8_SB(b, h) + boff + n * 2048 + k * 1024); } while (0)
; #define PG8_MMA(ai, bj, At, Bt) do { __builtin_amdgcn_s_setprio(1); _Pragma("unroll") for (int m = 0; m < 4; ++m) _Pragma("unroll") for (int n = 0; n < 2; ++n) _Pragma("unroll") for (int k = 0; k < 2; ++k) \
;         acc[ai][bj][m][n] = __builtin_amdgcn_mfma_f32_16x16x32_bf16(Bt[n][k], At[m][k], acc[ai][bj][m][n], 0, 0, 0); __builtin_amdgcn_s_setprio(0); } while (0)
; #define PG8_WAIT_V(n) asm volatile("s_waitcnt vmcnt(" #n ")" ::: "memory")
; #define PG8_WAIT_L(n) asm volatile("s_waitcnt lgkmcnt(" #n ")" ::: "memory")
; #define PG8_BAR __builtin_amdgcn_s_barrier()
; #define PG8_SCHED __builtin_amdgcn_sched_barrier(0)
; template <class Epi, class Sched, bool ALIGN_EPI = false, bool SP2 = false>
; __device__ __forceinline__ void gemm_phase(PG8_LAS unsigned char* lds, const Gemm g, const Sched& S, const Epi& E) {
;     ...
;             PG8_WAIT_V(8); PG8_WAIT_L(0); PG8_BAR; PG8_MMA(0, 0, At, B0); PG8_MMA(0, 1, At, B1); PG8_BAR; PG8_SCHED;
;             PG8_LDA(At, 0, 1); PG8_STAGE(PG8_SB(0, 0), b2, voffB); PG8_STAGE(PG8_SB(0, 1), b2 + hstep, voffB); PG8_STAGE(PG8_SA(0, 0), a2, voffA);
;             PG8_WAIT_V(8); PG8_WAIT_L(0); PG8_BAR; PG8_MMA(1, 0, At, B0); PG8_MMA(1, 1, At, B1); PG8_BAR; PG8_SCHED;
;             PG8_LDB(B0, 1, 0); PG8_LDB(B1, 1, 1); PG8_SCHED; PG8_LDA(At, 1, 0); PG8_STAGE(PG8_SA(0, 1), a2 + hstep, voffA);
;             PG8_WAIT_V(8); PG8_WAIT_L(0); PG8_BAR; PG8_MMA(0, 0, At, B0); PG8_MMA(0, 1, At, B1); PG8_BAR; PG8_SCHED;
	s_setprio 1
	s_waitcnt lgkmcnt(0)
	v_mfma_f32_16x16x32_bf16 v[62:65], v[146:149], v[194:197], v[62:65]
	v_mfma_f32_16x16x32_bf16 v[54:57], v[166:169], v[194:197], v[54:57]
	v_mfma_f32_16x16x32_bf16 v[46:49], v[146:149], v[202:205], v[46:49]
	v_mfma_f32_16x16x32_bf16 v[38:41], v[166:169], v[202:205], v[38:41]
	v_mfma_f32_16x16x32_bf16 v[30:33], v[146:149], v[210:213], v[30:33]
	v_mfma_f32_16x16x32_bf16 v[22:25], v[166:169], v[210:213], v[22:25]
	v_mfma_f32_16x16x32_bf16 v[14:17], v[146:149], v[218:221], v[14:17]
	v_mfma_f32_16x16x32_bf16 v[6:9], v[166:169], v[218:221], v[6:9]
	v_mfma_f32_16x16x32_bf16 v[62:65], v[156:159], v[198:201], v[62:65]
	v_mfma_f32_16x16x32_bf16 v[54:57], v[170:173], v[198:201], v[54:57]
	v_mfma_f32_16x16x32_bf16 v[46:49], v[156:159], v[206:209], v[46:49]
	v_mfma_f32_16x16x32_bf16 v[38:41], v[170:173], v[206:209], v[38:41]
	v_mfma_f32_16x16x32_bf16 v[30:33], v[156:159], v[214:217], v[30:33]
	v_mfma_f32_16x16x32_bf16 v[22:25], v[170:173], v[214:217], v[22:25]
	v_mfma_f32_16x16x32_bf16 v[14:17], v[156:159], v[222:225], v[14:17]
	v_mfma_f32_16x16x32_bf16 v[6:9], v[170:173], v[222:225], v[6:9]
	v_mfma_f32_16x16x32_bf16 v[58:61], v[174:177], v[194:197], v[58:61]
	v_mfma_f32_16x16x32_bf16 v[50:53], v[182:185], v[194:197], v[50:53]
	v_mfma_f32_16x16x32_bf16 v[42:45], v[174:177], v[202:205], v[42:45]
	v_mfma_f32_16x16x32_bf16 v[34:37], v[182:185], v[202:205], v[34:37]
	v_mfma_f32_16x16x32_bf16 v[26:29], v[174:177], v[210:213], v[26:29]
	v_mfma_f32_16x16x32_bf16 v[18:21], v[182:185], v[210:213], v[18:21]
	v_mfma_f32_16x16x32_bf16 v[10:13], v[174:177], v[218:221], v[10:13]
	v_mfma_f32_16x16x32_bf16 v[2:5], v[182:185], v[218:221], v[2:5]
	v_mfma_f32_16x16x32_bf16 v[58:61], v[178:181], v[198:201], v[58:61]
	v_mfma_f32_16x16x32_bf16 v[50:53], v[190:193], v[198:201], v[50:53]
	v_mfma_f32_16x16x32_bf16 v[42:45], v[178:181], v[206:209], v[42:45]
	v_mfma_f32_16x16x32_bf16 v[34:37], v[190:193], v[206:209], v[34:37]
	v_mfma_f32_16x16x32_bf16 v[26:29], v[178:181], v[214:217], v[26:29]
	v_mfma_f32_16x16x32_bf16 v[18:21], v[190:193], v[214:217], v[18:21]
	v_mfma_f32_16x16x32_bf16 v[10:13], v[178:181], v[222:225], v[10:13]
	v_mfma_f32_16x16x32_bf16 v[2:5], v[190:193], v[222:225], v[2:5]
	s_setprio 0
	s_barrier
	s_add_i32 s45, 0, 0x18000
	v_add_u32_e32 v162, s45, v151
	s_add_i32 s48, 0, 0x1c000
	ds_read_b128 v[146:149], v162
	ds_read_b128 v[156:159], v162 offset:1024
	ds_read_b128 v[166:169], v162 offset:2048
	ds_read_b128 v[170:173], v162 offset:3072
	v_add_u32_e32 v162, s48, v151
	ds_read_b128 v[174:177], v162
	ds_read_b128 v[178:181], v162 offset:1024
	ds_read_b128 v[182:185], v162 offset:2048
	ds_read_b128 v[190:193], v162 offset:3072
	s_add_u32 s30, s30, 0x80000
	s_addc_u32 s31, s31, 0
	s_mov_b32 m0, s11
	v_lshl_add_u64 v[230:231], s[30:31], 0, v[136:137]
	ds_read_b128 v[194:197], v155 offset:32768
	ds_read_b128 v[198:201], v155 offset:33792
	ds_read_b128 v[202:205], v155 offset:34816
	ds_read_b128 v[206:209], v155 offset:35840
	ds_read_b128 v[210:213], v155 offset:36864
	ds_read_b128 v[214:217], v155 offset:37888
	ds_read_b128 v[218:221], v155 offset:38912
	ds_read_b128 v[222:225], v155 offset:39936
	global_load_lds_dwordx4 v[230:231], off
	v_lshl_add_u64 v[230:231], s[30:31], 0, v[132:133]
	s_mov_b32 m0, s33
	s_nop 0
	global_load_lds_dwordx4 v[230:231], off
	s_waitcnt vmcnt(8)
	s_waitcnt lgkmcnt(0)
	s_barrier
	s_setprio 1
	s_waitcnt lgkmcnt(0)
	v_mfma_f32_16x16x32_bf16 v[126:129], v[146:149], v[194:197], v[126:129]
	v_mfma_f32_16x16x32_bf16 v[118:121], v[166:169], v[194:197], v[118:121]
	v_mfma_f32_16x16x32_bf16 v[110:113], v[146:149], v[202:205], v[110:113]
	v_mfma_f32_16x16x32_bf16 v[102:105], v[166:169], v[202:205], v[102:105]
	v_mfma_f32_16x16x32_bf16 v[94:97], v[146:149], v[210:213], v[94:97]
	v_mfma_f32_16x16x32_bf16 v[86:89], v[166:169], v[210:213], v[86:89]
	v_mfma_f32_16x16x32_bf16 v[78:81], v[146:149], v[218:221], v[78:81]
	v_mfma_f32_16x16x32_bf16 v[70:73], v[166:169], v[218:221], v[70:73]
	v_mfma_f32_16x16x32_bf16 v[126:129], v[156:159], v[198:201], v[126:129]
	v_mfma_f32_16x16x32_bf16 v[118:121], v[170:173], v[198:201], v[118:121]
	v_mfma_f32_16x16x32_bf16 v[110:113], v[156:159], v[206:209], v[110:113]
	v_mfma_f32_16x16x32_bf16 v[102:105], v[170:173], v[206:209], v[102:105]
	v_mfma_f32_16x16x32_bf16 v[94:97], v[156:159], v[214:217], v[94:97]
	v_mfma_f32_16x16x32_bf16 v[86:89], v[170:173], v[214:217], v[86:89]
	v_mfma_f32_16x16x32_bf16 v[78:81], v[156:159], v[222:225], v[78:81]
	v_mfma_f32_16x16x32_bf16 v[70:73], v[170:173], v[222:225], v[70:73]
	v_mfma_f32_16x16x32_bf16 v[122:125], v[174:177], v[194:197], v[122:125]
	v_mfma_f32_16x16x32_bf16 v[114:117], v[182:185], v[194:197], v[114:117]
	v_mfma_f32_16x16x32_bf16 v[106:109], v[174:177], v[202:205], v[106:109]
	v_mfma_f32_16x16x32_bf16 v[98:101], v[182:185], v[202:205], v[98:101]
	v_mfma_f32_16x16x32_bf16 v[90:93], v[174:177], v[210:213], v[90:93]
	v_mfma_f32_16x16x32_bf16 v[82:85], v[182:185], v[210:213], v[82:85]
	v_mfma_f32_16x16x32_bf16 v[74:77], v[174:177], v[218:221], v[74:77]
	v_mfma_f32_16x16x32_bf16 v[66:69], v[182:185], v[218:221], v[66:69]
	v_mfma_f32_16x16x32_bf16 v[122:125], v[178:181], v[198:201], v[122:125]
	v_mfma_f32_16x16x32_bf16 v[114:117], v[190:193], v[198:201], v[114:117]
	v_mfma_f32_16x16x32_bf16 v[106:109], v[178:181], v[206:209], v[106:109]
	v_mfma_f32_16x16x32_bf16 v[98:101], v[190:193], v[206:209], v[98:101]
	v_mfma_f32_16x16x32_bf16 v[90:93], v[178:181], v[214:217], v[90:93]
	v_mfma_f32_16x16x32_bf16 v[82:85], v[190:193], v[214:217], v[82:85]
	v_mfma_f32_16x16x32_bf16 v[74:77], v[178:181], v[222:225], v[74:77]
	v_mfma_f32_16x16x32_bf16 v[66:69], v[190:193], v[222:225], v[66:69]
	s_setprio 0
	s_barrier
; #define PG8_STAGE(bufoff, gbase, voff) do { _Pragma("unroll") for (int _i = 0; _i < 2; ++_i) \
;         __builtin_amdgcn_global_load_lds((const unsigned*)((const char*)(gbase) + (voff)[_i]), (PG8_LAS unsigned*)(lds + (bufoff) + ldsw + _i * 8192), 16, 0, 0); } while (0)
; #define PG8_LDA(dst, b, h) do { _Pragma("unroll") for (int m = 0; m < 4; ++m) _Pragma("unroll") for (int k = 0; k < 2; ++k) dst[m][k] = *(const PG8_LAS bf16x8*)(lds + PG8_SA(b, h) + aoff + m * 2048 + k * 1024); } while (0)
; #define PG8_LDB(dst, b, h) do { _Pragma("unroll") for (int n = 0; n < 2; ++n) _Pragma("unroll") for (int k = 0; k < 2; ++k) dst[n][k] = *(const PG8_LAS bf16x8*)(lds + PG8_SB(b, h) + boff + n * 2048 + k * 1024); } while (0)
; #define PG8_WAIT_V(n) asm volatile("s_waitcnt vmcnt(" #n ")" ::: "memory")
; #define PG8_WAIT_L(n) asm volatile("s_waitcnt lgkmcnt(" #n ")" ::: "memory")
; #define PG8_BAR __builtin_amdgcn_s_barrier()
; #define PG8_SCHED __builtin_amdgcn_sched_barrier(0)
; template <class Epi, class Sched, bool ALIGN_EPI = false, bool SP2 = false>
; __device__ __forceinline__ void gemm_phase(PG8_LAS unsigned char* lds, const Gemm g, const Sched& S, const Epi& E) {
;     ...
;             PG8_LDA(At, 1, 1); PG8_STAGE(PG8_SB(1, 0), b3, voffB); PG8_STAGE(PG8_SB(1, 1), b3 + hstep, voffB); PG8_STAGE(PG8_SA(1, 0), a3, voffA);
;             PG8_WAIT_V(8); PG8_WAIT_L(0); PG8_BAR; PG8_MMA(1, 0, At, B0); PG8_MMA(1, 1, At, B1); PG8_BAR; PG8_SCHED;
;             } else {
;             PG8_LDB(B0, 0, 0); PG8_SCHED; PG8_LDA(At, 0, 0); PG8_STAGE(PG8_SA(1, 1), a1 + hstep, voffA);
;             PG8_WAIT_L(8); PG8_BAR; PG8_WAIT_L(0); PG8_MMA(0, 0, At, B0); PG8_BAR; PG8_SCHED;
;             PG8_LDB(B1, 0, 1); PG8_STAGE(PG8_SB(0, 0), b2, voffB);
;             PG8_BAR; PG8_WAIT_L(0); PG8_MMA(0, 1, At, B1); PG8_BAR;
;             PG8_LDA(At, 0, 1); PG8_STAGE(PG8_SA(0, 0), a2, voffA);
;             PG8_BAR; PG8_WAIT_L(0); PG8_MMA(1, 0, At, B0); PG8_BAR; PG8_SCHED;
;             PG8_STAGE(PG8_SB(0, 1), b2 + hstep, voffB);
;             PG8_WAIT_V(6); PG8_BAR; PG8_MMA(1, 1, At, B1); PG8_BAR;
;             PG8_LDB(B0, 1, 0); PG8_SCHED; PG8_LDA(At, 1, 0); PG8_STAGE(PG8_SA(0, 1), a2 + hstep, voffA);
;             PG8_WAIT_L(8); PG8_BAR; PG8_WAIT_L(0); PG8_MMA(0, 0, At, B0); PG8_BAR; PG8_SCHED;
	s_add_i32 s30, s45, s2
	v_lshl_add_u64 v[160:161], v[160:161], 0, s[12:13]
	s_mov_b32 m0, s30
	ds_read_b128 v[194:197], v155 offset:49152
	ds_read_b128 v[198:201], v155 offset:50176
	ds_read_b128 v[202:205], v155 offset:51200
	ds_read_b128 v[206:209], v155 offset:52224
	ds_read_b128 v[210:213], v155 offset:53248
	ds_read_b128 v[214:217], v155 offset:54272
	ds_read_b128 v[218:221], v155 offset:55296
	ds_read_b128 v[222:225], v155 offset:56320
	global_load_lds_dwordx4 v[160:161], off
	s_add_i32 m0, s30, 0x2000
	s_add_u32 s28, s28, 0x80080
	v_lshl_add_u64 v[160:161], v[186:187], 0, s[12:13]
	s_addc_u32 s29, s29, 0
	s_add_i32 s30, s48, s2
	global_load_lds_dwordx4 v[160:161], off
	v_lshl_add_u64 v[160:161], s[28:29], 0, v[134:135]
	s_mov_b32 m0, s30
	s_nop 0
	global_load_lds_dwordx4 v[160:161], off
	v_lshl_add_u64 v[160:161], s[28:29], 0, v[130:131]
	s_add_i32 m0, s30, 0x2000
	s_nop 0
	global_load_lds_dwordx4 v[160:161], off
	v_lshl_add_u64 v[160:161], v[226:227], 0, s[12:13]
	s_mov_b32 m0, s35
	s_nop 0
	global_load_lds_dwordx4 v[160:161], off
	v_lshl_add_u64 v[160:161], v[228:229], 0, s[12:13]
	s_mov_b32 m0, s36
	s_nop 0
	global_load_lds_dwordx4 v[160:161], off
	s_waitcnt vmcnt(8)
	s_waitcnt lgkmcnt(0)
	s_barrier
	s_setprio 1
	s_waitcnt lgkmcnt(0)
	v_mfma_f32_16x16x32_bf16 v[62:65], v[146:149], v[194:197], v[62:65]
	v_mfma_f32_16x16x32_bf16 v[54:57], v[166:169], v[194:197], v[54:57]
	v_mfma_f32_16x16x32_bf16 v[46:49], v[146:149], v[202:205], v[46:49]
	v_mfma_f32_16x16x32_bf16 v[38:41], v[166:169], v[202:205], v[38:41]
	v_mfma_f32_16x16x32_bf16 v[30:33], v[146:149], v[210:213], v[30:33]
	v_mfma_f32_16x16x32_bf16 v[22:25], v[166:169], v[210:213], v[22:25]
	v_mfma_f32_16x16x32_bf16 v[14:17], v[146:149], v[218:221], v[14:17]
	v_mfma_f32_16x16x32_bf16 v[6:9], v[166:169], v[218:221], v[6:9]
	v_mfma_f32_16x16x32_bf16 v[62:65], v[156:159], v[198:201], v[62:65]
	v_mfma_f32_16x16x32_bf16 v[54:57], v[170:173], v[198:201], v[54:57]
	v_mfma_f32_16x16x32_bf16 v[46:49], v[156:159], v[206:209], v[46:49]
	v_mfma_f32_16x16x32_bf16 v[38:41], v[170:173], v[206:209], v[38:41]
	v_mfma_f32_16x16x32_bf16 v[30:33], v[156:159], v[214:217], v[30:33]
	v_mfma_f32_16x16x32_bf16 v[22:25], v[170:173], v[214:217], v[22:25]
	v_mfma_f32_16x16x32_bf16 v[14:17], v[156:159], v[222:225], v[14:17]
	v_mfma_f32_16x16x32_bf16 v[6:9], v[170:173], v[222:225], v[6:9]
	v_mfma_f32_16x16x32_bf16 v[58:61], v[174:177], v[194:197], v[58:61]
	v_mfma_f32_16x16x32_bf16 v[50:53], v[182:185], v[194:197], v[50:53]
	v_mfma_f32_16x16x32_bf16 v[42:45], v[174:177], v[202:205], v[42:45]
	v_mfma_f32_16x16x32_bf16 v[34:37], v[182:185], v[202:205], v[34:37]
	v_mfma_f32_16x16x32_bf16 v[26:29], v[174:177], v[210:213], v[26:29]
	v_mfma_f32_16x16x32_bf16 v[18:21], v[182:185], v[210:213], v[18:21]
	v_mfma_f32_16x16x32_bf16 v[10:13], v[174:177], v[218:221], v[10:13]
	v_mfma_f32_16x16x32_bf16 v[2:5], v[182:185], v[218:221], v[2:5]
	v_mfma_f32_16x16x32_bf16 v[58:61], v[178:181], v[198:201], v[58:61]
	v_mfma_f32_16x16x32_bf16 v[50:53], v[190:193], v[198:201], v[50:53]
	v_mfma_f32_16x16x32_bf16 v[42:45], v[178:181], v[206:209], v[42:45]
	v_mfma_f32_16x16x32_bf16 v[34:37], v[190:193], v[206:209], v[34:37]
	v_mfma_f32_16x16x32_bf16 v[26:29], v[178:181], v[214:217], v[26:29]
	v_mfma_f32_16x16x32_bf16 v[18:21], v[190:193], v[214:217], v[18:21]
	v_mfma_f32_16x16x32_bf16 v[10:13], v[178:181], v[222:225], v[10:13]
	v_mfma_f32_16x16x32_bf16 v[2:5], v[190:193], v[222:225], v[2:5]
	s_setprio 0
	s_barrier
	s_add_i32 s44, s44, 2
	s_add_u32 s26, s26, 0x100
	s_addc_u32 s27, s27, 0
	s_add_u32 s42, s42, 0x100
	s_addc_u32 s43, s43, 0
	s_cmp_gt_u32 s44, 29
	s_cbranch_scc0 .LBB0_1086
	s_and_b64 vcc, exec, s[14:15]
	s_cbranch_vccz .LBB0_1089
	s_barrier

; #define PG8_STAGE(bufoff, gbase, voff) do { _Pragma("unroll") for (int _i = 0; _i < 2; ++_i) \
;         __builtin_amdgcn_global_load_lds((const unsigned*)((const char*)(gbase) + (voff)[_i]), (PG8_LAS unsigned*)(lds + (bufoff) + ldsw + _i * 8192), 16, 0, 0); } while (0)
; #define PG8_LDA(dst, b, h) do { _Pragma("unroll") for (int m = 0; m < 4; ++m) _Pragma("unroll") for (int k = 0; k < 2; ++k) dst[m][k] = *(const PG8_LAS bf16x8*)(lds + PG8_SA(b, h) + aoff + m * 2048 + k * 1024); } while (0)
; #define PG8_LDB(dst, b, h) do { _Pragma("unroll") for (int n = 0; n < 2; ++n) _Pragma("unroll") for (int k = 0; k < 2; ++k) dst[n][k] = *(const PG8_LAS bf16x8*)(lds + PG8_SB(b, h) + boff + n * 2048 + k * 1024); } while (0)
; #define PG8_WAIT_V(n) asm volatile("s_waitcnt vmcnt(" #n ")" ::: "memory")
; #define PG8_WAIT_L(n) asm volatile("s_waitcnt lgkmcnt(" #n ")" ::: "memory")
; #define PG8_BAR __builtin_amdgcn_s_barrier()
; #define PG8_SCHED __builtin_amdgcn_sched_barrier(0)
; template <class Epi, class Sched, bool ALIGN_EPI = false, bool SP2 = false>
; __device__ __forceinline__ void gemm_phase(PG8_LAS unsigned char* lds, const Gemm g, const Sched& S, const Epi& E) {
;     ...
;         const char* nA = has_next ? (const char*)g.A + (size_t)nxt.pm * tstep + (size_t)nxt.k0 * 2 : cA; const char* nB = has_next ? (const char*)g.Bt + (size_t)nxt.pn * tstep + (size_t)nxt.k0 * 2 : cB;
;         for (int t = 0; t < nt; t += 2) {
;             const bool last = (t == nt - 2);
;             const char* a1 = cA + (size_t)(t + 1) * kstep;
;             const char* a2 = last ? nA : cA + (size_t)(t + 2) * kstep; const char* b2 = last ? nB : cB + (size_t)(t + 2) * kstep;
;             const char* a3 = a2 + kstep; const char* b3 = b2 + kstep;
;             if (last && has_next) S.a_ready(nxt);
;             if constexpr (SP2) {
;             PG8_LDB(B0, 0, 0); PG8_LDB(B1, 0, 1); PG8_SCHED; PG8_LDA(At, 0, 0); PG8_STAGE(PG8_SA(1, 1), a1 + hstep, voffA);
;             PG8_WAIT_V(8); PG8_WAIT_L(0); PG8_BAR; PG8_MMA(0, 0, At, B0); PG8_MMA(0, 1, At, B1); PG8_BAR; PG8_SCHED;
;             PG8_LDA(At, 0, 1); PG8_STAGE(PG8_SB(0, 0), b2, voffB); PG8_STAGE(PG8_SB(0, 1), b2 + hstep, voffB); PG8_STAGE(PG8_SA(0, 0), a2, voffA);
;             PG8_WAIT_V(8); PG8_WAIT_L(0); PG8_BAR; PG8_MMA(1, 0, At, B0); PG8_MMA(1, 1, At, B1); PG8_BAR; PG8_SCHED;
.LBB0_1165:
	ds_read_b128 v[144:147], v155
	ds_read_b128 v[148:151], v155 offset:1024
	ds_read_b128 v[166:169], v155 offset:2048
	ds_read_b128 v[170:173], v155 offset:3072
	ds_read_b128 v[174:177], v156
	ds_read_b128 v[178:181], v156 offset:1024
	ds_read_b128 v[182:185], v156 offset:2048
	ds_read_b128 v[190:193], v156 offset:3072
	s_add_u32 s6, s26, 0x100
	s_addc_u32 s7, s27, 0
	s_cmpk_eq_i32 s48, 0x54
	s_cselect_b32 s31, s23, s7
	s_cselect_b32 s30, s22, s6
	s_cselect_b32 s29, s25, s45
	s_cselect_b32 s28, s24, s44
	v_lshl_add_u64 v[160:161], s[26:27], 0, v[136:137]
	s_add_i32 m0, s3, 0xc000
	ds_read_b128 v[194:197], v157
	ds_read_b128 v[198:201], v157 offset:1024
	ds_read_b128 v[202:205], v157 offset:2048
	ds_read_b128 v[206:209], v157 offset:3072
	ds_read_b128 v[210:213], v157 offset:4096
	ds_read_b128 v[214:217], v157 offset:5120
	ds_read_b128 v[218:221], v157 offset:6144
	ds_read_b128 v[222:225], v157 offset:7168
	global_load_lds_dwordx4 v[160:161], off
	v_lshl_add_u64 v[160:161], s[26:27], 0, v[138:139]
	s_add_i32 m0, s3, 0xe000
	s_nop 0
	global_load_lds_dwordx4 v[160:161], off
	s_waitcnt vmcnt(8)
	s_waitcnt lgkmcnt(0)
	s_barrier
	s_setprio 1
	s_waitcnt lgkmcnt(0)
	v_mfma_f32_16x16x32_bf16 v[126:129], v[144:147], v[194:197], v[126:129]
	v_mfma_f32_16x16x32_bf16 v[122:125], v[166:169], v[194:197], v[122:125]
	v_mfma_f32_16x16x32_bf16 v[110:113], v[144:147], v[202:205], v[110:113]
	v_mfma_f32_16x16x32_bf16 v[106:109], v[166:169], v[202:205], v[106:109]
	v_mfma_f32_16x16x32_bf16 v[94:97], v[144:147], v[210:213], v[94:97]
	v_mfma_f32_16x16x32_bf16 v[90:93], v[166:169], v[210:213], v[90:93]
	v_mfma_f32_16x16x32_bf16 v[78:81], v[144:147], v[218:221], v[78:81]
	v_mfma_f32_16x16x32_bf16 v[74:77], v[166:169], v[218:221], v[74:77]
	v_mfma_f32_16x16x32_bf16 v[126:129], v[148:151], v[198:201], v[126:129]
	v_mfma_f32_16x16x32_bf16 v[122:125], v[170:173], v[198:201], v[122:125]
	v_mfma_f32_16x16x32_bf16 v[110:113], v[148:151], v[206:209], v[110:113]
	v_mfma_f32_16x16x32_bf16 v[106:109], v[170:173], v[206:209], v[106:109]
	v_mfma_f32_16x16x32_bf16 v[94:97], v[148:151], v[214:217], v[94:97]
	v_mfma_f32_16x16x32_bf16 v[90:93], v[170:173], v[214:217], v[90:93]
	v_mfma_f32_16x16x32_bf16 v[78:81], v[148:151], v[222:225], v[78:81]
	v_mfma_f32_16x16x32_bf16 v[74:77], v[170:173], v[222:225], v[74:77]
	v_mfma_f32_16x16x32_bf16 v[118:121], v[174:177], v[194:197], v[118:121]
	v_mfma_f32_16x16x32_bf16 v[114:117], v[182:185], v[194:197], v[114:117]
	v_mfma_f32_16x16x32_bf16 v[102:105], v[174:177], v[202:205], v[102:105]
	v_mfma_f32_16x16x32_bf16 v[98:101], v[182:185], v[202:205], v[98:101]
	v_mfma_f32_16x16x32_bf16 v[86:89], v[174:177], v[210:213], v[86:89]
	v_mfma_f32_16x16x32_bf16 v[82:85], v[182:185], v[210:213], v[82:85]
	v_mfma_f32_16x16x32_bf16 v[70:73], v[174:177], v[218:221], v[70:73]
	v_mfma_f32_16x16x32_bf16 v[66:69], v[182:185], v[218:221], v[66:69]
	v_mfma_f32_16x16x32_bf16 v[118:121], v[178:181], v[198:201], v[118:121]
	v_mfma_f32_16x16x32_bf16 v[114:117], v[190:193], v[198:201], v[114:117]
	v_mfma_f32_16x16x32_bf16 v[102:105], v[178:181], v[206:209], v[102:105]
	v_mfma_f32_16x16x32_bf16 v[98:101], v[190:193], v[206:209], v[98:101]
	v_mfma_f32_16x16x32_bf16 v[86:89], v[178:181], v[214:217], v[86:89]
	v_mfma_f32_16x16x32_bf16 v[82:85], v[190:193], v[214:217], v[82:85]
	v_mfma_f32_16x16x32_bf16 v[70:73], v[178:181], v[222:225], v[70:73]
	v_mfma_f32_16x16x32_bf16 v[66:69], v[190:193], v[222:225], v[66:69]
	s_setprio 0
	s_barrier
	s_add_i32 s26, s37, s2
	v_lshl_add_u64 v[160:161], s[28:29], 0, v[130:131]
	s_mov_b32 m0, s26
	ds_read_b128 v[194:197], v157 offset:16384
	ds_read_b128 v[198:201], v157 offset:17408
	ds_read_b128 v[202:205], v157 offset:18432
	ds_read_b128 v[206:209], v157 offset:19456
	ds_read_b128 v[210:213], v157 offset:20480
	ds_read_b128 v[214:217], v157 offset:21504
	ds_read_b128 v[218:221], v157 offset:22528
	ds_read_b128 v[222:225], v157 offset:23552
	global_load_lds_dwordx4 v[160:161], off
	s_add_i32 m0, s26, 0x2000
	s_add_u32 s26, s28, 0x160000
	v_lshl_add_u64 v[186:187], s[28:29], 0, v[132:133]
	s_addc_u32 s27, s29, 0
	s_add_i32 s49, s38, s2
	global_load_lds_dwordx4 v[186:187], off
	v_lshl_add_u64 v[226:227], s[26:27], 0, v[130:131]
	s_mov_b32 m0, s49
	v_lshl_add_u64 v[228:229], s[30:31], 0, v[132:133]
	global_load_lds_dwordx4 v[226:227], off
	v_lshl_add_u64 v[226:227], s[26:27], 0, v[132:133]
	s_add_i32 m0, s49, 0x2000
	s_nop 0
	global_load_lds_dwordx4 v[226:227], off
	v_lshl_add_u64 v[226:227], s[30:31], 0, v[130:131]
	s_mov_b32 m0, s3
	s_nop 0
	global_load_lds_dwordx4 v[226:227], off
	s_mov_b32 m0, s4
	s_nop 0
	global_load_lds_dwordx4 v[228:229], off
	s_waitcnt vmcnt(8)
	s_waitcnt lgkmcnt(0)
	s_barrier
; #define PG8_STAGE(bufoff, gbase, voff) do { _Pragma("unroll") for (int _i = 0; _i < 2; ++_i) \
;         __builtin_amdgcn_global_load_lds((const unsigned*)((const char*)(gbase) + (voff)[_i]), (PG8_LAS unsigned*)(lds + (bufoff) + ldsw + _i * 8192), 16, 0, 0); } while (0)
; #define PG8_LDA(dst, b, h) do { _Pragma("unroll") for (int m = 0; m < 4; ++m) _Pragma("unroll") for (int k = 0; k < 2; ++k) dst[m][k] = *(const PG8_LAS bf16x8*)(lds + PG8_SA(b, h) + aoff + m * 2048 + k * 1024); } while (0)
; #define PG8_LDB(dst, b, h) do { _Pragma("unroll") for (int n = 0; n < 2; ++n) _Pragma("unroll") for (int k = 0; k < 2; ++k) dst[n][k] = *(const PG8_LAS bf16x8*)(lds + PG8_SB(b, h) + boff + n * 2048 + k * 1024); } while (0)
; #define PG8_MMA(ai, bj, At, Bt) do { __builtin_amdgcn_s_setprio(1); _Pragma("unroll") for (int m = 0; m < 4; ++m) _Pragma("unroll") for (int n = 0; n < 2; ++n) _Pragma("unroll") for (int k = 0; k < 2; ++k) \
;         acc[ai][bj][m][n] = __builtin_amdgcn_mfma_f32_16x16x32_bf16(Bt[n][k], At[m][k], acc[ai][bj][m][n], 0, 0, 0); __builtin_amdgcn_s_setprio(0); } while (0)
; #define PG8_WAIT_V(n) asm volatile("s_waitcnt vmcnt(" #n ")" ::: "memory")
; #define PG8_WAIT_L(n) asm volatile("s_waitcnt lgkmcnt(" #n ")" ::: "memory")
; #define PG8_BAR __builtin_amdgcn_s_barrier()
; #define PG8_SCHED __builtin_amdgcn_sched_barrier(0)
; template <class Epi, class Sched, bool ALIGN_EPI = false, bool SP2 = false>
; __device__ __forceinline__ void gemm_phase(PG8_LAS unsigned char* lds, const Gemm g, const Sched& S, const Epi& E) {
;     ...
;             PG8_WAIT_V(8); PG8_WAIT_L(0); PG8_BAR; PG8_MMA(0, 0, At, B0); PG8_MMA(0, 1, At, B1); PG8_BAR; PG8_SCHED;
;             PG8_LDA(At, 0, 1); PG8_STAGE(PG8_SB(0, 0), b2, voffB); PG8_STAGE(PG8_SB(0, 1), b2 + hstep, voffB); PG8_STAGE(PG8_SA(0, 0), a2, voffA);
;             PG8_WAIT_V(8); PG8_WAIT_L(0); PG8_BAR; PG8_MMA(1, 0, At, B0); PG8_MMA(1, 1, At, B1); PG8_BAR; PG8_SCHED;
;             PG8_LDB(B0, 1, 0); PG8_LDB(B1, 1, 1); PG8_SCHED; PG8_LDA(At, 1, 0); PG8_STAGE(PG8_SA(0, 1), a2 + hstep, voffA);
;             PG8_WAIT_V(8); PG8_WAIT_L(0); PG8_BAR; PG8_MMA(0, 0, At, B0); PG8_MMA(0, 1, At, B1); PG8_BAR; PG8_SCHED;
	s_setprio 1
	s_waitcnt lgkmcnt(0)
	v_mfma_f32_16x16x32_bf16 v[62:65], v[144:147], v[194:197], v[62:65]
	v_mfma_f32_16x16x32_bf16 v[58:61], v[166:169], v[194:197], v[58:61]
	v_mfma_f32_16x16x32_bf16 v[46:49], v[144:147], v[202:205], v[46:49]
	v_mfma_f32_16x16x32_bf16 v[42:45], v[166:169], v[202:205], v[42:45]
	v_mfma_f32_16x16x32_bf16 v[30:33], v[144:147], v[210:213], v[30:33]
	v_mfma_f32_16x16x32_bf16 v[26:29], v[166:169], v[210:213], v[26:29]
	v_mfma_f32_16x16x32_bf16 v[14:17], v[144:147], v[218:221], v[14:17]
	v_mfma_f32_16x16x32_bf16 v[10:13], v[166:169], v[218:221], v[10:13]
	v_mfma_f32_16x16x32_bf16 v[62:65], v[148:151], v[198:201], v[62:65]
	v_mfma_f32_16x16x32_bf16 v[58:61], v[170:173], v[198:201], v[58:61]
	v_mfma_f32_16x16x32_bf16 v[46:49], v[148:151], v[206:209], v[46:49]
	v_mfma_f32_16x16x32_bf16 v[42:45], v[170:173], v[206:209], v[42:45]
	v_mfma_f32_16x16x32_bf16 v[30:33], v[148:151], v[214:217], v[30:33]
	v_mfma_f32_16x16x32_bf16 v[26:29], v[170:173], v[214:217], v[26:29]
	v_mfma_f32_16x16x32_bf16 v[14:17], v[148:151], v[222:225], v[14:17]
	v_mfma_f32_16x16x32_bf16 v[10:13], v[170:173], v[222:225], v[10:13]
	v_mfma_f32_16x16x32_bf16 v[54:57], v[174:177], v[194:197], v[54:57]
	v_mfma_f32_16x16x32_bf16 v[50:53], v[182:185], v[194:197], v[50:53]
	v_mfma_f32_16x16x32_bf16 v[38:41], v[174:177], v[202:205], v[38:41]
	v_mfma_f32_16x16x32_bf16 v[34:37], v[182:185], v[202:205], v[34:37]
	v_mfma_f32_16x16x32_bf16 v[22:25], v[174:177], v[210:213], v[22:25]
	v_mfma_f32_16x16x32_bf16 v[18:21], v[182:185], v[210:213], v[18:21]
	v_mfma_f32_16x16x32_bf16 v[6:9], v[174:177], v[218:221], v[6:9]
	v_mfma_f32_16x16x32_bf16 v[2:5], v[182:185], v[218:221], v[2:5]
	v_mfma_f32_16x16x32_bf16 v[54:57], v[178:181], v[198:201], v[54:57]
	v_mfma_f32_16x16x32_bf16 v[50:53], v[190:193], v[198:201], v[50:53]
	v_mfma_f32_16x16x32_bf16 v[38:41], v[178:181], v[206:209], v[38:41]
	v_mfma_f32_16x16x32_bf16 v[34:37], v[190:193], v[206:209], v[34:37]
	v_mfma_f32_16x16x32_bf16 v[22:25], v[178:181], v[214:217], v[22:25]
	v_mfma_f32_16x16x32_bf16 v[18:21], v[190:193], v[214:217], v[18:21]
	v_mfma_f32_16x16x32_bf16 v[6:9], v[178:181], v[222:225], v[6:9]
	v_mfma_f32_16x16x32_bf16 v[2:5], v[190:193], v[222:225], v[2:5]
	s_setprio 0
	s_barrier
	s_add_i32 s49, 0, 0x18000
	v_add_u32_e32 v134, s49, v153
	s_add_i32 s50, 0, 0x1c000
	ds_read_b128 v[144:147], v134
	ds_read_b128 v[148:151], v134 offset:1024
	ds_read_b128 v[166:169], v134 offset:2048
	ds_read_b128 v[170:173], v134 offset:3072
	v_add_u32_e32 v134, s50, v153
	ds_read_b128 v[174:177], v134
	ds_read_b128 v[178:181], v134 offset:1024
	ds_read_b128 v[182:185], v134 offset:2048
	ds_read_b128 v[190:193], v134 offset:3072
	s_add_u32 s26, s30, 0x160000
	s_addc_u32 s27, s31, 0
	s_mov_b32 m0, s5
	v_lshl_add_u64 v[230:231], s[26:27], 0, v[130:131]
	ds_read_b128 v[194:197], v157 offset:32768
	ds_read_b128 v[198:201], v157 offset:33792
	ds_read_b128 v[202:205], v157 offset:34816
	ds_read_b128 v[206:209], v157 offset:35840
	ds_read_b128 v[210:213], v157 offset:36864
	ds_read_b128 v[214:217], v157 offset:37888
	ds_read_b128 v[218:221], v157 offset:38912
	ds_read_b128 v[222:225], v157 offset:39936
	global_load_lds_dwordx4 v[230:231], off
	v_lshl_add_u64 v[230:231], s[26:27], 0, v[132:133]
	s_mov_b32 m0, s11
	s_nop 0
	global_load_lds_dwordx4 v[230:231], off
	s_waitcnt vmcnt(8)
	s_waitcnt lgkmcnt(0)
	s_barrier
	s_setprio 1
	s_waitcnt lgkmcnt(0)
	v_mfma_f32_16x16x32_bf16 v[126:129], v[144:147], v[194:197], v[126:129]
	v_mfma_f32_16x16x32_bf16 v[122:125], v[166:169], v[194:197], v[122:125]
	v_mfma_f32_16x16x32_bf16 v[110:113], v[144:147], v[202:205], v[110:113]
	v_mfma_f32_16x16x32_bf16 v[106:109], v[166:169], v[202:205], v[106:109]
	v_mfma_f32_16x16x32_bf16 v[94:97], v[144:147], v[210:213], v[94:97]
	v_mfma_f32_16x16x32_bf16 v[90:93], v[166:169], v[210:213], v[90:93]
	v_mfma_f32_16x16x32_bf16 v[78:81], v[144:147], v[218:221], v[78:81]
	v_mfma_f32_16x16x32_bf16 v[74:77], v[166:169], v[218:221], v[74:77]
	v_mfma_f32_16x16x32_bf16 v[126:129], v[148:151], v[198:201], v[126:129]
	v_mfma_f32_16x16x32_bf16 v[122:125], v[170:173], v[198:201], v[122:125]
	v_mfma_f32_16x16x32_bf16 v[110:113], v[148:151], v[206:209], v[110:113]
	v_mfma_f32_16x16x32_bf16 v[106:109], v[170:173], v[206:209], v[106:109]
	v_mfma_f32_16x16x32_bf16 v[94:97], v[148:151], v[214:217], v[94:97]
	v_mfma_f32_16x16x32_bf16 v[90:93], v[170:173], v[214:217], v[90:93]
	v_mfma_f32_16x16x32_bf16 v[78:81], v[148:151], v[222:225], v[78:81]
	v_mfma_f32_16x16x32_bf16 v[74:77], v[170:173], v[222:225], v[74:77]
	v_mfma_f32_16x16x32_bf16 v[118:121], v[174:177], v[194:197], v[118:121]
	v_mfma_f32_16x16x32_bf16 v[114:117], v[182:185], v[194:197], v[114:117]
	v_mfma_f32_16x16x32_bf16 v[102:105], v[174:177], v[202:205], v[102:105]
	v_mfma_f32_16x16x32_bf16 v[98:101], v[182:185], v[202:205], v[98:101]
	v_mfma_f32_16x16x32_bf16 v[86:89], v[174:177], v[210:213], v[86:89]
	v_mfma_f32_16x16x32_bf16 v[82:85], v[182:185], v[210:213], v[82:85]
	v_mfma_f32_16x16x32_bf16 v[70:73], v[174:177], v[218:221], v[70:73]
	v_mfma_f32_16x16x32_bf16 v[66:69], v[182:185], v[218:221], v[66:69]
	v_mfma_f32_16x16x32_bf16 v[118:121], v[178:181], v[198:201], v[118:121]
	v_mfma_f32_16x16x32_bf16 v[114:117], v[190:193], v[198:201], v[114:117]
	v_mfma_f32_16x16x32_bf16 v[102:105], v[178:181], v[206:209], v[102:105]
	v_mfma_f32_16x16x32_bf16 v[98:101], v[190:193], v[206:209], v[98:101]
	v_mfma_f32_16x16x32_bf16 v[86:89], v[178:181], v[214:217], v[86:89]
	v_mfma_f32_16x16x32_bf16 v[82:85], v[190:193], v[214:217], v[82:85]
	v_mfma_f32_16x16x32_bf16 v[70:73], v[178:181], v[222:225], v[70:73]
	v_mfma_f32_16x16x32_bf16 v[66:69], v[190:193], v[222:225], v[66:69]
	s_setprio 0
	s_barrier
; #define PG8_STAGE(bufoff, gbase, voff) do { _Pragma("unroll") for (int _i = 0; _i < 2; ++_i) \
;         __builtin_amdgcn_global_load_lds((const unsigned*)((const char*)(gbase) + (voff)[_i]), (PG8_LAS unsigned*)(lds + (bufoff) + ldsw + _i * 8192), 16, 0, 0); } while (0)
; #define PG8_LDA(dst, b, h) do { _Pragma("unroll") for (int m = 0; m < 4; ++m) _Pragma("unroll") for (int k = 0; k < 2; ++k) dst[m][k] = *(const PG8_LAS bf16x8*)(lds + PG8_SA(b, h) + aoff + m * 2048 + k * 1024); } while (0)
; #define PG8_LDB(dst, b, h) do { _Pragma("unroll") for (int n = 0; n < 2; ++n) _Pragma("unroll") for (int k = 0; k < 2; ++k) dst[n][k] = *(const PG8_LAS bf16x8*)(lds + PG8_SB(b, h) + boff + n * 2048 + k * 1024); } while (0)
; #define PG8_WAIT_V(n) asm volatile("s_waitcnt vmcnt(" #n ")" ::: "memory")
; #define PG8_WAIT_L(n) asm volatile("s_waitcnt lgkmcnt(" #n ")" ::: "memory")
; #define PG8_BAR __builtin_amdgcn_s_barrier()
; #define PG8_SCHED __builtin_amdgcn_sched_barrier(0)
; template <class Epi, class Sched, bool ALIGN_EPI = false, bool SP2 = false>
; __device__ __forceinline__ void gemm_phase(PG8_LAS unsigned char* lds, const Gemm g, const Sched& S, const Epi& E) {
;     ...
;             PG8_LDA(At, 1, 1); PG8_STAGE(PG8_SB(1, 0), b3, voffB); PG8_STAGE(PG8_SB(1, 1), b3 + hstep, voffB); PG8_STAGE(PG8_SA(1, 0), a3, voffA);
;             PG8_WAIT_V(8); PG8_WAIT_L(0); PG8_BAR; PG8_MMA(1, 0, At, B0); PG8_MMA(1, 1, At, B1); PG8_BAR; PG8_SCHED;
;             } else {
;             PG8_LDB(B0, 0, 0); PG8_SCHED; PG8_LDA(At, 0, 0); PG8_STAGE(PG8_SA(1, 1), a1 + hstep, voffA);
;             PG8_WAIT_L(8); PG8_BAR; PG8_WAIT_L(0); PG8_MMA(0, 0, At, B0); PG8_BAR; PG8_SCHED;
;             PG8_LDB(B1, 0, 1); PG8_STAGE(PG8_SB(0, 0), b2, voffB);
;             PG8_BAR; PG8_WAIT_L(0); PG8_MMA(0, 1, At, B1); PG8_BAR;
;             PG8_LDA(At, 0, 1); PG8_STAGE(PG8_SA(0, 0), a2, voffA);
;             PG8_BAR; PG8_WAIT_L(0); PG8_MMA(1, 0, At, B0); PG8_BAR; PG8_SCHED;
;             PG8_STAGE(PG8_SB(0, 1), b2 + hstep, voffB);
;             PG8_WAIT_V(6); PG8_BAR; PG8_MMA(1, 1, At, B1); PG8_BAR;
;             PG8_LDB(B0, 1, 0); PG8_SCHED; PG8_LDA(At, 1, 0); PG8_STAGE(PG8_SA(0, 1), a2 + hstep, voffA);
;             PG8_WAIT_L(8); PG8_BAR; PG8_WAIT_L(0); PG8_MMA(0, 0, At, B0); PG8_BAR; PG8_SCHED;
	s_add_i32 s26, s49, s2
	v_lshl_add_u64 v[160:161], v[160:161], 0, s[18:19]
	s_mov_b32 m0, s26
	ds_read_b128 v[194:197], v157 offset:49152
	ds_read_b128 v[198:201], v157 offset:50176
	ds_read_b128 v[202:205], v157 offset:51200
	ds_read_b128 v[206:209], v157 offset:52224
	ds_read_b128 v[210:213], v157 offset:53248
	ds_read_b128 v[214:217], v157 offset:54272
	ds_read_b128 v[218:221], v157 offset:55296
	ds_read_b128 v[222:225], v157 offset:56320
	global_load_lds_dwordx4 v[160:161], off
	s_add_i32 m0, s26, 0x2000
	s_add_u32 s26, s28, 0x160080
	v_lshl_add_u64 v[160:161], v[186:187], 0, s[18:19]
	s_addc_u32 s27, s29, 0
	s_add_i32 s28, s50, s2
	global_load_lds_dwordx4 v[160:161], off
	v_lshl_add_u64 v[160:161], s[26:27], 0, v[130:131]
	s_mov_b32 m0, s28
	s_nop 0
	global_load_lds_dwordx4 v[160:161], off
	v_lshl_add_u64 v[160:161], s[26:27], 0, v[132:133]
	s_add_i32 m0, s28, 0x2000
	s_nop 0
	global_load_lds_dwordx4 v[160:161], off
	v_lshl_add_u64 v[160:161], v[226:227], 0, s[18:19]
	s_mov_b32 m0, s35
	s_nop 0
	global_load_lds_dwordx4 v[160:161], off
	v_lshl_add_u64 v[160:161], v[228:229], 0, s[18:19]
	s_mov_b32 m0, s36
	s_nop 0
	global_load_lds_dwordx4 v[160:161], off
	s_waitcnt vmcnt(8)
	s_waitcnt lgkmcnt(0)
	s_barrier
	s_setprio 1
	s_waitcnt lgkmcnt(0)
	v_mfma_f32_16x16x32_bf16 v[62:65], v[144:147], v[194:197], v[62:65]
	v_mfma_f32_16x16x32_bf16 v[58:61], v[166:169], v[194:197], v[58:61]
	v_mfma_f32_16x16x32_bf16 v[46:49], v[144:147], v[202:205], v[46:49]
	v_mfma_f32_16x16x32_bf16 v[42:45], v[166:169], v[202:205], v[42:45]
	v_mfma_f32_16x16x32_bf16 v[30:33], v[144:147], v[210:213], v[30:33]
	v_mfma_f32_16x16x32_bf16 v[26:29], v[166:169], v[210:213], v[26:29]
	v_mfma_f32_16x16x32_bf16 v[14:17], v[144:147], v[218:221], v[14:17]
	v_mfma_f32_16x16x32_bf16 v[10:13], v[166:169], v[218:221], v[10:13]
	v_mfma_f32_16x16x32_bf16 v[62:65], v[148:151], v[198:201], v[62:65]
	v_mfma_f32_16x16x32_bf16 v[58:61], v[170:173], v[198:201], v[58:61]
	v_mfma_f32_16x16x32_bf16 v[46:49], v[148:151], v[206:209], v[46:49]
	v_mfma_f32_16x16x32_bf16 v[42:45], v[170:173], v[206:209], v[42:45]
	v_mfma_f32_16x16x32_bf16 v[30:33], v[148:151], v[214:217], v[30:33]
	v_mfma_f32_16x16x32_bf16 v[26:29], v[170:173], v[214:217], v[26:29]
	v_mfma_f32_16x16x32_bf16 v[14:17], v[148:151], v[222:225], v[14:17]
	v_mfma_f32_16x16x32_bf16 v[10:13], v[170:173], v[222:225], v[10:13]
	v_mfma_f32_16x16x32_bf16 v[54:57], v[174:177], v[194:197], v[54:57]
	v_mfma_f32_16x16x32_bf16 v[50:53], v[182:185], v[194:197], v[50:53]
	v_mfma_f32_16x16x32_bf16 v[38:41], v[174:177], v[202:205], v[38:41]
	v_mfma_f32_16x16x32_bf16 v[34:37], v[182:185], v[202:205], v[34:37]
	v_mfma_f32_16x16x32_bf16 v[22:25], v[174:177], v[210:213], v[22:25]
	v_mfma_f32_16x16x32_bf16 v[18:21], v[182:185], v[210:213], v[18:21]
	v_mfma_f32_16x16x32_bf16 v[6:9], v[174:177], v[218:221], v[6:9]
	v_mfma_f32_16x16x32_bf16 v[2:5], v[182:185], v[218:221], v[2:5]
	v_mfma_f32_16x16x32_bf16 v[54:57], v[178:181], v[198:201], v[54:57]
	v_mfma_f32_16x16x32_bf16 v[50:53], v[190:193], v[198:201], v[50:53]
	v_mfma_f32_16x16x32_bf16 v[38:41], v[178:181], v[206:209], v[38:41]
	v_mfma_f32_16x16x32_bf16 v[34:37], v[190:193], v[206:209], v[34:37]
	v_mfma_f32_16x16x32_bf16 v[22:25], v[178:181], v[214:217], v[22:25]
	v_mfma_f32_16x16x32_bf16 v[18:21], v[190:193], v[214:217], v[18:21]
	v_mfma_f32_16x16x32_bf16 v[6:9], v[178:181], v[222:225], v[6:9]
	v_mfma_f32_16x16x32_bf16 v[2:5], v[190:193], v[222:225], v[2:5]
	s_setprio 0
	s_barrier
	s_add_i32 s48, s48, 2
	s_add_u32 s44, s44, 0x100
	s_addc_u32 s45, s45, 0
	s_cmpk_gt_u32 s48, 0x55
	s_mov_b64 s[26:27], s[6:7]
	s_cbranch_scc0 .LBB0_1165
	s_and_b64 vcc, exec, s[20:21]
	s_cbranch_vccz .LBB0_1168
	s_barrier

; #define PG8_STAGE(bufoff, gbase, voff) do { _Pragma("unroll") for (int _i = 0; _i < 2; ++_i) \
;         __builtin_amdgcn_global_load_lds((const unsigned*)((const char*)(gbase) + (voff)[_i]), (PG8_LAS unsigned*)(lds + (bufoff) + ldsw + _i * 8192), 16, 0, 0); } while (0)
; #define PG8_LDA(dst, b, h) do { _Pragma("unroll") for (int m = 0; m < 4; ++m) _Pragma("unroll") for (int k = 0; k < 2; ++k) dst[m][k] = *(const PG8_LAS bf16x8*)(lds + PG8_SA(b, h) + aoff + m * 2048 + k * 1024); } while (0)
; #define PG8_LDB(dst, b, h) do { _Pragma("unroll") for (int n = 0; n < 2; ++n) _Pragma("unroll") for (int k = 0; k < 2; ++k) dst[n][k] = *(const PG8_LAS bf16x8*)(lds + PG8_SB(b, h) + boff + n * 2048 + k * 1024); } while (0)
; #define PG8_WAIT_V(n) asm volatile("s_waitcnt vmcnt(" #n ")" ::: "memory")
; #define PG8_WAIT_L(n) asm volatile("s_waitcnt lgkmcnt(" #n ")" ::: "memory")
; #define PG8_BAR __builtin_amdgcn_s_barrier()
; #define PG8_SCHED __builtin_amdgcn_sched_barrier(0)
; template <class Epi, class Sched, bool ALIGN_EPI = false, bool SP2 = false>
; __device__ __forceinline__ void gemm_phase(PG8_LAS unsigned char* lds, const Gemm g, const Sched& S, const Epi& E) {
;     ...
;         const char* nA = has_next ? (const char*)g.A + (size_t)nxt.pm * tstep + (size_t)nxt.k0 * 2 : cA; const char* nB = has_next ? (const char*)g.Bt + (size_t)nxt.pn * tstep + (size_t)nxt.k0 * 2 : cB;
;         for (int t = 0; t < nt; t += 2) {
;             const bool last = (t == nt - 2);
;             const char* a1 = cA + (size_t)(t + 1) * kstep;
;             const char* a2 = last ? nA : cA + (size_t)(t + 2) * kstep; const char* b2 = last ? nB : cB + (size_t)(t + 2) * kstep;
;             const char* a3 = a2 + kstep; const char* b3 = b2 + kstep;
;             if (last && has_next) S.a_ready(nxt);
;             if constexpr (SP2) {
;             PG8_LDB(B0, 0, 0); PG8_LDB(B1, 0, 1); PG8_SCHED; PG8_LDA(At, 0, 0); PG8_STAGE(PG8_SA(1, 1), a1 + hstep, voffA);
;             PG8_WAIT_V(8); PG8_WAIT_L(0); PG8_BAR; PG8_MMA(0, 0, At, B0); PG8_MMA(0, 1, At, B1); PG8_BAR; PG8_SCHED;
;             PG8_LDA(At, 0, 1); PG8_STAGE(PG8_SB(0, 0), b2, voffB); PG8_STAGE(PG8_SB(0, 1), b2 + hstep, voffB); PG8_STAGE(PG8_SA(0, 0), a2, voffA);
;             PG8_WAIT_V(8); PG8_WAIT_L(0); PG8_BAR; PG8_MMA(1, 0, At, B0); PG8_MMA(1, 1, At, B1); PG8_BAR; PG8_SCHED;
.LBB0_1217:
	ds_read_b128 v[148:151], v145
	ds_read_b128 v[152:155], v145 offset:1024
	ds_read_b128 v[156:159], v145 offset:2048
	ds_read_b128 v[166:169], v145 offset:3072
	ds_read_b128 v[170:173], v146
	ds_read_b128 v[174:177], v146 offset:1024
	ds_read_b128 v[178:181], v146 offset:2048
	ds_read_b128 v[182:185], v146 offset:3072
	s_add_u32 s28, s26, 0x100
	s_addc_u32 s29, s27, 0
	s_cmp_eq_u32 s42, 4
	s_cselect_b32 s35, s7, s29
	s_cselect_b32 s34, s6, s28
	s_cselect_b32 s31, s25, s41
	s_cselect_b32 s30, s24, s23
	v_lshl_add_u64 v[160:161], s[26:27], 0, v[134:135]
	s_add_i32 m0, s3, 0xc000
	ds_read_b128 v[190:193], v147
	ds_read_b128 v[194:197], v147 offset:1024
	ds_read_b128 v[198:201], v147 offset:2048
	ds_read_b128 v[202:205], v147 offset:3072
	ds_read_b128 v[206:209], v147 offset:4096
	ds_read_b128 v[210:213], v147 offset:5120
	ds_read_b128 v[214:217], v147 offset:6144
	ds_read_b128 v[218:221], v147 offset:7168
	global_load_lds_dwordx4 v[160:161], off
	v_lshl_add_u64 v[160:161], s[26:27], 0, v[136:137]
	s_add_i32 m0, s3, 0xe000
	s_nop 0
	global_load_lds_dwordx4 v[160:161], off
	s_waitcnt vmcnt(8)
	s_waitcnt lgkmcnt(0)
	s_barrier
	s_setprio 1
	s_waitcnt lgkmcnt(0)
	v_mfma_f32_16x16x32_bf16 v[126:129], v[148:151], v[190:193], v[126:129]
	v_mfma_f32_16x16x32_bf16 v[122:125], v[156:159], v[190:193], v[122:125]
	v_mfma_f32_16x16x32_bf16 v[118:121], v[148:151], v[198:201], v[118:121]
	v_mfma_f32_16x16x32_bf16 v[114:117], v[156:159], v[198:201], v[114:117]
	v_mfma_f32_16x16x32_bf16 v[106:109], v[148:151], v[206:209], v[106:109]
	v_mfma_f32_16x16x32_bf16 v[98:101], v[156:159], v[206:209], v[98:101]
	v_mfma_f32_16x16x32_bf16 v[90:93], v[148:151], v[214:217], v[90:93]
	v_mfma_f32_16x16x32_bf16 v[82:85], v[156:159], v[214:217], v[82:85]
	v_mfma_f32_16x16x32_bf16 v[126:129], v[152:155], v[194:197], v[126:129]
	v_mfma_f32_16x16x32_bf16 v[122:125], v[166:169], v[194:197], v[122:125]
	v_mfma_f32_16x16x32_bf16 v[118:121], v[152:155], v[202:205], v[118:121]
	v_mfma_f32_16x16x32_bf16 v[114:117], v[166:169], v[202:205], v[114:117]
	v_mfma_f32_16x16x32_bf16 v[106:109], v[152:155], v[210:213], v[106:109]
	v_mfma_f32_16x16x32_bf16 v[98:101], v[166:169], v[210:213], v[98:101]
	v_mfma_f32_16x16x32_bf16 v[90:93], v[152:155], v[218:221], v[90:93]
	v_mfma_f32_16x16x32_bf16 v[82:85], v[166:169], v[218:221], v[82:85]
	v_mfma_f32_16x16x32_bf16 v[110:113], v[170:173], v[190:193], v[110:113]
	v_mfma_f32_16x16x32_bf16 v[102:105], v[178:181], v[190:193], v[102:105]
	v_mfma_f32_16x16x32_bf16 v[94:97], v[170:173], v[198:201], v[94:97]
	v_mfma_f32_16x16x32_bf16 v[86:89], v[178:181], v[198:201], v[86:89]
	v_mfma_f32_16x16x32_bf16 v[78:81], v[170:173], v[206:209], v[78:81]
	v_mfma_f32_16x16x32_bf16 v[74:77], v[178:181], v[206:209], v[74:77]
	v_mfma_f32_16x16x32_bf16 v[70:73], v[170:173], v[214:217], v[70:73]
	v_mfma_f32_16x16x32_bf16 v[66:69], v[178:181], v[214:217], v[66:69]
	v_mfma_f32_16x16x32_bf16 v[110:113], v[174:177], v[194:197], v[110:113]
	v_mfma_f32_16x16x32_bf16 v[102:105], v[182:185], v[194:197], v[102:105]
	v_mfma_f32_16x16x32_bf16 v[94:97], v[174:177], v[202:205], v[94:97]
	v_mfma_f32_16x16x32_bf16 v[86:89], v[182:185], v[202:205], v[86:89]
	v_mfma_f32_16x16x32_bf16 v[78:81], v[174:177], v[210:213], v[78:81]
	v_mfma_f32_16x16x32_bf16 v[74:77], v[182:185], v[210:213], v[74:77]
	v_mfma_f32_16x16x32_bf16 v[70:73], v[174:177], v[218:221], v[70:73]
	v_mfma_f32_16x16x32_bf16 v[66:69], v[182:185], v[218:221], v[66:69]
	s_setprio 0
	s_barrier
	s_add_i32 s26, s37, s2
	v_lshl_add_u64 v[160:161], s[30:31], 0, v[132:133]
	s_mov_b32 m0, s26
	ds_read_b128 v[190:193], v147 offset:16384
	ds_read_b128 v[194:197], v147 offset:17408
	ds_read_b128 v[198:201], v147 offset:18432
	ds_read_b128 v[202:205], v147 offset:19456
	ds_read_b128 v[206:209], v147 offset:20480
	ds_read_b128 v[210:213], v147 offset:21504
	ds_read_b128 v[214:217], v147 offset:22528
	ds_read_b128 v[218:221], v147 offset:23552
	global_load_lds_dwordx4 v[160:161], off
	s_add_i32 m0, s26, 0x2000
	s_add_u32 s26, s30, 0x160000
	v_lshl_add_u64 v[186:187], s[30:31], 0, v[130:131]
	s_addc_u32 s27, s31, 0
	s_add_i32 s43, s38, s2
	global_load_lds_dwordx4 v[186:187], off
	v_lshl_add_u64 v[222:223], s[26:27], 0, v[132:133]
	s_mov_b32 m0, s43
	v_lshl_add_u64 v[224:225], s[34:35], 0, v[130:131]
	global_load_lds_dwordx4 v[222:223], off
	v_lshl_add_u64 v[222:223], s[26:27], 0, v[130:131]
	s_add_i32 m0, s43, 0x2000
	s_nop 0
	global_load_lds_dwordx4 v[222:223], off
	v_lshl_add_u64 v[222:223], s[34:35], 0, v[132:133]
	s_mov_b32 m0, s3
	s_nop 0
	global_load_lds_dwordx4 v[222:223], off
	s_mov_b32 m0, s4
	s_nop 0
	global_load_lds_dwordx4 v[224:225], off
	s_waitcnt vmcnt(8)
	s_waitcnt lgkmcnt(0)
	s_barrier
; #define PG8_STAGE(bufoff, gbase, voff) do { _Pragma("unroll") for (int _i = 0; _i < 2; ++_i) \
;         __builtin_amdgcn_global_load_lds((const unsigned*)((const char*)(gbase) + (voff)[_i]), (PG8_LAS unsigned*)(lds + (bufoff) + ldsw + _i * 8192), 16, 0, 0); } while (0)
; #define PG8_LDA(dst, b, h) do { _Pragma("unroll") for (int m = 0; m < 4; ++m) _Pragma("unroll") for (int k = 0; k < 2; ++k) dst[m][k] = *(const PG8_LAS bf16x8*)(lds + PG8_SA(b, h) + aoff + m * 2048 + k * 1024); } while (0)
; #define PG8_LDB(dst, b, h) do { _Pragma("unroll") for (int n = 0; n < 2; ++n) _Pragma("unroll") for (int k = 0; k < 2; ++k) dst[n][k] = *(const PG8_LAS bf16x8*)(lds + PG8_SB(b, h) + boff + n * 2048 + k * 1024); } while (0)
; #define PG8_MMA(ai, bj, At, Bt) do { __builtin_amdgcn_s_setprio(1); _Pragma("unroll") for (int m = 0; m < 4; ++m) _Pragma("unroll") for (int n = 0; n < 2; ++n) _Pragma("unroll") for (int k = 0; k < 2; ++k) \
;         acc[ai][bj][m][n] = __builtin_amdgcn_mfma_f32_16x16x32_bf16(Bt[n][k], At[m][k], acc[ai][bj][m][n], 0, 0, 0); __builtin_amdgcn_s_setprio(0); } while (0)
; #define PG8_WAIT_V(n) asm volatile("s_waitcnt vmcnt(" #n ")" ::: "memory")
; #define PG8_WAIT_L(n) asm volatile("s_waitcnt lgkmcnt(" #n ")" ::: "memory")
; #define PG8_BAR __builtin_amdgcn_s_barrier()
; #define PG8_SCHED __builtin_amdgcn_sched_barrier(0)
; template <class Epi, class Sched, bool ALIGN_EPI = false, bool SP2 = false>
; __device__ __forceinline__ void gemm_phase(PG8_LAS unsigned char* lds, const Gemm g, const Sched& S, const Epi& E) {
;     ...
;             PG8_WAIT_V(8); PG8_WAIT_L(0); PG8_BAR; PG8_MMA(0, 0, At, B0); PG8_MMA(0, 1, At, B1); PG8_BAR; PG8_SCHED;
;             PG8_LDA(At, 0, 1); PG8_STAGE(PG8_SB(0, 0), b2, voffB); PG8_STAGE(PG8_SB(0, 1), b2 + hstep, voffB); PG8_STAGE(PG8_SA(0, 0), a2, voffA);
;             PG8_WAIT_V(8); PG8_WAIT_L(0); PG8_BAR; PG8_MMA(1, 0, At, B0); PG8_MMA(1, 1, At, B1); PG8_BAR; PG8_SCHED;
;             PG8_LDB(B0, 1, 0); PG8_LDB(B1, 1, 1); PG8_SCHED; PG8_LDA(At, 1, 0); PG8_STAGE(PG8_SA(0, 1), a2 + hstep, voffA);
;             PG8_WAIT_V(8); PG8_WAIT_L(0); PG8_BAR; PG8_MMA(0, 0, At, B0); PG8_MMA(0, 1, At, B1); PG8_BAR; PG8_SCHED;
	s_setprio 1
	s_waitcnt lgkmcnt(0)
	v_mfma_f32_16x16x32_bf16 v[62:65], v[148:151], v[190:193], v[62:65]
	v_mfma_f32_16x16x32_bf16 v[58:61], v[156:159], v[190:193], v[58:61]
	v_mfma_f32_16x16x32_bf16 v[54:57], v[148:151], v[198:201], v[54:57]
	v_mfma_f32_16x16x32_bf16 v[50:53], v[156:159], v[198:201], v[50:53]
	v_mfma_f32_16x16x32_bf16 v[38:41], v[148:151], v[206:209], v[38:41]
	v_mfma_f32_16x16x32_bf16 v[34:37], v[156:159], v[206:209], v[34:37]
	v_mfma_f32_16x16x32_bf16 v[22:25], v[148:151], v[214:217], v[22:25]
	v_mfma_f32_16x16x32_bf16 v[18:21], v[156:159], v[214:217], v[18:21]
	v_mfma_f32_16x16x32_bf16 v[62:65], v[152:155], v[194:197], v[62:65]
	v_mfma_f32_16x16x32_bf16 v[58:61], v[166:169], v[194:197], v[58:61]
	v_mfma_f32_16x16x32_bf16 v[54:57], v[152:155], v[202:205], v[54:57]
	v_mfma_f32_16x16x32_bf16 v[50:53], v[166:169], v[202:205], v[50:53]
	v_mfma_f32_16x16x32_bf16 v[38:41], v[152:155], v[210:213], v[38:41]
	v_mfma_f32_16x16x32_bf16 v[34:37], v[166:169], v[210:213], v[34:37]
	v_mfma_f32_16x16x32_bf16 v[22:25], v[152:155], v[218:221], v[22:25]
	v_mfma_f32_16x16x32_bf16 v[18:21], v[166:169], v[218:221], v[18:21]
	v_mfma_f32_16x16x32_bf16 v[46:49], v[170:173], v[190:193], v[46:49]
	v_mfma_f32_16x16x32_bf16 v[42:45], v[178:181], v[190:193], v[42:45]
	v_mfma_f32_16x16x32_bf16 v[30:33], v[170:173], v[198:201], v[30:33]
	v_mfma_f32_16x16x32_bf16 v[26:29], v[178:181], v[198:201], v[26:29]
	v_mfma_f32_16x16x32_bf16 v[14:17], v[170:173], v[206:209], v[14:17]
	v_mfma_f32_16x16x32_bf16 v[10:13], v[178:181], v[206:209], v[10:13]
	v_mfma_f32_16x16x32_bf16 v[6:9], v[170:173], v[214:217], v[6:9]
	v_mfma_f32_16x16x32_bf16 v[2:5], v[178:181], v[214:217], v[2:5]
	v_mfma_f32_16x16x32_bf16 v[46:49], v[174:177], v[194:197], v[46:49]
	v_mfma_f32_16x16x32_bf16 v[42:45], v[182:185], v[194:197], v[42:45]
	v_mfma_f32_16x16x32_bf16 v[30:33], v[174:177], v[202:205], v[30:33]
	v_mfma_f32_16x16x32_bf16 v[26:29], v[182:185], v[202:205], v[26:29]
	v_mfma_f32_16x16x32_bf16 v[14:17], v[174:177], v[210:213], v[14:17]
	v_mfma_f32_16x16x32_bf16 v[10:13], v[182:185], v[210:213], v[10:13]
	v_mfma_f32_16x16x32_bf16 v[6:9], v[174:177], v[218:221], v[6:9]
	v_mfma_f32_16x16x32_bf16 v[2:5], v[182:185], v[218:221], v[2:5]
	s_setprio 0
	s_barrier
	s_add_i32 s43, 0, 0x18000
	v_add_u32_e32 v162, s43, v142
	s_add_i32 s44, 0, 0x1c000
	ds_read_b128 v[148:151], v162
	ds_read_b128 v[152:155], v162 offset:1024
	ds_read_b128 v[156:159], v162 offset:2048
	ds_read_b128 v[166:169], v162 offset:3072
	v_add_u32_e32 v162, s44, v142
	ds_read_b128 v[170:173], v162
	ds_read_b128 v[174:177], v162 offset:1024
	ds_read_b128 v[178:181], v162 offset:2048
	ds_read_b128 v[182:185], v162 offset:3072
	s_add_u32 s26, s34, 0x160000
	s_addc_u32 s27, s35, 0
	s_mov_b32 m0, s5
	v_lshl_add_u64 v[226:227], s[26:27], 0, v[132:133]
	ds_read_b128 v[190:193], v147 offset:32768
	ds_read_b128 v[194:197], v147 offset:33792
	ds_read_b128 v[198:201], v147 offset:34816
	ds_read_b128 v[202:205], v147 offset:35840
	ds_read_b128 v[206:209], v147 offset:36864
	ds_read_b128 v[210:213], v147 offset:37888
	ds_read_b128 v[214:217], v147 offset:38912
	ds_read_b128 v[218:221], v147 offset:39936
	global_load_lds_dwordx4 v[226:227], off
	v_lshl_add_u64 v[226:227], s[26:27], 0, v[130:131]
	s_mov_b32 m0, s11
	s_nop 0
	global_load_lds_dwordx4 v[226:227], off
	s_waitcnt vmcnt(8)
	s_waitcnt lgkmcnt(0)
	s_barrier
	s_setprio 1
	s_waitcnt lgkmcnt(0)
	v_mfma_f32_16x16x32_bf16 v[126:129], v[148:151], v[190:193], v[126:129]
	v_mfma_f32_16x16x32_bf16 v[122:125], v[156:159], v[190:193], v[122:125]
	v_mfma_f32_16x16x32_bf16 v[118:121], v[148:151], v[198:201], v[118:121]
	v_mfma_f32_16x16x32_bf16 v[114:117], v[156:159], v[198:201], v[114:117]
	v_mfma_f32_16x16x32_bf16 v[106:109], v[148:151], v[206:209], v[106:109]
	v_mfma_f32_16x16x32_bf16 v[98:101], v[156:159], v[206:209], v[98:101]
	v_mfma_f32_16x16x32_bf16 v[90:93], v[148:151], v[214:217], v[90:93]
	v_mfma_f32_16x16x32_bf16 v[82:85], v[156:159], v[214:217], v[82:85]
	v_mfma_f32_16x16x32_bf16 v[126:129], v[152:155], v[194:197], v[126:129]
	v_mfma_f32_16x16x32_bf16 v[122:125], v[166:169], v[194:197], v[122:125]
	v_mfma_f32_16x16x32_bf16 v[118:121], v[152:155], v[202:205], v[118:121]
	v_mfma_f32_16x16x32_bf16 v[114:117], v[166:169], v[202:205], v[114:117]
	v_mfma_f32_16x16x32_bf16 v[106:109], v[152:155], v[210:213], v[106:109]
	v_mfma_f32_16x16x32_bf16 v[98:101], v[166:169], v[210:213], v[98:101]
	v_mfma_f32_16x16x32_bf16 v[90:93], v[152:155], v[218:221], v[90:93]
	v_mfma_f32_16x16x32_bf16 v[82:85], v[166:169], v[218:221], v[82:85]
	v_mfma_f32_16x16x32_bf16 v[110:113], v[170:173], v[190:193], v[110:113]
	v_mfma_f32_16x16x32_bf16 v[102:105], v[178:181], v[190:193], v[102:105]
	v_mfma_f32_16x16x32_bf16 v[94:97], v[170:173], v[198:201], v[94:97]
	v_mfma_f32_16x16x32_bf16 v[86:89], v[178:181], v[198:201], v[86:89]
	v_mfma_f32_16x16x32_bf16 v[78:81], v[170:173], v[206:209], v[78:81]
	v_mfma_f32_16x16x32_bf16 v[74:77], v[178:181], v[206:209], v[74:77]
	v_mfma_f32_16x16x32_bf16 v[70:73], v[170:173], v[214:217], v[70:73]
	v_mfma_f32_16x16x32_bf16 v[66:69], v[178:181], v[214:217], v[66:69]
	v_mfma_f32_16x16x32_bf16 v[110:113], v[174:177], v[194:197], v[110:113]
	v_mfma_f32_16x16x32_bf16 v[102:105], v[182:185], v[194:197], v[102:105]
	v_mfma_f32_16x16x32_bf16 v[94:97], v[174:177], v[202:205], v[94:97]
	v_mfma_f32_16x16x32_bf16 v[86:89], v[182:185], v[202:205], v[86:89]
	v_mfma_f32_16x16x32_bf16 v[78:81], v[174:177], v[210:213], v[78:81]
	v_mfma_f32_16x16x32_bf16 v[74:77], v[182:185], v[210:213], v[74:77]
	v_mfma_f32_16x16x32_bf16 v[70:73], v[174:177], v[218:221], v[70:73]
	v_mfma_f32_16x16x32_bf16 v[66:69], v[182:185], v[218:221], v[66:69]
	s_setprio 0
	s_barrier
; #define PG8_STAGE(bufoff, gbase, voff) do { _Pragma("unroll") for (int _i = 0; _i < 2; ++_i) \
;         __builtin_amdgcn_global_load_lds((const unsigned*)((const char*)(gbase) + (voff)[_i]), (PG8_LAS unsigned*)(lds + (bufoff) + ldsw + _i * 8192), 16, 0, 0); } while (0)
; #define PG8_LDA(dst, b, h) do { _Pragma("unroll") for (int m = 0; m < 4; ++m) _Pragma("unroll") for (int k = 0; k < 2; ++k) dst[m][k] = *(const PG8_LAS bf16x8*)(lds + PG8_SA(b, h) + aoff + m * 2048 + k * 1024); } while (0)
; #define PG8_WAIT_V(n) asm volatile("s_waitcnt vmcnt(" #n ")" ::: "memory")
; template <class Epi, class Sched, bool ALIGN_EPI = false, bool SP2 = false>
; __device__ __forceinline__ void gemm_phase(PG8_LAS unsigned char* lds, const Gemm g, const Sched& S, const Epi& E) {
;     ...
;             PG8_LDA(At, 1, 1); PG8_STAGE(PG8_SB(1, 0), b3, voffB); PG8_STAGE(PG8_SB(1, 1), b3 + hstep, voffB); PG8_STAGE(PG8_SA(1, 0), a3, voffA);
;             PG8_WAIT_V(8); PG8_WAIT_L(0); PG8_BAR; PG8_MMA(1, 0, At, B0); PG8_MMA(1, 1, At, B1); PG8_BAR; PG8_SCHED;
;             } else {
;             PG8_LDB(B0, 0, 0); PG8_SCHED; PG8_LDA(At, 0, 0); PG8_STAGE(PG8_SA(1, 1), a1 + hstep, voffA);
;             PG8_WAIT_L(8); PG8_BAR; PG8_WAIT_L(0); PG8_MMA(0, 0, At, B0); PG8_BAR; PG8_SCHED;
;             PG8_LDB(B1, 0, 1); PG8_STAGE(PG8_SB(0, 0), b2, voffB);
;             PG8_BAR; PG8_WAIT_L(0); PG8_MMA(0, 1, At, B1); PG8_BAR;
;             PG8_LDA(At, 0, 1); PG8_STAGE(PG8_SA(0, 0), a2, voffA);
;             PG8_BAR; PG8_WAIT_L(0); PG8_MMA(1, 0, At, B0); PG8_BAR; PG8_SCHED;
;             PG8_STAGE(PG8_SB(0, 1), b2 + hstep, voffB);
;             PG8_WAIT_V(6); PG8_BAR; PG8_MMA(1, 1, At, B1); PG8_BAR;
;             PG8_LDB(B0, 1, 0); PG8_SCHED; PG8_LDA(At, 1, 0); PG8_STAGE(PG8_SA(0, 1), a2 + hstep, voffA);
;             PG8_WAIT_L(8); PG8_BAR; PG8_WAIT_L(0); PG8_MMA(0, 0, At, B0); PG8_BAR; PG8_SCHED;
;             PG8_LDB(B1, 1, 1); PG8_STAGE(PG8_SB(1, 0), b3, voffB);
;             PG8_BAR; PG8_WAIT_L(0); PG8_MMA(0, 1, At, B1); PG8_BAR;
;             PG8_LDA(At, 1, 1); PG8_STAGE(PG8_SA(1, 0), a3, voffA);
;             PG8_BAR; PG8_WAIT_L(0); PG8_MMA(1, 0, At, B0); PG8_BAR; PG8_SCHED;
;             PG8_STAGE(PG8_SB(1, 1), b3 + hstep, voffB);
;             PG8_WAIT_V(6); PG8_BAR; PG8_MMA(1, 1, At, B1); PG8_BAR;
;             }
;         }
;         if constexpr (ALIGN_EPI) { if (wr == 0) PG8_BAR; }
	s_add_i32 s26, s43, s2
	v_lshl_add_u64 v[160:161], v[160:161], 0, s[18:19]
	s_mov_b32 m0, s26
	ds_read_b128 v[190:193], v147 offset:49152
	ds_read_b128 v[194:197], v147 offset:50176
	ds_read_b128 v[198:201], v147 offset:51200
	ds_read_b128 v[202:205], v147 offset:52224
	ds_read_b128 v[206:209], v147 offset:53248
	ds_read_b128 v[210:213], v147 offset:54272
	ds_read_b128 v[214:217], v147 offset:55296
	ds_read_b128 v[218:221], v147 offset:56320
	global_load_lds_dwordx4 v[160:161], off
	s_add_i32 m0, s26, 0x2000
	s_add_u32 s26, s30, 0x160080
	v_lshl_add_u64 v[160:161], v[186:187], 0, s[18:19]
	s_addc_u32 s27, s31, 0
	s_add_i32 s30, s44, s2
	global_load_lds_dwordx4 v[160:161], off
	v_lshl_add_u64 v[160:161], s[26:27], 0, v[132:133]
	s_mov_b32 m0, s30
	s_nop 0
	global_load_lds_dwordx4 v[160:161], off
	v_lshl_add_u64 v[160:161], s[26:27], 0, v[130:131]
	s_add_i32 m0, s30, 0x2000
	s_nop 0
	global_load_lds_dwordx4 v[160:161], off
	v_lshl_add_u64 v[160:161], v[222:223], 0, s[18:19]
	s_mov_b32 m0, s33
	s_nop 0
	global_load_lds_dwordx4 v[160:161], off
	v_lshl_add_u64 v[160:161], v[224:225], 0, s[18:19]
	s_mov_b32 m0, s36
	s_nop 0
	global_load_lds_dwordx4 v[160:161], off
	s_waitcnt vmcnt(8)
	s_waitcnt lgkmcnt(0)
	s_barrier
	s_setprio 1
	s_waitcnt lgkmcnt(0)
	v_mfma_f32_16x16x32_bf16 v[62:65], v[148:151], v[190:193], v[62:65]
	v_mfma_f32_16x16x32_bf16 v[58:61], v[156:159], v[190:193], v[58:61]
	v_mfma_f32_16x16x32_bf16 v[54:57], v[148:151], v[198:201], v[54:57]
	v_mfma_f32_16x16x32_bf16 v[50:53], v[156:159], v[198:201], v[50:53]
	v_mfma_f32_16x16x32_bf16 v[38:41], v[148:151], v[206:209], v[38:41]
	v_mfma_f32_16x16x32_bf16 v[34:37], v[156:159], v[206:209], v[34:37]
	v_mfma_f32_16x16x32_bf16 v[22:25], v[148:151], v[214:217], v[22:25]
	v_mfma_f32_16x16x32_bf16 v[18:21], v[156:159], v[214:217], v[18:21]
	v_mfma_f32_16x16x32_bf16 v[62:65], v[152:155], v[194:197], v[62:65]
	v_mfma_f32_16x16x32_bf16 v[58:61], v[166:169], v[194:197], v[58:61]
	v_mfma_f32_16x16x32_bf16 v[54:57], v[152:155], v[202:205], v[54:57]
	v_mfma_f32_16x16x32_bf16 v[50:53], v[166:169], v[202:205], v[50:53]
	v_mfma_f32_16x16x32_bf16 v[38:41], v[152:155], v[210:213], v[38:41]
	v_mfma_f32_16x16x32_bf16 v[34:37], v[166:169], v[210:213], v[34:37]
	v_mfma_f32_16x16x32_bf16 v[22:25], v[152:155], v[218:221], v[22:25]
	v_mfma_f32_16x16x32_bf16 v[18:21], v[166:169], v[218:221], v[18:21]
	v_mfma_f32_16x16x32_bf16 v[46:49], v[170:173], v[190:193], v[46:49]
	v_mfma_f32_16x16x32_bf16 v[42:45], v[178:181], v[190:193], v[42:45]
	v_mfma_f32_16x16x32_bf16 v[30:33], v[170:173], v[198:201], v[30:33]
	v_mfma_f32_16x16x32_bf16 v[26:29], v[178:181], v[198:201], v[26:29]
	v_mfma_f32_16x16x32_bf16 v[14:17], v[170:173], v[206:209], v[14:17]
	v_mfma_f32_16x16x32_bf16 v[10:13], v[178:181], v[206:209], v[10:13]
	v_mfma_f32_16x16x32_bf16 v[6:9], v[170:173], v[214:217], v[6:9]
	v_mfma_f32_16x16x32_bf16 v[2:5], v[178:181], v[214:217], v[2:5]
	v_mfma_f32_16x16x32_bf16 v[46:49], v[174:177], v[194:197], v[46:49]
	v_mfma_f32_16x16x32_bf16 v[42:45], v[182:185], v[194:197], v[42:45]
	v_mfma_f32_16x16x32_bf16 v[30:33], v[174:177], v[202:205], v[30:33]
	v_mfma_f32_16x16x32_bf16 v[26:29], v[182:185], v[202:205], v[26:29]
	v_mfma_f32_16x16x32_bf16 v[14:17], v[174:177], v[210:213], v[14:17]
	v_mfma_f32_16x16x32_bf16 v[10:13], v[182:185], v[210:213], v[10:13]
	v_mfma_f32_16x16x32_bf16 v[6:9], v[174:177], v[218:221], v[6:9]
	v_mfma_f32_16x16x32_bf16 v[2:5], v[182:185], v[218:221], v[2:5]
	s_setprio 0
	s_barrier
	s_add_i32 s42, s42, 2
	s_add_u32 s23, s23, 0x100
	s_addc_u32 s41, s41, 0
	s_cmp_gt_u32 s42, 5
	s_mov_b64 s[26:27], s[28:29]
	s_cbranch_scc0 .LBB0_1217
	s_and_b64 vcc, exec, s[20:21]
	s_cbranch_vccz .LBB0_1220
	s_barrier

; #define PG8_STAGE(bufoff, gbase, voff) do { _Pragma("unroll") for (int _i = 0; _i < 2; ++_i) \
;         __builtin_amdgcn_global_load_lds((const unsigned*)((const char*)(gbase) + (voff)[_i]), (PG8_LAS unsigned*)(lds + (bufoff) + ldsw + _i * 8192), 16, 0, 0); } while (0)
; #define PG8_LDA(dst, b, h) do { _Pragma("unroll") for (int m = 0; m < 4; ++m) _Pragma("unroll") for (int k = 0; k < 2; ++k) dst[m][k] = *(const PG8_LAS bf16x8*)(lds + PG8_SA(b, h) + aoff + m * 2048 + k * 1024); } while (0)
; #define PG8_LDB(dst, b, h) do { _Pragma("unroll") for (int n = 0; n < 2; ++n) _Pragma("unroll") for (int k = 0; k < 2; ++k) dst[n][k] = *(const PG8_LAS bf16x8*)(lds + PG8_SB(b, h) + boff + n * 2048 + k * 1024); } while (0)
; #define PG8_WAIT_V(n) asm volatile("s_waitcnt vmcnt(" #n ")" ::: "memory")
; #define PG8_WAIT_L(n) asm volatile("s_waitcnt lgkmcnt(" #n ")" ::: "memory")
; #define PG8_BAR __builtin_amdgcn_s_barrier()
; #define PG8_SCHED __builtin_amdgcn_sched_barrier(0)
; template <class Epi, class Sched, bool ALIGN_EPI = false, bool SP2 = false>
; __device__ __forceinline__ void gemm_phase(PG8_LAS unsigned char* lds, const Gemm g, const Sched& S, const Epi& E) {
;     ...
;         const char* nA = has_next ? (const char*)g.A + (size_t)nxt.pm * tstep + (size_t)nxt.k0 * 2 : cA; const char* nB = has_next ? (const char*)g.Bt + (size_t)nxt.pn * tstep + (size_t)nxt.k0 * 2 : cB;
;         for (int t = 0; t < nt; t += 2) {
;             const bool last = (t == nt - 2);
;             const char* a1 = cA + (size_t)(t + 1) * kstep;
;             const char* a2 = last ? nA : cA + (size_t)(t + 2) * kstep; const char* b2 = last ? nB : cB + (size_t)(t + 2) * kstep;
;             const char* a3 = a2 + kstep; const char* b3 = b2 + kstep;
;             if (last && has_next) S.a_ready(nxt);
;             if constexpr (SP2) {
;             PG8_LDB(B0, 0, 0); PG8_LDB(B1, 0, 1); PG8_SCHED; PG8_LDA(At, 0, 0); PG8_STAGE(PG8_SA(1, 1), a1 + hstep, voffA);
;             PG8_WAIT_V(8); PG8_WAIT_L(0); PG8_BAR; PG8_MMA(0, 0, At, B0); PG8_MMA(0, 1, At, B1); PG8_BAR; PG8_SCHED;
;             PG8_LDA(At, 0, 1); PG8_STAGE(PG8_SB(0, 0), b2, voffB); PG8_STAGE(PG8_SB(0, 1), b2 + hstep, voffB); PG8_STAGE(PG8_SA(0, 0), a2, voffA);
;             PG8_WAIT_V(8); PG8_WAIT_L(0); PG8_BAR; PG8_MMA(1, 0, At, B0); PG8_MMA(1, 1, At, B1); PG8_BAR; PG8_SCHED;
.LBB0_1350:
	ds_read_b128 v[148:151], v159
	ds_read_b128 v[152:155], v159 offset:1024
	ds_read_b128 v[166:169], v159 offset:2048
	ds_read_b128 v[170:173], v159 offset:3072
	ds_read_b128 v[174:177], v160
	ds_read_b128 v[178:181], v160 offset:1024
	ds_read_b128 v[182:185], v160 offset:2048
	ds_read_b128 v[190:193], v160 offset:3072
	s_add_u32 s28, s26, 0xfff80080
	s_addc_u32 s29, s27, -1
	s_cmp_eq_u32 s42, 28
	s_cselect_b32 s31, s7, s29
	s_cselect_b32 s30, s21, s28
	s_cselect_b32 s29, s19, s41
	s_cselect_b32 s28, s39, s40
	v_lshl_add_u64 v[186:187], s[26:27], 0, v[140:141]
	s_add_i32 m0, s3, 0xc000
	ds_read_b128 v[194:197], v161
	ds_read_b128 v[198:201], v161 offset:1024
	ds_read_b128 v[202:205], v161 offset:2048
	ds_read_b128 v[206:209], v161 offset:3072
	ds_read_b128 v[210:213], v161 offset:4096
	ds_read_b128 v[214:217], v161 offset:5120
	ds_read_b128 v[218:221], v161 offset:6144
	ds_read_b128 v[222:225], v161 offset:7168
	global_load_lds_dwordx4 v[186:187], off
	v_lshl_add_u64 v[186:187], s[26:27], 0, v[142:143]
	s_add_i32 m0, s3, 0xe000
	s_nop 0
	global_load_lds_dwordx4 v[186:187], off
	s_waitcnt vmcnt(8)
	s_waitcnt lgkmcnt(0)
	s_barrier
	s_setprio 1
	s_waitcnt lgkmcnt(0)
	v_mfma_f32_16x16x32_bf16 v[126:129], v[148:151], v[194:197], v[126:129]
	v_mfma_f32_16x16x32_bf16 v[122:125], v[166:169], v[194:197], v[122:125]
	v_mfma_f32_16x16x32_bf16 v[110:113], v[148:151], v[202:205], v[110:113]
	v_mfma_f32_16x16x32_bf16 v[106:109], v[166:169], v[202:205], v[106:109]
	v_mfma_f32_16x16x32_bf16 v[94:97], v[148:151], v[210:213], v[94:97]
	v_mfma_f32_16x16x32_bf16 v[90:93], v[166:169], v[210:213], v[90:93]
	v_mfma_f32_16x16x32_bf16 v[78:81], v[148:151], v[218:221], v[78:81]
	v_mfma_f32_16x16x32_bf16 v[74:77], v[166:169], v[218:221], v[74:77]
	v_mfma_f32_16x16x32_bf16 v[126:129], v[152:155], v[198:201], v[126:129]
	v_mfma_f32_16x16x32_bf16 v[122:125], v[170:173], v[198:201], v[122:125]
	v_mfma_f32_16x16x32_bf16 v[110:113], v[152:155], v[206:209], v[110:113]
	v_mfma_f32_16x16x32_bf16 v[106:109], v[170:173], v[206:209], v[106:109]
	v_mfma_f32_16x16x32_bf16 v[94:97], v[152:155], v[214:217], v[94:97]
	v_mfma_f32_16x16x32_bf16 v[90:93], v[170:173], v[214:217], v[90:93]
	v_mfma_f32_16x16x32_bf16 v[78:81], v[152:155], v[222:225], v[78:81]
	v_mfma_f32_16x16x32_bf16 v[74:77], v[170:173], v[222:225], v[74:77]
	v_mfma_f32_16x16x32_bf16 v[118:121], v[174:177], v[194:197], v[118:121]
	v_mfma_f32_16x16x32_bf16 v[114:117], v[182:185], v[194:197], v[114:117]
	v_mfma_f32_16x16x32_bf16 v[102:105], v[174:177], v[202:205], v[102:105]
	v_mfma_f32_16x16x32_bf16 v[98:101], v[182:185], v[202:205], v[98:101]
	v_mfma_f32_16x16x32_bf16 v[86:89], v[174:177], v[210:213], v[86:89]
	v_mfma_f32_16x16x32_bf16 v[82:85], v[182:185], v[210:213], v[82:85]
	v_mfma_f32_16x16x32_bf16 v[70:73], v[174:177], v[218:221], v[70:73]
	v_mfma_f32_16x16x32_bf16 v[66:69], v[182:185], v[218:221], v[66:69]
	v_mfma_f32_16x16x32_bf16 v[118:121], v[178:181], v[198:201], v[118:121]
	v_mfma_f32_16x16x32_bf16 v[114:117], v[190:193], v[198:201], v[114:117]
	v_mfma_f32_16x16x32_bf16 v[102:105], v[178:181], v[206:209], v[102:105]
	v_mfma_f32_16x16x32_bf16 v[98:101], v[190:193], v[206:209], v[98:101]
	v_mfma_f32_16x16x32_bf16 v[86:89], v[178:181], v[214:217], v[86:89]
	v_mfma_f32_16x16x32_bf16 v[82:85], v[190:193], v[214:217], v[82:85]
	v_mfma_f32_16x16x32_bf16 v[70:73], v[178:181], v[222:225], v[70:73]
	v_mfma_f32_16x16x32_bf16 v[66:69], v[190:193], v[222:225], v[66:69]
	s_setprio 0
	s_barrier
	s_add_i32 s43, s36, s2
	v_lshl_add_u64 v[186:187], s[28:29], 0, v[132:133]
	s_mov_b32 m0, s43
	ds_read_b128 v[194:197], v161 offset:16384
	ds_read_b128 v[198:201], v161 offset:17408
	ds_read_b128 v[202:205], v161 offset:18432
	ds_read_b128 v[206:209], v161 offset:19456
	ds_read_b128 v[210:213], v161 offset:20480
	ds_read_b128 v[214:217], v161 offset:21504
	ds_read_b128 v[218:221], v161 offset:22528
	ds_read_b128 v[222:225], v161 offset:23552
	global_load_lds_dwordx4 v[186:187], off
	s_add_i32 m0, s43, 0x2000
	s_add_u32 s44, s28, 0x80000
	v_lshl_add_u64 v[226:227], s[28:29], 0, v[136:137]
	s_addc_u32 s45, s29, 0
	s_add_i32 s43, s37, s2
	global_load_lds_dwordx4 v[226:227], off
	v_lshl_add_u64 v[228:229], s[44:45], 0, v[132:133]
	s_mov_b32 m0, s43
	v_lshl_add_u64 v[230:231], s[30:31], 0, v[134:135]
	global_load_lds_dwordx4 v[228:229], off
	v_lshl_add_u64 v[228:229], s[44:45], 0, v[136:137]
	s_add_i32 m0, s43, 0x2000
	s_nop 0
	global_load_lds_dwordx4 v[228:229], off
	v_lshl_add_u64 v[228:229], s[30:31], 0, v[130:131]
	s_mov_b32 m0, s3
	s_nop 0
	global_load_lds_dwordx4 v[228:229], off
	s_mov_b32 m0, s4
	s_nop 0
	global_load_lds_dwordx4 v[230:231], off
	s_waitcnt vmcnt(8)
	s_waitcnt lgkmcnt(0)
	s_barrier
; #define PG8_STAGE(bufoff, gbase, voff) do { _Pragma("unroll") for (int _i = 0; _i < 2; ++_i) \
;         __builtin_amdgcn_global_load_lds((const unsigned*)((const char*)(gbase) + (voff)[_i]), (PG8_LAS unsigned*)(lds + (bufoff) + ldsw + _i * 8192), 16, 0, 0); } while (0)
; #define PG8_LDA(dst, b, h) do { _Pragma("unroll") for (int m = 0; m < 4; ++m) _Pragma("unroll") for (int k = 0; k < 2; ++k) dst[m][k] = *(const PG8_LAS bf16x8*)(lds + PG8_SA(b, h) + aoff + m * 2048 + k * 1024); } while (0)
; #define PG8_LDB(dst, b, h) do { _Pragma("unroll") for (int n = 0; n < 2; ++n) _Pragma("unroll") for (int k = 0; k < 2; ++k) dst[n][k] = *(const PG8_LAS bf16x8*)(lds + PG8_SB(b, h) + boff + n * 2048 + k * 1024); } while (0)
; #define PG8_MMA(ai, bj, At, Bt) do { __builtin_amdgcn_s_setprio(1); _Pragma("unroll") for (int m = 0; m < 4; ++m) _Pragma("unroll") for (int n = 0; n < 2; ++n) _Pragma("unroll") for (int k = 0; k < 2; ++k) \
;         acc[ai][bj][m][n] = __builtin_amdgcn_mfma_f32_16x16x32_bf16(Bt[n][k], At[m][k], acc[ai][bj][m][n], 0, 0, 0); __builtin_amdgcn_s_setprio(0); } while (0)
; #define PG8_WAIT_V(n) asm volatile("s_waitcnt vmcnt(" #n ")" ::: "memory")
; #define PG8_WAIT_L(n) asm volatile("s_waitcnt lgkmcnt(" #n ")" ::: "memory")
; #define PG8_BAR __builtin_amdgcn_s_barrier()
; #define PG8_SCHED __builtin_amdgcn_sched_barrier(0)
; template <class Epi, class Sched, bool ALIGN_EPI = false, bool SP2 = false>
; __device__ __forceinline__ void gemm_phase(PG8_LAS unsigned char* lds, const Gemm g, const Sched& S, const Epi& E) {
;     ...
;             PG8_WAIT_V(8); PG8_WAIT_L(0); PG8_BAR; PG8_MMA(0, 0, At, B0); PG8_MMA(0, 1, At, B1); PG8_BAR; PG8_SCHED;
;             PG8_LDA(At, 0, 1); PG8_STAGE(PG8_SB(0, 0), b2, voffB); PG8_STAGE(PG8_SB(0, 1), b2 + hstep, voffB); PG8_STAGE(PG8_SA(0, 0), a2, voffA);
;             PG8_WAIT_V(8); PG8_WAIT_L(0); PG8_BAR; PG8_MMA(1, 0, At, B0); PG8_MMA(1, 1, At, B1); PG8_BAR; PG8_SCHED;
;             PG8_LDB(B0, 1, 0); PG8_LDB(B1, 1, 1); PG8_SCHED; PG8_LDA(At, 1, 0); PG8_STAGE(PG8_SA(0, 1), a2 + hstep, voffA);
;             PG8_WAIT_V(8); PG8_WAIT_L(0); PG8_BAR; PG8_MMA(0, 0, At, B0); PG8_MMA(0, 1, At, B1); PG8_BAR; PG8_SCHED;
	s_setprio 1
	s_waitcnt lgkmcnt(0)
	v_mfma_f32_16x16x32_bf16 v[62:65], v[148:151], v[194:197], v[62:65]
	v_mfma_f32_16x16x32_bf16 v[58:61], v[166:169], v[194:197], v[58:61]
	v_mfma_f32_16x16x32_bf16 v[46:49], v[148:151], v[202:205], v[46:49]
	v_mfma_f32_16x16x32_bf16 v[42:45], v[166:169], v[202:205], v[42:45]
	v_mfma_f32_16x16x32_bf16 v[30:33], v[148:151], v[210:213], v[30:33]
	v_mfma_f32_16x16x32_bf16 v[26:29], v[166:169], v[210:213], v[26:29]
	v_mfma_f32_16x16x32_bf16 v[14:17], v[148:151], v[218:221], v[14:17]
	v_mfma_f32_16x16x32_bf16 v[10:13], v[166:169], v[218:221], v[10:13]
	v_mfma_f32_16x16x32_bf16 v[62:65], v[152:155], v[198:201], v[62:65]
	v_mfma_f32_16x16x32_bf16 v[58:61], v[170:173], v[198:201], v[58:61]
	v_mfma_f32_16x16x32_bf16 v[46:49], v[152:155], v[206:209], v[46:49]
	v_mfma_f32_16x16x32_bf16 v[42:45], v[170:173], v[206:209], v[42:45]
	v_mfma_f32_16x16x32_bf16 v[30:33], v[152:155], v[214:217], v[30:33]
	v_mfma_f32_16x16x32_bf16 v[26:29], v[170:173], v[214:217], v[26:29]
	v_mfma_f32_16x16x32_bf16 v[14:17], v[152:155], v[222:225], v[14:17]
	v_mfma_f32_16x16x32_bf16 v[10:13], v[170:173], v[222:225], v[10:13]
	v_mfma_f32_16x16x32_bf16 v[54:57], v[174:177], v[194:197], v[54:57]
	v_mfma_f32_16x16x32_bf16 v[50:53], v[182:185], v[194:197], v[50:53]
	v_mfma_f32_16x16x32_bf16 v[38:41], v[174:177], v[202:205], v[38:41]
	v_mfma_f32_16x16x32_bf16 v[34:37], v[182:185], v[202:205], v[34:37]
	v_mfma_f32_16x16x32_bf16 v[22:25], v[174:177], v[210:213], v[22:25]
	v_mfma_f32_16x16x32_bf16 v[18:21], v[182:185], v[210:213], v[18:21]
	v_mfma_f32_16x16x32_bf16 v[6:9], v[174:177], v[218:221], v[6:9]
	v_mfma_f32_16x16x32_bf16 v[2:5], v[182:185], v[218:221], v[2:5]
	v_mfma_f32_16x16x32_bf16 v[54:57], v[178:181], v[198:201], v[54:57]
	v_mfma_f32_16x16x32_bf16 v[50:53], v[190:193], v[198:201], v[50:53]
	v_mfma_f32_16x16x32_bf16 v[38:41], v[178:181], v[206:209], v[38:41]
	v_mfma_f32_16x16x32_bf16 v[34:37], v[190:193], v[206:209], v[34:37]
	v_mfma_f32_16x16x32_bf16 v[22:25], v[178:181], v[214:217], v[22:25]
	v_mfma_f32_16x16x32_bf16 v[18:21], v[190:193], v[214:217], v[18:21]
	v_mfma_f32_16x16x32_bf16 v[6:9], v[178:181], v[222:225], v[6:9]
	v_mfma_f32_16x16x32_bf16 v[2:5], v[190:193], v[222:225], v[2:5]
	s_setprio 0
	s_barrier
	s_add_i32 s43, 0, 0x18000
	v_add_u32_e32 v162, s43, v157
	s_add_i32 s44, 0, 0x1c000
	ds_read_b128 v[148:151], v162
	ds_read_b128 v[152:155], v162 offset:1024
	ds_read_b128 v[166:169], v162 offset:2048
	ds_read_b128 v[170:173], v162 offset:3072
	v_add_u32_e32 v162, s44, v157
	ds_read_b128 v[174:177], v162
	ds_read_b128 v[178:181], v162 offset:1024
	ds_read_b128 v[182:185], v162 offset:2048
	ds_read_b128 v[190:193], v162 offset:3072
	s_add_u32 s30, s30, 0x80000
	s_addc_u32 s31, s31, 0
	s_mov_b32 m0, s5
	v_lshl_add_u64 v[232:233], s[30:31], 0, v[130:131]
	ds_read_b128 v[194:197], v161 offset:32768
	ds_read_b128 v[198:201], v161 offset:33792
	ds_read_b128 v[202:205], v161 offset:34816
	ds_read_b128 v[206:209], v161 offset:35840
	ds_read_b128 v[210:213], v161 offset:36864
	ds_read_b128 v[214:217], v161 offset:37888
	ds_read_b128 v[218:221], v161 offset:38912
	ds_read_b128 v[222:225], v161 offset:39936
	global_load_lds_dwordx4 v[232:233], off
	v_lshl_add_u64 v[232:233], s[30:31], 0, v[134:135]
	s_mov_b32 m0, s17
	s_nop 0
	global_load_lds_dwordx4 v[232:233], off
	s_waitcnt vmcnt(8)
	s_waitcnt lgkmcnt(0)
	s_barrier
	s_setprio 1
	s_waitcnt lgkmcnt(0)
	v_mfma_f32_16x16x32_bf16 v[126:129], v[148:151], v[194:197], v[126:129]
	v_mfma_f32_16x16x32_bf16 v[122:125], v[166:169], v[194:197], v[122:125]
	v_mfma_f32_16x16x32_bf16 v[110:113], v[148:151], v[202:205], v[110:113]
	v_mfma_f32_16x16x32_bf16 v[106:109], v[166:169], v[202:205], v[106:109]
	v_mfma_f32_16x16x32_bf16 v[94:97], v[148:151], v[210:213], v[94:97]
	v_mfma_f32_16x16x32_bf16 v[90:93], v[166:169], v[210:213], v[90:93]
	v_mfma_f32_16x16x32_bf16 v[78:81], v[148:151], v[218:221], v[78:81]
	v_mfma_f32_16x16x32_bf16 v[74:77], v[166:169], v[218:221], v[74:77]
	v_mfma_f32_16x16x32_bf16 v[126:129], v[152:155], v[198:201], v[126:129]
	v_mfma_f32_16x16x32_bf16 v[122:125], v[170:173], v[198:201], v[122:125]
	v_mfma_f32_16x16x32_bf16 v[110:113], v[152:155], v[206:209], v[110:113]
	v_mfma_f32_16x16x32_bf16 v[106:109], v[170:173], v[206:209], v[106:109]
	v_mfma_f32_16x16x32_bf16 v[94:97], v[152:155], v[214:217], v[94:97]
	v_mfma_f32_16x16x32_bf16 v[90:93], v[170:173], v[214:217], v[90:93]
	v_mfma_f32_16x16x32_bf16 v[78:81], v[152:155], v[222:225], v[78:81]
	v_mfma_f32_16x16x32_bf16 v[74:77], v[170:173], v[222:225], v[74:77]
	v_mfma_f32_16x16x32_bf16 v[118:121], v[174:177], v[194:197], v[118:121]
	v_mfma_f32_16x16x32_bf16 v[114:117], v[182:185], v[194:197], v[114:117]
	v_mfma_f32_16x16x32_bf16 v[102:105], v[174:177], v[202:205], v[102:105]
	v_mfma_f32_16x16x32_bf16 v[98:101], v[182:185], v[202:205], v[98:101]
	v_mfma_f32_16x16x32_bf16 v[86:89], v[174:177], v[210:213], v[86:89]
	v_mfma_f32_16x16x32_bf16 v[82:85], v[182:185], v[210:213], v[82:85]
	v_mfma_f32_16x16x32_bf16 v[70:73], v[174:177], v[218:221], v[70:73]
	v_mfma_f32_16x16x32_bf16 v[66:69], v[182:185], v[218:221], v[66:69]
	v_mfma_f32_16x16x32_bf16 v[118:121], v[178:181], v[198:201], v[118:121]
	v_mfma_f32_16x16x32_bf16 v[114:117], v[190:193], v[198:201], v[114:117]
	v_mfma_f32_16x16x32_bf16 v[102:105], v[178:181], v[206:209], v[102:105]
	v_mfma_f32_16x16x32_bf16 v[98:101], v[190:193], v[206:209], v[98:101]
	v_mfma_f32_16x16x32_bf16 v[86:89], v[178:181], v[214:217], v[86:89]
	v_mfma_f32_16x16x32_bf16 v[82:85], v[190:193], v[214:217], v[82:85]
	v_mfma_f32_16x16x32_bf16 v[70:73], v[178:181], v[222:225], v[70:73]
	v_mfma_f32_16x16x32_bf16 v[66:69], v[190:193], v[222:225], v[66:69]
	s_setprio 0
	s_barrier
; #define PG8_STAGE(bufoff, gbase, voff) do { _Pragma("unroll") for (int _i = 0; _i < 2; ++_i) \
;         __builtin_amdgcn_global_load_lds((const unsigned*)((const char*)(gbase) + (voff)[_i]), (PG8_LAS unsigned*)(lds + (bufoff) + ldsw + _i * 8192), 16, 0, 0); } while (0)
; #define PG8_LDA(dst, b, h) do { _Pragma("unroll") for (int m = 0; m < 4; ++m) _Pragma("unroll") for (int k = 0; k < 2; ++k) dst[m][k] = *(const PG8_LAS bf16x8*)(lds + PG8_SA(b, h) + aoff + m * 2048 + k * 1024); } while (0)
; #define PG8_LDB(dst, b, h) do { _Pragma("unroll") for (int n = 0; n < 2; ++n) _Pragma("unroll") for (int k = 0; k < 2; ++k) dst[n][k] = *(const PG8_LAS bf16x8*)(lds + PG8_SB(b, h) + boff + n * 2048 + k * 1024); } while (0)
; #define PG8_WAIT_V(n) asm volatile("s_waitcnt vmcnt(" #n ")" ::: "memory")
; #define PG8_WAIT_L(n) asm volatile("s_waitcnt lgkmcnt(" #n ")" ::: "memory")
; #define PG8_BAR __builtin_amdgcn_s_barrier()
; #define PG8_SCHED __builtin_amdgcn_sched_barrier(0)
; template <class Epi, class Sched, bool ALIGN_EPI = false, bool SP2 = false>
; __device__ __forceinline__ void gemm_phase(PG8_LAS unsigned char* lds, const Gemm g, const Sched& S, const Epi& E) {
;     ...
;             PG8_LDA(At, 1, 1); PG8_STAGE(PG8_SB(1, 0), b3, voffB); PG8_STAGE(PG8_SB(1, 1), b3 + hstep, voffB); PG8_STAGE(PG8_SA(1, 0), a3, voffA);
;             PG8_WAIT_V(8); PG8_WAIT_L(0); PG8_BAR; PG8_MMA(1, 0, At, B0); PG8_MMA(1, 1, At, B1); PG8_BAR; PG8_SCHED;
;             } else {
;             PG8_LDB(B0, 0, 0); PG8_SCHED; PG8_LDA(At, 0, 0); PG8_STAGE(PG8_SA(1, 1), a1 + hstep, voffA);
;             PG8_WAIT_L(8); PG8_BAR; PG8_WAIT_L(0); PG8_MMA(0, 0, At, B0); PG8_BAR; PG8_SCHED;
;             PG8_LDB(B1, 0, 1); PG8_STAGE(PG8_SB(0, 0), b2, voffB);
;             PG8_BAR; PG8_WAIT_L(0); PG8_MMA(0, 1, At, B1); PG8_BAR;
;             PG8_LDA(At, 0, 1); PG8_STAGE(PG8_SA(0, 0), a2, voffA);
;             PG8_BAR; PG8_WAIT_L(0); PG8_MMA(1, 0, At, B0); PG8_BAR; PG8_SCHED;
;             PG8_STAGE(PG8_SB(0, 1), b2 + hstep, voffB);
;             PG8_WAIT_V(6); PG8_BAR; PG8_MMA(1, 1, At, B1); PG8_BAR;
;             PG8_LDB(B0, 1, 0); PG8_SCHED; PG8_LDA(At, 1, 0); PG8_STAGE(PG8_SA(0, 1), a2 + hstep, voffA);
;             PG8_WAIT_L(8); PG8_BAR; PG8_WAIT_L(0); PG8_MMA(0, 0, At, B0); PG8_BAR; PG8_SCHED;
	s_add_i32 s30, s43, s2
	v_lshl_add_u64 v[186:187], v[186:187], 0, s[12:13]
	s_mov_b32 m0, s30
	ds_read_b128 v[194:197], v161 offset:49152
	ds_read_b128 v[198:201], v161 offset:50176
	ds_read_b128 v[202:205], v161 offset:51200
	ds_read_b128 v[206:209], v161 offset:52224
	ds_read_b128 v[210:213], v161 offset:53248
	ds_read_b128 v[214:217], v161 offset:54272
	ds_read_b128 v[218:221], v161 offset:55296
	ds_read_b128 v[222:225], v161 offset:56320
	global_load_lds_dwordx4 v[186:187], off
	s_add_i32 m0, s30, 0x2000
	s_add_u32 s28, s28, 0x80080
	v_lshl_add_u64 v[186:187], v[226:227], 0, s[12:13]
	s_addc_u32 s29, s29, 0
	s_add_i32 s30, s44, s2
	global_load_lds_dwordx4 v[186:187], off
	v_lshl_add_u64 v[186:187], s[28:29], 0, v[132:133]
	s_mov_b32 m0, s30
	s_nop 0
	global_load_lds_dwordx4 v[186:187], off
	v_lshl_add_u64 v[186:187], s[28:29], 0, v[136:137]
	s_add_i32 m0, s30, 0x2000
	s_nop 0
	global_load_lds_dwordx4 v[186:187], off
	v_lshl_add_u64 v[186:187], v[228:229], 0, s[12:13]
	s_mov_b32 m0, s34
	s_nop 0
	global_load_lds_dwordx4 v[186:187], off
	v_lshl_add_u64 v[186:187], v[230:231], 0, s[12:13]
	s_mov_b32 m0, s35
	s_nop 0
	global_load_lds_dwordx4 v[186:187], off
	s_waitcnt vmcnt(8)
	s_waitcnt lgkmcnt(0)
	s_barrier
	s_setprio 1
	s_waitcnt lgkmcnt(0)
	v_mfma_f32_16x16x32_bf16 v[62:65], v[148:151], v[194:197], v[62:65]
	v_mfma_f32_16x16x32_bf16 v[58:61], v[166:169], v[194:197], v[58:61]
	v_mfma_f32_16x16x32_bf16 v[46:49], v[148:151], v[202:205], v[46:49]
	v_mfma_f32_16x16x32_bf16 v[42:45], v[166:169], v[202:205], v[42:45]
	v_mfma_f32_16x16x32_bf16 v[30:33], v[148:151], v[210:213], v[30:33]
	v_mfma_f32_16x16x32_bf16 v[26:29], v[166:169], v[210:213], v[26:29]
	v_mfma_f32_16x16x32_bf16 v[14:17], v[148:151], v[218:221], v[14:17]
	v_mfma_f32_16x16x32_bf16 v[10:13], v[166:169], v[218:221], v[10:13]
	v_mfma_f32_16x16x32_bf16 v[62:65], v[152:155], v[198:201], v[62:65]
	v_mfma_f32_16x16x32_bf16 v[58:61], v[170:173], v[198:201], v[58:61]
	v_mfma_f32_16x16x32_bf16 v[46:49], v[152:155], v[206:209], v[46:49]
	v_mfma_f32_16x16x32_bf16 v[42:45], v[170:173], v[206:209], v[42:45]
	v_mfma_f32_16x16x32_bf16 v[30:33], v[152:155], v[214:217], v[30:33]
	v_mfma_f32_16x16x32_bf16 v[26:29], v[170:173], v[214:217], v[26:29]
	v_mfma_f32_16x16x32_bf16 v[14:17], v[152:155], v[222:225], v[14:17]
	v_mfma_f32_16x16x32_bf16 v[10:13], v[170:173], v[222:225], v[10:13]
	v_mfma_f32_16x16x32_bf16 v[54:57], v[174:177], v[194:197], v[54:57]
	v_mfma_f32_16x16x32_bf16 v[50:53], v[182:185], v[194:197], v[50:53]
	v_mfma_f32_16x16x32_bf16 v[38:41], v[174:177], v[202:205], v[38:41]
	v_mfma_f32_16x16x32_bf16 v[34:37], v[182:185], v[202:205], v[34:37]
	v_mfma_f32_16x16x32_bf16 v[22:25], v[174:177], v[210:213], v[22:25]
	v_mfma_f32_16x16x32_bf16 v[18:21], v[182:185], v[210:213], v[18:21]
	v_mfma_f32_16x16x32_bf16 v[6:9], v[174:177], v[218:221], v[6:9]
	v_mfma_f32_16x16x32_bf16 v[2:5], v[182:185], v[218:221], v[2:5]
	v_mfma_f32_16x16x32_bf16 v[54:57], v[178:181], v[198:201], v[54:57]
	v_mfma_f32_16x16x32_bf16 v[50:53], v[190:193], v[198:201], v[50:53]
	v_mfma_f32_16x16x32_bf16 v[38:41], v[178:181], v[206:209], v[38:41]
	v_mfma_f32_16x16x32_bf16 v[34:37], v[190:193], v[206:209], v[34:37]
	v_mfma_f32_16x16x32_bf16 v[22:25], v[178:181], v[214:217], v[22:25]
	v_mfma_f32_16x16x32_bf16 v[18:21], v[190:193], v[214:217], v[18:21]
	v_mfma_f32_16x16x32_bf16 v[6:9], v[178:181], v[222:225], v[6:9]
	v_mfma_f32_16x16x32_bf16 v[2:5], v[190:193], v[222:225], v[2:5]
	s_setprio 0
	s_barrier
	s_add_i32 s42, s42, 2
	s_add_u32 s26, s26, 0x100
	s_addc_u32 s27, s27, 0
	s_add_u32 s40, s40, 0x100
	s_addc_u32 s41, s41, 0
	s_cmp_gt_u32 s42, 29
	s_cbranch_scc0 .LBB0_1350
	s_and_b64 vcc, exec, s[14:15]
	s_cbranch_vccz .LBB0_1353
	s_barrier

; #define PG8_STAGE(bufoff, gbase, voff) do { _Pragma("unroll") for (int _i = 0; _i < 2; ++_i) \
;         __builtin_amdgcn_global_load_lds((const unsigned*)((const char*)(gbase) + (voff)[_i]), (PG8_LAS unsigned*)(lds + (bufoff) + ldsw + _i * 8192), 16, 0, 0); } while (0)
; #define PG8_LDA(dst, b, h) do { _Pragma("unroll") for (int m = 0; m < 4; ++m) _Pragma("unroll") for (int k = 0; k < 2; ++k) dst[m][k] = *(const PG8_LAS bf16x8*)(lds + PG8_SA(b, h) + aoff + m * 2048 + k * 1024); } while (0)
; #define PG8_LDB(dst, b, h) do { _Pragma("unroll") for (int n = 0; n < 2; ++n) _Pragma("unroll") for (int k = 0; k < 2; ++k) dst[n][k] = *(const PG8_LAS bf16x8*)(lds + PG8_SB(b, h) + boff + n * 2048 + k * 1024); } while (0)
; #define PG8_WAIT_V(n) asm volatile("s_waitcnt vmcnt(" #n ")" ::: "memory")
; #define PG8_WAIT_L(n) asm volatile("s_waitcnt lgkmcnt(" #n ")" ::: "memory")
; #define PG8_BAR __builtin_amdgcn_s_barrier()
; #define PG8_SCHED __builtin_amdgcn_sched_barrier(0)
; template <class Epi, class Sched, bool ALIGN_EPI = false, bool SP2 = false>
; __device__ __forceinline__ void gemm_phase(PG8_LAS unsigned char* lds, const Gemm g, const Sched& S, const Epi& E) {
;     ...
;         const char* nA = has_next ? (const char*)g.A + (size_t)nxt.pm * tstep + (size_t)nxt.k0 * 2 : cA; const char* nB = has_next ? (const char*)g.Bt + (size_t)nxt.pn * tstep + (size_t)nxt.k0 * 2 : cB;
;         for (int t = 0; t < nt; t += 2) {
;             const bool last = (t == nt - 2);
;             const char* a1 = cA + (size_t)(t + 1) * kstep;
;             const char* a2 = last ? nA : cA + (size_t)(t + 2) * kstep; const char* b2 = last ? nB : cB + (size_t)(t + 2) * kstep;
;             const char* a3 = a2 + kstep; const char* b3 = b2 + kstep;
;             if (last && has_next) S.a_ready(nxt);
;             if constexpr (SP2) {
;             PG8_LDB(B0, 0, 0); PG8_LDB(B1, 0, 1); PG8_SCHED; PG8_LDA(At, 0, 0); PG8_STAGE(PG8_SA(1, 1), a1 + hstep, voffA);
;             PG8_WAIT_V(8); PG8_WAIT_L(0); PG8_BAR; PG8_MMA(0, 0, At, B0); PG8_MMA(0, 1, At, B1); PG8_BAR; PG8_SCHED;
;             PG8_LDA(At, 0, 1); PG8_STAGE(PG8_SB(0, 0), b2, voffB); PG8_STAGE(PG8_SB(0, 1), b2 + hstep, voffB); PG8_STAGE(PG8_SA(0, 0), a2, voffA);
;             PG8_WAIT_V(8); PG8_WAIT_L(0); PG8_BAR; PG8_MMA(1, 0, At, B0); PG8_MMA(1, 1, At, B1); PG8_BAR; PG8_SCHED;
.LBB0_1828:
	ds_read_b128 v[144:147], v155
	ds_read_b128 v[148:151], v155 offset:1024
	ds_read_b128 v[166:169], v155 offset:2048
	ds_read_b128 v[170:173], v155 offset:3072
	ds_read_b128 v[174:177], v156
	ds_read_b128 v[178:181], v156 offset:1024
	ds_read_b128 v[182:185], v156 offset:2048
	ds_read_b128 v[190:193], v156 offset:3072
	s_add_u32 s28, s4, 0x100
	s_addc_u32 s29, s5, 0
	s_cmp_eq_u32 s47, 28
	s_cselect_b32 s35, s19, s29
	s_cselect_b32 s34, s43, s28
	s_cselect_b32 s31, s17, s46
	s_cselect_b32 s30, s44, s45
	v_lshl_add_u64 v[160:161], s[4:5], 0, v[136:137]
	s_add_i32 m0, s3, 0xc000
	ds_read_b128 v[194:197], v157
	ds_read_b128 v[198:201], v157 offset:1024
	ds_read_b128 v[202:205], v157 offset:2048
	ds_read_b128 v[206:209], v157 offset:3072
	ds_read_b128 v[210:213], v157 offset:4096
	ds_read_b128 v[214:217], v157 offset:5120
	ds_read_b128 v[218:221], v157 offset:6144
	ds_read_b128 v[222:225], v157 offset:7168
	global_load_lds_dwordx4 v[160:161], off
	v_lshl_add_u64 v[160:161], s[4:5], 0, v[138:139]
	s_add_i32 m0, s3, 0xe000
	s_nop 0
	global_load_lds_dwordx4 v[160:161], off
	s_waitcnt vmcnt(8)
	s_waitcnt lgkmcnt(0)
	s_barrier
	s_setprio 1
	s_waitcnt lgkmcnt(0)
	v_mfma_f32_16x16x32_bf16 v[126:129], v[144:147], v[194:197], v[126:129]
	v_mfma_f32_16x16x32_bf16 v[122:125], v[166:169], v[194:197], v[122:125]
	v_mfma_f32_16x16x32_bf16 v[110:113], v[144:147], v[202:205], v[110:113]
	v_mfma_f32_16x16x32_bf16 v[106:109], v[166:169], v[202:205], v[106:109]
	v_mfma_f32_16x16x32_bf16 v[94:97], v[144:147], v[210:213], v[94:97]
	v_mfma_f32_16x16x32_bf16 v[90:93], v[166:169], v[210:213], v[90:93]
	v_mfma_f32_16x16x32_bf16 v[78:81], v[144:147], v[218:221], v[78:81]
	v_mfma_f32_16x16x32_bf16 v[74:77], v[166:169], v[218:221], v[74:77]
	v_mfma_f32_16x16x32_bf16 v[126:129], v[148:151], v[198:201], v[126:129]
	v_mfma_f32_16x16x32_bf16 v[122:125], v[170:173], v[198:201], v[122:125]
	v_mfma_f32_16x16x32_bf16 v[110:113], v[148:151], v[206:209], v[110:113]
	v_mfma_f32_16x16x32_bf16 v[106:109], v[170:173], v[206:209], v[106:109]
	v_mfma_f32_16x16x32_bf16 v[94:97], v[148:151], v[214:217], v[94:97]
	v_mfma_f32_16x16x32_bf16 v[90:93], v[170:173], v[214:217], v[90:93]
	v_mfma_f32_16x16x32_bf16 v[78:81], v[148:151], v[222:225], v[78:81]
	v_mfma_f32_16x16x32_bf16 v[74:77], v[170:173], v[222:225], v[74:77]
	v_mfma_f32_16x16x32_bf16 v[118:121], v[174:177], v[194:197], v[118:121]
	v_mfma_f32_16x16x32_bf16 v[114:117], v[182:185], v[194:197], v[114:117]
	v_mfma_f32_16x16x32_bf16 v[102:105], v[174:177], v[202:205], v[102:105]
	v_mfma_f32_16x16x32_bf16 v[98:101], v[182:185], v[202:205], v[98:101]
	v_mfma_f32_16x16x32_bf16 v[86:89], v[174:177], v[210:213], v[86:89]
	v_mfma_f32_16x16x32_bf16 v[82:85], v[182:185], v[210:213], v[82:85]
	v_mfma_f32_16x16x32_bf16 v[70:73], v[174:177], v[218:221], v[70:73]
	v_mfma_f32_16x16x32_bf16 v[66:69], v[182:185], v[218:221], v[66:69]
	v_mfma_f32_16x16x32_bf16 v[118:121], v[178:181], v[198:201], v[118:121]
	v_mfma_f32_16x16x32_bf16 v[114:117], v[190:193], v[198:201], v[114:117]
	v_mfma_f32_16x16x32_bf16 v[102:105], v[178:181], v[206:209], v[102:105]
	v_mfma_f32_16x16x32_bf16 v[98:101], v[190:193], v[206:209], v[98:101]
	v_mfma_f32_16x16x32_bf16 v[86:89], v[178:181], v[214:217], v[86:89]
	v_mfma_f32_16x16x32_bf16 v[82:85], v[190:193], v[214:217], v[82:85]
	v_mfma_f32_16x16x32_bf16 v[70:73], v[178:181], v[222:225], v[70:73]
	v_mfma_f32_16x16x32_bf16 v[66:69], v[190:193], v[222:225], v[66:69]
	s_setprio 0
	s_barrier
	s_add_i32 s4, s40, s2
	v_lshl_add_u64 v[160:161], s[30:31], 0, v[130:131]
	s_mov_b32 m0, s4
	ds_read_b128 v[194:197], v157 offset:16384
	ds_read_b128 v[198:201], v157 offset:17408
	ds_read_b128 v[202:205], v157 offset:18432
	ds_read_b128 v[206:209], v157 offset:19456
	ds_read_b128 v[210:213], v157 offset:20480
	ds_read_b128 v[214:217], v157 offset:21504
	ds_read_b128 v[218:221], v157 offset:22528
	ds_read_b128 v[222:225], v157 offset:23552
	global_load_lds_dwordx4 v[160:161], off
	s_add_i32 m0, s4, 0x2000
	s_add_u32 s4, s30, 0x80000
	v_lshl_add_u64 v[186:187], s[30:31], 0, v[132:133]
	s_addc_u32 s5, s31, 0
	s_add_i32 s48, s41, s2
	global_load_lds_dwordx4 v[186:187], off
	v_lshl_add_u64 v[226:227], s[4:5], 0, v[130:131]
	s_mov_b32 m0, s48
	v_lshl_add_u64 v[228:229], s[34:35], 0, v[132:133]
	global_load_lds_dwordx4 v[226:227], off
	v_lshl_add_u64 v[226:227], s[4:5], 0, v[132:133]
	s_add_i32 m0, s48, 0x2000
	s_nop 0
	global_load_lds_dwordx4 v[226:227], off
	v_lshl_add_u64 v[226:227], s[34:35], 0, v[130:131]
	s_mov_b32 m0, s3
	s_nop 0
	global_load_lds_dwordx4 v[226:227], off
	s_mov_b32 m0, s25
	s_nop 0
	global_load_lds_dwordx4 v[228:229], off
	s_waitcnt vmcnt(8)
	s_waitcnt lgkmcnt(0)
	s_barrier
; #define PG8_STAGE(bufoff, gbase, voff) do { _Pragma("unroll") for (int _i = 0; _i < 2; ++_i) \
;         __builtin_amdgcn_global_load_lds((const unsigned*)((const char*)(gbase) + (voff)[_i]), (PG8_LAS unsigned*)(lds + (bufoff) + ldsw + _i * 8192), 16, 0, 0); } while (0)
; #define PG8_LDA(dst, b, h) do { _Pragma("unroll") for (int m = 0; m < 4; ++m) _Pragma("unroll") for (int k = 0; k < 2; ++k) dst[m][k] = *(const PG8_LAS bf16x8*)(lds + PG8_SA(b, h) + aoff + m * 2048 + k * 1024); } while (0)
; #define PG8_LDB(dst, b, h) do { _Pragma("unroll") for (int n = 0; n < 2; ++n) _Pragma("unroll") for (int k = 0; k < 2; ++k) dst[n][k] = *(const PG8_LAS bf16x8*)(lds + PG8_SB(b, h) + boff + n * 2048 + k * 1024); } while (0)
; #define PG8_MMA(ai, bj, At, Bt) do { __builtin_amdgcn_s_setprio(1); _Pragma("unroll") for (int m = 0; m < 4; ++m) _Pragma("unroll") for (int n = 0; n < 2; ++n) _Pragma("unroll") for (int k = 0; k < 2; ++k) \
;         acc[ai][bj][m][n] = __builtin_amdgcn_mfma_f32_16x16x32_bf16(Bt[n][k], At[m][k], acc[ai][bj][m][n], 0, 0, 0); __builtin_amdgcn_s_setprio(0); } while (0)
; #define PG8_WAIT_V(n) asm volatile("s_waitcnt vmcnt(" #n ")" ::: "memory")
; #define PG8_WAIT_L(n) asm volatile("s_waitcnt lgkmcnt(" #n ")" ::: "memory")
; #define PG8_BAR __builtin_amdgcn_s_barrier()
; #define PG8_SCHED __builtin_amdgcn_sched_barrier(0)
; template <class Epi, class Sched, bool ALIGN_EPI = false, bool SP2 = false>
; __device__ __forceinline__ void gemm_phase(PG8_LAS unsigned char* lds, const Gemm g, const Sched& S, const Epi& E) {
;     ...
;             PG8_WAIT_V(8); PG8_WAIT_L(0); PG8_BAR; PG8_MMA(0, 0, At, B0); PG8_MMA(0, 1, At, B1); PG8_BAR; PG8_SCHED;
;             PG8_LDA(At, 0, 1); PG8_STAGE(PG8_SB(0, 0), b2, voffB); PG8_STAGE(PG8_SB(0, 1), b2 + hstep, voffB); PG8_STAGE(PG8_SA(0, 0), a2, voffA);
;             PG8_WAIT_V(8); PG8_WAIT_L(0); PG8_BAR; PG8_MMA(1, 0, At, B0); PG8_MMA(1, 1, At, B1); PG8_BAR; PG8_SCHED;
;             PG8_LDB(B0, 1, 0); PG8_LDB(B1, 1, 1); PG8_SCHED; PG8_LDA(At, 1, 0); PG8_STAGE(PG8_SA(0, 1), a2 + hstep, voffA);
;             PG8_WAIT_V(8); PG8_WAIT_L(0); PG8_BAR; PG8_MMA(0, 0, At, B0); PG8_MMA(0, 1, At, B1); PG8_BAR; PG8_SCHED;
	s_setprio 1
	s_waitcnt lgkmcnt(0)
	v_mfma_f32_16x16x32_bf16 v[62:65], v[144:147], v[194:197], v[62:65]
	v_mfma_f32_16x16x32_bf16 v[58:61], v[166:169], v[194:197], v[58:61]
	v_mfma_f32_16x16x32_bf16 v[46:49], v[144:147], v[202:205], v[46:49]
	v_mfma_f32_16x16x32_bf16 v[42:45], v[166:169], v[202:205], v[42:45]
	v_mfma_f32_16x16x32_bf16 v[30:33], v[144:147], v[210:213], v[30:33]
	v_mfma_f32_16x16x32_bf16 v[26:29], v[166:169], v[210:213], v[26:29]
	v_mfma_f32_16x16x32_bf16 v[14:17], v[144:147], v[218:221], v[14:17]
	v_mfma_f32_16x16x32_bf16 v[10:13], v[166:169], v[218:221], v[10:13]
	v_mfma_f32_16x16x32_bf16 v[62:65], v[148:151], v[198:201], v[62:65]
	v_mfma_f32_16x16x32_bf16 v[58:61], v[170:173], v[198:201], v[58:61]
	v_mfma_f32_16x16x32_bf16 v[46:49], v[148:151], v[206:209], v[46:49]
	v_mfma_f32_16x16x32_bf16 v[42:45], v[170:173], v[206:209], v[42:45]
	v_mfma_f32_16x16x32_bf16 v[30:33], v[148:151], v[214:217], v[30:33]
	v_mfma_f32_16x16x32_bf16 v[26:29], v[170:173], v[214:217], v[26:29]
	v_mfma_f32_16x16x32_bf16 v[14:17], v[148:151], v[222:225], v[14:17]
	v_mfma_f32_16x16x32_bf16 v[10:13], v[170:173], v[222:225], v[10:13]
	v_mfma_f32_16x16x32_bf16 v[54:57], v[174:177], v[194:197], v[54:57]
	v_mfma_f32_16x16x32_bf16 v[50:53], v[182:185], v[194:197], v[50:53]
	v_mfma_f32_16x16x32_bf16 v[38:41], v[174:177], v[202:205], v[38:41]
	v_mfma_f32_16x16x32_bf16 v[34:37], v[182:185], v[202:205], v[34:37]
	v_mfma_f32_16x16x32_bf16 v[22:25], v[174:177], v[210:213], v[22:25]
	v_mfma_f32_16x16x32_bf16 v[18:21], v[182:185], v[210:213], v[18:21]
	v_mfma_f32_16x16x32_bf16 v[6:9], v[174:177], v[218:221], v[6:9]
	v_mfma_f32_16x16x32_bf16 v[2:5], v[182:185], v[218:221], v[2:5]
	v_mfma_f32_16x16x32_bf16 v[54:57], v[178:181], v[198:201], v[54:57]
	v_mfma_f32_16x16x32_bf16 v[50:53], v[190:193], v[198:201], v[50:53]
	v_mfma_f32_16x16x32_bf16 v[38:41], v[178:181], v[206:209], v[38:41]
	v_mfma_f32_16x16x32_bf16 v[34:37], v[190:193], v[206:209], v[34:37]
	v_mfma_f32_16x16x32_bf16 v[22:25], v[178:181], v[214:217], v[22:25]
	v_mfma_f32_16x16x32_bf16 v[18:21], v[190:193], v[214:217], v[18:21]
	v_mfma_f32_16x16x32_bf16 v[6:9], v[178:181], v[222:225], v[6:9]
	v_mfma_f32_16x16x32_bf16 v[2:5], v[190:193], v[222:225], v[2:5]
	s_setprio 0
	s_barrier
	s_add_i32 s48, 0, 0x18000
	v_add_u32_e32 v134, s48, v153
	s_add_i32 s49, 0, 0x1c000
	ds_read_b128 v[144:147], v134
	ds_read_b128 v[148:151], v134 offset:1024
	ds_read_b128 v[166:169], v134 offset:2048
	ds_read_b128 v[170:173], v134 offset:3072
	v_add_u32_e32 v134, s49, v153
	ds_read_b128 v[174:177], v134
	ds_read_b128 v[178:181], v134 offset:1024
	ds_read_b128 v[182:185], v134 offset:2048
	ds_read_b128 v[190:193], v134 offset:3072
	s_add_u32 s4, s34, 0x80000
	s_addc_u32 s5, s35, 0
	s_mov_b32 m0, s27
	v_lshl_add_u64 v[230:231], s[4:5], 0, v[130:131]
	ds_read_b128 v[194:197], v157 offset:32768
	ds_read_b128 v[198:201], v157 offset:33792
	ds_read_b128 v[202:205], v157 offset:34816
	ds_read_b128 v[206:209], v157 offset:35840
	ds_read_b128 v[210:213], v157 offset:36864
	ds_read_b128 v[214:217], v157 offset:37888
	ds_read_b128 v[218:221], v157 offset:38912
	ds_read_b128 v[222:225], v157 offset:39936
	global_load_lds_dwordx4 v[230:231], off
	v_lshl_add_u64 v[230:231], s[4:5], 0, v[132:133]
	s_mov_b32 m0, s33
	s_nop 0
	global_load_lds_dwordx4 v[230:231], off
	s_waitcnt vmcnt(8)
	s_waitcnt lgkmcnt(0)
	s_barrier
	s_setprio 1
	s_waitcnt lgkmcnt(0)
	v_mfma_f32_16x16x32_bf16 v[126:129], v[144:147], v[194:197], v[126:129]
	v_mfma_f32_16x16x32_bf16 v[122:125], v[166:169], v[194:197], v[122:125]
	v_mfma_f32_16x16x32_bf16 v[110:113], v[144:147], v[202:205], v[110:113]
	v_mfma_f32_16x16x32_bf16 v[106:109], v[166:169], v[202:205], v[106:109]
	v_mfma_f32_16x16x32_bf16 v[94:97], v[144:147], v[210:213], v[94:97]
	v_mfma_f32_16x16x32_bf16 v[90:93], v[166:169], v[210:213], v[90:93]
	v_mfma_f32_16x16x32_bf16 v[78:81], v[144:147], v[218:221], v[78:81]
	v_mfma_f32_16x16x32_bf16 v[74:77], v[166:169], v[218:221], v[74:77]
	v_mfma_f32_16x16x32_bf16 v[126:129], v[148:151], v[198:201], v[126:129]
	v_mfma_f32_16x16x32_bf16 v[122:125], v[170:173], v[198:201], v[122:125]
	v_mfma_f32_16x16x32_bf16 v[110:113], v[148:151], v[206:209], v[110:113]
	v_mfma_f32_16x16x32_bf16 v[106:109], v[170:173], v[206:209], v[106:109]
	v_mfma_f32_16x16x32_bf16 v[94:97], v[148:151], v[214:217], v[94:97]
	v_mfma_f32_16x16x32_bf16 v[90:93], v[170:173], v[214:217], v[90:93]
	v_mfma_f32_16x16x32_bf16 v[78:81], v[148:151], v[222:225], v[78:81]
	v_mfma_f32_16x16x32_bf16 v[74:77], v[170:173], v[222:225], v[74:77]
	v_mfma_f32_16x16x32_bf16 v[118:121], v[174:177], v[194:197], v[118:121]
	v_mfma_f32_16x16x32_bf16 v[114:117], v[182:185], v[194:197], v[114:117]
	v_mfma_f32_16x16x32_bf16 v[102:105], v[174:177], v[202:205], v[102:105]
	v_mfma_f32_16x16x32_bf16 v[98:101], v[182:185], v[202:205], v[98:101]
	v_mfma_f32_16x16x32_bf16 v[86:89], v[174:177], v[210:213], v[86:89]
	v_mfma_f32_16x16x32_bf16 v[82:85], v[182:185], v[210:213], v[82:85]
	v_mfma_f32_16x16x32_bf16 v[70:73], v[174:177], v[218:221], v[70:73]
	v_mfma_f32_16x16x32_bf16 v[66:69], v[182:185], v[218:221], v[66:69]
	v_mfma_f32_16x16x32_bf16 v[118:121], v[178:181], v[198:201], v[118:121]
	v_mfma_f32_16x16x32_bf16 v[114:117], v[190:193], v[198:201], v[114:117]
	v_mfma_f32_16x16x32_bf16 v[102:105], v[178:181], v[206:209], v[102:105]
	v_mfma_f32_16x16x32_bf16 v[98:101], v[190:193], v[206:209], v[98:101]
	v_mfma_f32_16x16x32_bf16 v[86:89], v[178:181], v[214:217], v[86:89]
	v_mfma_f32_16x16x32_bf16 v[82:85], v[190:193], v[214:217], v[82:85]
	v_mfma_f32_16x16x32_bf16 v[70:73], v[178:181], v[222:225], v[70:73]
	v_mfma_f32_16x16x32_bf16 v[66:69], v[190:193], v[222:225], v[66:69]
	s_setprio 0
	s_barrier
; #define PG8_STAGE(bufoff, gbase, voff) do { _Pragma("unroll") for (int _i = 0; _i < 2; ++_i) \
;         __builtin_amdgcn_global_load_lds((const unsigned*)((const char*)(gbase) + (voff)[_i]), (PG8_LAS unsigned*)(lds + (bufoff) + ldsw + _i * 8192), 16, 0, 0); } while (0)
; #define PG8_LDA(dst, b, h) do { _Pragma("unroll") for (int m = 0; m < 4; ++m) _Pragma("unroll") for (int k = 0; k < 2; ++k) dst[m][k] = *(const PG8_LAS bf16x8*)(lds + PG8_SA(b, h) + aoff + m * 2048 + k * 1024); } while (0)
; #define PG8_LDB(dst, b, h) do { _Pragma("unroll") for (int n = 0; n < 2; ++n) _Pragma("unroll") for (int k = 0; k < 2; ++k) dst[n][k] = *(const PG8_LAS bf16x8*)(lds + PG8_SB(b, h) + boff + n * 2048 + k * 1024); } while (0)
; #define PG8_WAIT_V(n) asm volatile("s_waitcnt vmcnt(" #n ")" ::: "memory")
; #define PG8_WAIT_L(n) asm volatile("s_waitcnt lgkmcnt(" #n ")" ::: "memory")
; #define PG8_BAR __builtin_amdgcn_s_barrier()
; #define PG8_SCHED __builtin_amdgcn_sched_barrier(0)
; template <class Epi, class Sched, bool ALIGN_EPI = false, bool SP2 = false>
; __device__ __forceinline__ void gemm_phase(PG8_LAS unsigned char* lds, const Gemm g, const Sched& S, const Epi& E) {
;     ...
;             PG8_LDA(At, 1, 1); PG8_STAGE(PG8_SB(1, 0), b3, voffB); PG8_STAGE(PG8_SB(1, 1), b3 + hstep, voffB); PG8_STAGE(PG8_SA(1, 0), a3, voffA);
;             PG8_WAIT_V(8); PG8_WAIT_L(0); PG8_BAR; PG8_MMA(1, 0, At, B0); PG8_MMA(1, 1, At, B1); PG8_BAR; PG8_SCHED;
;             } else {
;             PG8_LDB(B0, 0, 0); PG8_SCHED; PG8_LDA(At, 0, 0); PG8_STAGE(PG8_SA(1, 1), a1 + hstep, voffA);
;             PG8_WAIT_L(8); PG8_BAR; PG8_WAIT_L(0); PG8_MMA(0, 0, At, B0); PG8_BAR; PG8_SCHED;
;             PG8_LDB(B1, 0, 1); PG8_STAGE(PG8_SB(0, 0), b2, voffB);
;             PG8_BAR; PG8_WAIT_L(0); PG8_MMA(0, 1, At, B1); PG8_BAR;
;             PG8_LDA(At, 0, 1); PG8_STAGE(PG8_SA(0, 0), a2, voffA);
;             PG8_BAR; PG8_WAIT_L(0); PG8_MMA(1, 0, At, B0); PG8_BAR; PG8_SCHED;
;             PG8_STAGE(PG8_SB(0, 1), b2 + hstep, voffB);
;             PG8_WAIT_V(6); PG8_BAR; PG8_MMA(1, 1, At, B1); PG8_BAR;
;             PG8_LDB(B0, 1, 0); PG8_SCHED; PG8_LDA(At, 1, 0); PG8_STAGE(PG8_SA(0, 1), a2 + hstep, voffA);
;             PG8_WAIT_L(8); PG8_BAR; PG8_WAIT_L(0); PG8_MMA(0, 0, At, B0); PG8_BAR; PG8_SCHED;
	s_add_i32 s4, s48, s2
	v_lshl_add_u64 v[160:161], v[160:161], 0, s[12:13]
	s_mov_b32 m0, s4
	ds_read_b128 v[194:197], v157 offset:49152
	ds_read_b128 v[198:201], v157 offset:50176
	ds_read_b128 v[202:205], v157 offset:51200
	ds_read_b128 v[206:209], v157 offset:52224
	ds_read_b128 v[210:213], v157 offset:53248
	ds_read_b128 v[214:217], v157 offset:54272
	ds_read_b128 v[218:221], v157 offset:55296
	ds_read_b128 v[222:225], v157 offset:56320
	global_load_lds_dwordx4 v[160:161], off
	s_add_i32 m0, s4, 0x2000
	s_add_u32 s4, s30, 0x80080
	v_lshl_add_u64 v[160:161], v[186:187], 0, s[12:13]
	s_addc_u32 s5, s31, 0
	s_add_i32 s30, s49, s2
	global_load_lds_dwordx4 v[160:161], off
	v_lshl_add_u64 v[160:161], s[4:5], 0, v[130:131]
	s_mov_b32 m0, s30
	s_nop 0
	global_load_lds_dwordx4 v[160:161], off
	v_lshl_add_u64 v[160:161], s[4:5], 0, v[132:133]
	s_add_i32 m0, s30, 0x2000
	s_nop 0
	global_load_lds_dwordx4 v[160:161], off
	v_lshl_add_u64 v[160:161], v[226:227], 0, s[12:13]
	s_mov_b32 m0, s38
	s_nop 0
	global_load_lds_dwordx4 v[160:161], off
	v_lshl_add_u64 v[160:161], v[228:229], 0, s[12:13]
	s_mov_b32 m0, s39
	s_nop 0
	global_load_lds_dwordx4 v[160:161], off
	s_waitcnt vmcnt(8)
	s_waitcnt lgkmcnt(0)
	s_barrier
	s_setprio 1
	s_waitcnt lgkmcnt(0)
	v_mfma_f32_16x16x32_bf16 v[62:65], v[144:147], v[194:197], v[62:65]
	v_mfma_f32_16x16x32_bf16 v[58:61], v[166:169], v[194:197], v[58:61]
	v_mfma_f32_16x16x32_bf16 v[46:49], v[144:147], v[202:205], v[46:49]
	v_mfma_f32_16x16x32_bf16 v[42:45], v[166:169], v[202:205], v[42:45]
	v_mfma_f32_16x16x32_bf16 v[30:33], v[144:147], v[210:213], v[30:33]
	v_mfma_f32_16x16x32_bf16 v[26:29], v[166:169], v[210:213], v[26:29]
	v_mfma_f32_16x16x32_bf16 v[14:17], v[144:147], v[218:221], v[14:17]
	v_mfma_f32_16x16x32_bf16 v[10:13], v[166:169], v[218:221], v[10:13]
	v_mfma_f32_16x16x32_bf16 v[62:65], v[148:151], v[198:201], v[62:65]
	v_mfma_f32_16x16x32_bf16 v[58:61], v[170:173], v[198:201], v[58:61]
	v_mfma_f32_16x16x32_bf16 v[46:49], v[148:151], v[206:209], v[46:49]
	v_mfma_f32_16x16x32_bf16 v[42:45], v[170:173], v[206:209], v[42:45]
	v_mfma_f32_16x16x32_bf16 v[30:33], v[148:151], v[214:217], v[30:33]
	v_mfma_f32_16x16x32_bf16 v[26:29], v[170:173], v[214:217], v[26:29]
	v_mfma_f32_16x16x32_bf16 v[14:17], v[148:151], v[222:225], v[14:17]
	v_mfma_f32_16x16x32_bf16 v[10:13], v[170:173], v[222:225], v[10:13]
	v_mfma_f32_16x16x32_bf16 v[54:57], v[174:177], v[194:197], v[54:57]
	v_mfma_f32_16x16x32_bf16 v[50:53], v[182:185], v[194:197], v[50:53]
	v_mfma_f32_16x16x32_bf16 v[38:41], v[174:177], v[202:205], v[38:41]
	v_mfma_f32_16x16x32_bf16 v[34:37], v[182:185], v[202:205], v[34:37]
	v_mfma_f32_16x16x32_bf16 v[22:25], v[174:177], v[210:213], v[22:25]
	v_mfma_f32_16x16x32_bf16 v[18:21], v[182:185], v[210:213], v[18:21]
	v_mfma_f32_16x16x32_bf16 v[6:9], v[174:177], v[218:221], v[6:9]
	v_mfma_f32_16x16x32_bf16 v[2:5], v[182:185], v[218:221], v[2:5]
	v_mfma_f32_16x16x32_bf16 v[54:57], v[178:181], v[198:201], v[54:57]
	v_mfma_f32_16x16x32_bf16 v[50:53], v[190:193], v[198:201], v[50:53]
	v_mfma_f32_16x16x32_bf16 v[38:41], v[178:181], v[206:209], v[38:41]
	v_mfma_f32_16x16x32_bf16 v[34:37], v[190:193], v[206:209], v[34:37]
	v_mfma_f32_16x16x32_bf16 v[22:25], v[178:181], v[214:217], v[22:25]
	v_mfma_f32_16x16x32_bf16 v[18:21], v[190:193], v[214:217], v[18:21]
	v_mfma_f32_16x16x32_bf16 v[6:9], v[178:181], v[222:225], v[6:9]
	v_mfma_f32_16x16x32_bf16 v[2:5], v[190:193], v[222:225], v[2:5]
	s_setprio 0
	s_barrier
	s_add_i32 s47, s47, 2
	s_add_u32 s45, s45, 0x100
	s_addc_u32 s46, s46, 0
	s_cmp_gt_u32 s47, 29
	s_mov_b64 s[4:5], s[28:29]
	s_cbranch_scc0 .LBB0_1828
	s_and_b64 vcc, exec, s[14:15]
	s_cbranch_vccz .LBB0_1831
	s_barrier

; #define PG8_STAGE(bufoff, gbase, voff) do { _Pragma("unroll") for (int _i = 0; _i < 2; ++_i) \
;         __builtin_amdgcn_global_load_lds((const unsigned*)((const char*)(gbase) + (voff)[_i]), (PG8_LAS unsigned*)(lds + (bufoff) + ldsw + _i * 8192), 16, 0, 0); } while (0)
; #define PG8_LDA(dst, b, h) do { _Pragma("unroll") for (int m = 0; m < 4; ++m) _Pragma("unroll") for (int k = 0; k < 2; ++k) dst[m][k] = *(const PG8_LAS bf16x8*)(lds + PG8_SA(b, h) + aoff + m * 2048 + k * 1024); } while (0)
; #define PG8_LDB(dst, b, h) do { _Pragma("unroll") for (int n = 0; n < 2; ++n) _Pragma("unroll") for (int k = 0; k < 2; ++k) dst[n][k] = *(const PG8_LAS bf16x8*)(lds + PG8_SB(b, h) + boff + n * 2048 + k * 1024); } while (0)
; #define PG8_WAIT_V(n) asm volatile("s_waitcnt vmcnt(" #n ")" ::: "memory")
; #define PG8_WAIT_L(n) asm volatile("s_waitcnt lgkmcnt(" #n ")" ::: "memory")
; #define PG8_BAR __builtin_amdgcn_s_barrier()
; #define PG8_SCHED __builtin_amdgcn_sched_barrier(0)
; template <class Epi, class Sched, bool ALIGN_EPI = false, bool SP2 = false>
; __device__ __forceinline__ void gemm_phase(PG8_LAS unsigned char* lds, const Gemm g, const Sched& S, const Epi& E) {
;     ...
;         const char* nA = has_next ? (const char*)g.A + (size_t)nxt.pm * tstep + (size_t)nxt.k0 * 2 : cA; const char* nB = has_next ? (const char*)g.Bt + (size_t)nxt.pn * tstep + (size_t)nxt.k0 * 2 : cB;
;         for (int t = 0; t < nt; t += 2) {
;             const bool last = (t == nt - 2);
;             const char* a1 = cA + (size_t)(t + 1) * kstep;
;             const char* a2 = last ? nA : cA + (size_t)(t + 2) * kstep; const char* b2 = last ? nB : cB + (size_t)(t + 2) * kstep;
;             const char* a3 = a2 + kstep; const char* b3 = b2 + kstep;
;             if (last && has_next) S.a_ready(nxt);
;             if constexpr (SP2) {
;             PG8_LDB(B0, 0, 0); PG8_LDB(B1, 0, 1); PG8_SCHED; PG8_LDA(At, 0, 0); PG8_STAGE(PG8_SA(1, 1), a1 + hstep, voffA);
;             PG8_WAIT_V(8); PG8_WAIT_L(0); PG8_BAR; PG8_MMA(0, 0, At, B0); PG8_MMA(0, 1, At, B1); PG8_BAR; PG8_SCHED;
;             PG8_LDA(At, 0, 1); PG8_STAGE(PG8_SB(0, 0), b2, voffB); PG8_STAGE(PG8_SB(0, 1), b2 + hstep, voffB); PG8_STAGE(PG8_SA(0, 0), a2, voffA);
;             PG8_WAIT_V(8); PG8_WAIT_L(0); PG8_BAR; PG8_MMA(1, 0, At, B0); PG8_MMA(1, 1, At, B1); PG8_BAR; PG8_SCHED;
.LBB0_2172:
	ds_read_b128 v[144:147], v150
	ds_read_b128 v[154:157], v150 offset:1024
	ds_read_b128 v[158:161], v150 offset:2048
	ds_read_b128 v[162:165], v150 offset:3072
	ds_read_b128 v[166:169], v151
	ds_read_b128 v[170:173], v151 offset:1024
	ds_read_b128 v[174:177], v151 offset:2048
	ds_read_b128 v[178:181], v151 offset:3072
	s_add_u32 s24, s22, 0xfff80080
	s_addc_u32 s25, s23, -1
	s_cmp_eq_u32 s45, 28
	s_cselect_b32 s27, s11, s25
	s_cselect_b32 s26, s41, s24
	s_cselect_b32 s25, s13, s44
	s_cselect_b32 s24, s42, s43
	v_lshl_add_u64 v[214:215], s[22:23], 0, v[138:139]
	s_add_i32 m0, s19, 0xc000
	ds_read_b128 v[182:185], v152
	ds_read_b128 v[186:189], v152 offset:1024
	ds_read_b128 v[190:193], v152 offset:2048
	ds_read_b128 v[194:197], v152 offset:3072
	ds_read_b128 v[198:201], v152 offset:4096
	ds_read_b128 v[202:205], v152 offset:5120
	ds_read_b128 v[206:209], v152 offset:6144
	ds_read_b128 v[210:213], v152 offset:7168
	global_load_lds_dwordx4 v[214:215], off
	v_lshl_add_u64 v[214:215], s[22:23], 0, v[140:141]
	s_add_i32 m0, s19, 0xe000
	s_nop 0
	global_load_lds_dwordx4 v[214:215], off
	s_waitcnt vmcnt(8)
	s_waitcnt lgkmcnt(0)
	s_barrier
	s_setprio 1
	s_waitcnt lgkmcnt(0)
	v_mfma_f32_16x16x32_bf16 v[126:129], v[144:147], v[182:185], v[126:129]
	v_mfma_f32_16x16x32_bf16 v[118:121], v[158:161], v[182:185], v[118:121]
	v_mfma_f32_16x16x32_bf16 v[110:113], v[144:147], v[190:193], v[110:113]
	v_mfma_f32_16x16x32_bf16 v[102:105], v[158:161], v[190:193], v[102:105]
	v_mfma_f32_16x16x32_bf16 v[94:97], v[144:147], v[198:201], v[94:97]
	v_mfma_f32_16x16x32_bf16 v[86:89], v[158:161], v[198:201], v[86:89]
	v_mfma_f32_16x16x32_bf16 v[78:81], v[144:147], v[206:209], v[78:81]
	v_mfma_f32_16x16x32_bf16 v[70:73], v[158:161], v[206:209], v[70:73]
	v_mfma_f32_16x16x32_bf16 v[126:129], v[154:157], v[186:189], v[126:129]
	v_mfma_f32_16x16x32_bf16 v[118:121], v[162:165], v[186:189], v[118:121]
	v_mfma_f32_16x16x32_bf16 v[110:113], v[154:157], v[194:197], v[110:113]
	v_mfma_f32_16x16x32_bf16 v[102:105], v[162:165], v[194:197], v[102:105]
	v_mfma_f32_16x16x32_bf16 v[94:97], v[154:157], v[202:205], v[94:97]
	v_mfma_f32_16x16x32_bf16 v[86:89], v[162:165], v[202:205], v[86:89]
	v_mfma_f32_16x16x32_bf16 v[78:81], v[154:157], v[210:213], v[78:81]
	v_mfma_f32_16x16x32_bf16 v[70:73], v[162:165], v[210:213], v[70:73]
	v_mfma_f32_16x16x32_bf16 v[122:125], v[166:169], v[182:185], v[122:125]
	v_mfma_f32_16x16x32_bf16 v[114:117], v[174:177], v[182:185], v[114:117]
	v_mfma_f32_16x16x32_bf16 v[106:109], v[166:169], v[190:193], v[106:109]
	v_mfma_f32_16x16x32_bf16 v[98:101], v[174:177], v[190:193], v[98:101]
	v_mfma_f32_16x16x32_bf16 v[90:93], v[166:169], v[198:201], v[90:93]
	v_mfma_f32_16x16x32_bf16 v[82:85], v[174:177], v[198:201], v[82:85]
	v_mfma_f32_16x16x32_bf16 v[74:77], v[166:169], v[206:209], v[74:77]
	v_mfma_f32_16x16x32_bf16 v[66:69], v[174:177], v[206:209], v[66:69]
	v_mfma_f32_16x16x32_bf16 v[122:125], v[170:173], v[186:189], v[122:125]
	v_mfma_f32_16x16x32_bf16 v[114:117], v[178:181], v[186:189], v[114:117]
	v_mfma_f32_16x16x32_bf16 v[106:109], v[170:173], v[194:197], v[106:109]
	v_mfma_f32_16x16x32_bf16 v[98:101], v[178:181], v[194:197], v[98:101]
	v_mfma_f32_16x16x32_bf16 v[90:93], v[170:173], v[202:205], v[90:93]
	v_mfma_f32_16x16x32_bf16 v[82:85], v[178:181], v[202:205], v[82:85]
	v_mfma_f32_16x16x32_bf16 v[74:77], v[170:173], v[210:213], v[74:77]
	v_mfma_f32_16x16x32_bf16 v[66:69], v[178:181], v[210:213], v[66:69]
	s_setprio 0
	s_barrier
	s_add_i32 s46, s38, s3
	v_lshl_add_u64 v[214:215], s[24:25], 0, v[130:131]
	s_mov_b32 m0, s46
	ds_read_b128 v[182:185], v152 offset:16384
	ds_read_b128 v[186:189], v152 offset:17408
	ds_read_b128 v[190:193], v152 offset:18432
	ds_read_b128 v[194:197], v152 offset:19456
	ds_read_b128 v[198:201], v152 offset:20480
	ds_read_b128 v[202:205], v152 offset:21504
	ds_read_b128 v[206:209], v152 offset:22528
	ds_read_b128 v[210:213], v152 offset:23552
	global_load_lds_dwordx4 v[214:215], off
	s_add_i32 m0, s46, 0x2000
	s_add_u32 s46, s24, 0x80000
	v_lshl_add_u64 v[216:217], s[24:25], 0, v[134:135]
	s_addc_u32 s47, s25, 0
	s_add_i32 s48, s39, s3
	global_load_lds_dwordx4 v[216:217], off
	v_lshl_add_u64 v[218:219], s[46:47], 0, v[130:131]
	s_mov_b32 m0, s48
	v_lshl_add_u64 v[220:221], s[26:27], 0, v[136:137]
	global_load_lds_dwordx4 v[218:219], off
	v_lshl_add_u64 v[218:219], s[46:47], 0, v[134:135]
	s_add_i32 m0, s48, 0x2000
	s_nop 0
	global_load_lds_dwordx4 v[218:219], off
	v_lshl_add_u64 v[218:219], s[26:27], 0, v[132:133]
	s_mov_b32 m0, s19
	s_nop 0
	global_load_lds_dwordx4 v[218:219], off
	s_mov_b32 m0, s21
	s_nop 0
	global_load_lds_dwordx4 v[220:221], off
	s_waitcnt vmcnt(8)
	s_waitcnt lgkmcnt(0)
	s_barrier
; #define PG8_STAGE(bufoff, gbase, voff) do { _Pragma("unroll") for (int _i = 0; _i < 2; ++_i) \
;         __builtin_amdgcn_global_load_lds((const unsigned*)((const char*)(gbase) + (voff)[_i]), (PG8_LAS unsigned*)(lds + (bufoff) + ldsw + _i * 8192), 16, 0, 0); } while (0)
; #define PG8_LDA(dst, b, h) do { _Pragma("unroll") for (int m = 0; m < 4; ++m) _Pragma("unroll") for (int k = 0; k < 2; ++k) dst[m][k] = *(const PG8_LAS bf16x8*)(lds + PG8_SA(b, h) + aoff + m * 2048 + k * 1024); } while (0)
; #define PG8_LDB(dst, b, h) do { _Pragma("unroll") for (int n = 0; n < 2; ++n) _Pragma("unroll") for (int k = 0; k < 2; ++k) dst[n][k] = *(const PG8_LAS bf16x8*)(lds + PG8_SB(b, h) + boff + n * 2048 + k * 1024); } while (0)
; #define PG8_MMA(ai, bj, At, Bt) do { __builtin_amdgcn_s_setprio(1); _Pragma("unroll") for (int m = 0; m < 4; ++m) _Pragma("unroll") for (int n = 0; n < 2; ++n) _Pragma("unroll") for (int k = 0; k < 2; ++k) \
;         acc[ai][bj][m][n] = __builtin_amdgcn_mfma_f32_16x16x32_bf16(Bt[n][k], At[m][k], acc[ai][bj][m][n], 0, 0, 0); __builtin_amdgcn_s_setprio(0); } while (0)
; #define PG8_WAIT_V(n) asm volatile("s_waitcnt vmcnt(" #n ")" ::: "memory")
; #define PG8_WAIT_L(n) asm volatile("s_waitcnt lgkmcnt(" #n ")" ::: "memory")
; #define PG8_BAR __builtin_amdgcn_s_barrier()
; #define PG8_SCHED __builtin_amdgcn_sched_barrier(0)
; template <class Epi, class Sched, bool ALIGN_EPI = false, bool SP2 = false>
; __device__ __forceinline__ void gemm_phase(PG8_LAS unsigned char* lds, const Gemm g, const Sched& S, const Epi& E) {
;     ...
;             PG8_WAIT_V(8); PG8_WAIT_L(0); PG8_BAR; PG8_MMA(0, 0, At, B0); PG8_MMA(0, 1, At, B1); PG8_BAR; PG8_SCHED;
;             PG8_LDA(At, 0, 1); PG8_STAGE(PG8_SB(0, 0), b2, voffB); PG8_STAGE(PG8_SB(0, 1), b2 + hstep, voffB); PG8_STAGE(PG8_SA(0, 0), a2, voffA);
;             PG8_WAIT_V(8); PG8_WAIT_L(0); PG8_BAR; PG8_MMA(1, 0, At, B0); PG8_MMA(1, 1, At, B1); PG8_BAR; PG8_SCHED;
;             PG8_LDB(B0, 1, 0); PG8_LDB(B1, 1, 1); PG8_SCHED; PG8_LDA(At, 1, 0); PG8_STAGE(PG8_SA(0, 1), a2 + hstep, voffA);
;             PG8_WAIT_V(8); PG8_WAIT_L(0); PG8_BAR; PG8_MMA(0, 0, At, B0); PG8_MMA(0, 1, At, B1); PG8_BAR; PG8_SCHED;
	s_setprio 1
	s_waitcnt lgkmcnt(0)
	v_mfma_f32_16x16x32_bf16 v[62:65], v[144:147], v[182:185], v[62:65]
	v_mfma_f32_16x16x32_bf16 v[54:57], v[158:161], v[182:185], v[54:57]
	v_mfma_f32_16x16x32_bf16 v[46:49], v[144:147], v[190:193], v[46:49]
	v_mfma_f32_16x16x32_bf16 v[38:41], v[158:161], v[190:193], v[38:41]
	v_mfma_f32_16x16x32_bf16 v[30:33], v[144:147], v[198:201], v[30:33]
	v_mfma_f32_16x16x32_bf16 v[22:25], v[158:161], v[198:201], v[22:25]
	v_mfma_f32_16x16x32_bf16 v[14:17], v[144:147], v[206:209], v[14:17]
	v_mfma_f32_16x16x32_bf16 v[6:9], v[158:161], v[206:209], v[6:9]
	v_mfma_f32_16x16x32_bf16 v[62:65], v[154:157], v[186:189], v[62:65]
	v_mfma_f32_16x16x32_bf16 v[54:57], v[162:165], v[186:189], v[54:57]
	v_mfma_f32_16x16x32_bf16 v[46:49], v[154:157], v[194:197], v[46:49]
	v_mfma_f32_16x16x32_bf16 v[38:41], v[162:165], v[194:197], v[38:41]
	v_mfma_f32_16x16x32_bf16 v[30:33], v[154:157], v[202:205], v[30:33]
	v_mfma_f32_16x16x32_bf16 v[22:25], v[162:165], v[202:205], v[22:25]
	v_mfma_f32_16x16x32_bf16 v[14:17], v[154:157], v[210:213], v[14:17]
	v_mfma_f32_16x16x32_bf16 v[6:9], v[162:165], v[210:213], v[6:9]
	v_mfma_f32_16x16x32_bf16 v[58:61], v[166:169], v[182:185], v[58:61]
	v_mfma_f32_16x16x32_bf16 v[50:53], v[174:177], v[182:185], v[50:53]
	v_mfma_f32_16x16x32_bf16 v[42:45], v[166:169], v[190:193], v[42:45]
	v_mfma_f32_16x16x32_bf16 v[34:37], v[174:177], v[190:193], v[34:37]
	v_mfma_f32_16x16x32_bf16 v[26:29], v[166:169], v[198:201], v[26:29]
	v_mfma_f32_16x16x32_bf16 v[18:21], v[174:177], v[198:201], v[18:21]
	v_mfma_f32_16x16x32_bf16 v[10:13], v[166:169], v[206:209], v[10:13]
	v_mfma_f32_16x16x32_bf16 v[2:5], v[174:177], v[206:209], v[2:5]
	v_mfma_f32_16x16x32_bf16 v[58:61], v[170:173], v[186:189], v[58:61]
	v_mfma_f32_16x16x32_bf16 v[50:53], v[178:181], v[186:189], v[50:53]
	v_mfma_f32_16x16x32_bf16 v[42:45], v[170:173], v[194:197], v[42:45]
	v_mfma_f32_16x16x32_bf16 v[34:37], v[178:181], v[194:197], v[34:37]
	v_mfma_f32_16x16x32_bf16 v[26:29], v[170:173], v[202:205], v[26:29]
	v_mfma_f32_16x16x32_bf16 v[18:21], v[178:181], v[202:205], v[18:21]
	v_mfma_f32_16x16x32_bf16 v[10:13], v[170:173], v[210:213], v[10:13]
	v_mfma_f32_16x16x32_bf16 v[2:5], v[178:181], v[210:213], v[2:5]
	s_setprio 0
	s_barrier
	s_add_i32 s46, 0, 0x18000
	v_add_u32_e32 v153, s46, v148
	s_add_i32 s47, 0, 0x1c000
	ds_read_b128 v[144:147], v153
	ds_read_b128 v[154:157], v153 offset:1024
	ds_read_b128 v[158:161], v153 offset:2048
	ds_read_b128 v[162:165], v153 offset:3072
	v_add_u32_e32 v153, s47, v148
	ds_read_b128 v[166:169], v153
	ds_read_b128 v[170:173], v153 offset:1024
	ds_read_b128 v[174:177], v153 offset:2048
	ds_read_b128 v[178:181], v153 offset:3072
	s_add_u32 s26, s26, 0x80000
	s_addc_u32 s27, s27, 0
	s_mov_b32 m0, s33
	v_lshl_add_u64 v[222:223], s[26:27], 0, v[132:133]
	ds_read_b128 v[182:185], v152 offset:32768
	ds_read_b128 v[186:189], v152 offset:33792
	ds_read_b128 v[190:193], v152 offset:34816
	ds_read_b128 v[194:197], v152 offset:35840
	ds_read_b128 v[198:201], v152 offset:36864
	ds_read_b128 v[202:205], v152 offset:37888
	ds_read_b128 v[206:209], v152 offset:38912
	ds_read_b128 v[210:213], v152 offset:39936
	global_load_lds_dwordx4 v[222:223], off
	v_lshl_add_u64 v[222:223], s[26:27], 0, v[136:137]
	s_mov_b32 m0, s34
	s_nop 0
	global_load_lds_dwordx4 v[222:223], off
	s_waitcnt vmcnt(8)
	s_waitcnt lgkmcnt(0)
	s_barrier
	s_setprio 1
	s_waitcnt lgkmcnt(0)
	v_mfma_f32_16x16x32_bf16 v[126:129], v[144:147], v[182:185], v[126:129]
	v_mfma_f32_16x16x32_bf16 v[118:121], v[158:161], v[182:185], v[118:121]
	v_mfma_f32_16x16x32_bf16 v[110:113], v[144:147], v[190:193], v[110:113]
	v_mfma_f32_16x16x32_bf16 v[102:105], v[158:161], v[190:193], v[102:105]
	v_mfma_f32_16x16x32_bf16 v[94:97], v[144:147], v[198:201], v[94:97]
	v_mfma_f32_16x16x32_bf16 v[86:89], v[158:161], v[198:201], v[86:89]
	v_mfma_f32_16x16x32_bf16 v[78:81], v[144:147], v[206:209], v[78:81]
	v_mfma_f32_16x16x32_bf16 v[70:73], v[158:161], v[206:209], v[70:73]
	v_mfma_f32_16x16x32_bf16 v[126:129], v[154:157], v[186:189], v[126:129]
	v_mfma_f32_16x16x32_bf16 v[118:121], v[162:165], v[186:189], v[118:121]
	v_mfma_f32_16x16x32_bf16 v[110:113], v[154:157], v[194:197], v[110:113]
	v_mfma_f32_16x16x32_bf16 v[102:105], v[162:165], v[194:197], v[102:105]
	v_mfma_f32_16x16x32_bf16 v[94:97], v[154:157], v[202:205], v[94:97]
	v_mfma_f32_16x16x32_bf16 v[86:89], v[162:165], v[202:205], v[86:89]
	v_mfma_f32_16x16x32_bf16 v[78:81], v[154:157], v[210:213], v[78:81]
	v_mfma_f32_16x16x32_bf16 v[70:73], v[162:165], v[210:213], v[70:73]
	v_mfma_f32_16x16x32_bf16 v[122:125], v[166:169], v[182:185], v[122:125]
	v_mfma_f32_16x16x32_bf16 v[114:117], v[174:177], v[182:185], v[114:117]
	v_mfma_f32_16x16x32_bf16 v[106:109], v[166:169], v[190:193], v[106:109]
	v_mfma_f32_16x16x32_bf16 v[98:101], v[174:177], v[190:193], v[98:101]
	v_mfma_f32_16x16x32_bf16 v[90:93], v[166:169], v[198:201], v[90:93]
	v_mfma_f32_16x16x32_bf16 v[82:85], v[174:177], v[198:201], v[82:85]
	v_mfma_f32_16x16x32_bf16 v[74:77], v[166:169], v[206:209], v[74:77]
	v_mfma_f32_16x16x32_bf16 v[66:69], v[174:177], v[206:209], v[66:69]
	v_mfma_f32_16x16x32_bf16 v[122:125], v[170:173], v[186:189], v[122:125]
	v_mfma_f32_16x16x32_bf16 v[114:117], v[178:181], v[186:189], v[114:117]
	v_mfma_f32_16x16x32_bf16 v[106:109], v[170:173], v[194:197], v[106:109]
	v_mfma_f32_16x16x32_bf16 v[98:101], v[178:181], v[194:197], v[98:101]
	v_mfma_f32_16x16x32_bf16 v[90:93], v[170:173], v[202:205], v[90:93]
	v_mfma_f32_16x16x32_bf16 v[82:85], v[178:181], v[202:205], v[82:85]
	v_mfma_f32_16x16x32_bf16 v[74:77], v[170:173], v[210:213], v[74:77]
	v_mfma_f32_16x16x32_bf16 v[66:69], v[178:181], v[210:213], v[66:69]
	s_setprio 0
	s_barrier
; #define PG8_STAGE(bufoff, gbase, voff) do { _Pragma("unroll") for (int _i = 0; _i < 2; ++_i) \
;         __builtin_amdgcn_global_load_lds((const unsigned*)((const char*)(gbase) + (voff)[_i]), (PG8_LAS unsigned*)(lds + (bufoff) + ldsw + _i * 8192), 16, 0, 0); } while (0)
; #define PG8_LDA(dst, b, h) do { _Pragma("unroll") for (int m = 0; m < 4; ++m) _Pragma("unroll") for (int k = 0; k < 2; ++k) dst[m][k] = *(const PG8_LAS bf16x8*)(lds + PG8_SA(b, h) + aoff + m * 2048 + k * 1024); } while (0)
; #define PG8_LDB(dst, b, h) do { _Pragma("unroll") for (int n = 0; n < 2; ++n) _Pragma("unroll") for (int k = 0; k < 2; ++k) dst[n][k] = *(const PG8_LAS bf16x8*)(lds + PG8_SB(b, h) + boff + n * 2048 + k * 1024); } while (0)
; #define PG8_WAIT_V(n) asm volatile("s_waitcnt vmcnt(" #n ")" ::: "memory")
; #define PG8_WAIT_L(n) asm volatile("s_waitcnt lgkmcnt(" #n ")" ::: "memory")
; #define PG8_BAR __builtin_amdgcn_s_barrier()
; #define PG8_SCHED __builtin_amdgcn_sched_barrier(0)
; template <class Epi, class Sched, bool ALIGN_EPI = false, bool SP2 = false>
; __device__ __forceinline__ void gemm_phase(PG8_LAS unsigned char* lds, const Gemm g, const Sched& S, const Epi& E) {
;     ...
;             PG8_LDA(At, 1, 1); PG8_STAGE(PG8_SB(1, 0), b3, voffB); PG8_STAGE(PG8_SB(1, 1), b3 + hstep, voffB); PG8_STAGE(PG8_SA(1, 0), a3, voffA);
;             PG8_WAIT_V(8); PG8_WAIT_L(0); PG8_BAR; PG8_MMA(1, 0, At, B0); PG8_MMA(1, 1, At, B1); PG8_BAR; PG8_SCHED;
;             } else {
;             PG8_LDB(B0, 0, 0); PG8_SCHED; PG8_LDA(At, 0, 0); PG8_STAGE(PG8_SA(1, 1), a1 + hstep, voffA);
;             PG8_WAIT_L(8); PG8_BAR; PG8_WAIT_L(0); PG8_MMA(0, 0, At, B0); PG8_BAR; PG8_SCHED;
;             PG8_LDB(B1, 0, 1); PG8_STAGE(PG8_SB(0, 0), b2, voffB);
;             PG8_BAR; PG8_WAIT_L(0); PG8_MMA(0, 1, At, B1); PG8_BAR;
;             PG8_LDA(At, 0, 1); PG8_STAGE(PG8_SA(0, 0), a2, voffA);
;             PG8_BAR; PG8_WAIT_L(0); PG8_MMA(1, 0, At, B0); PG8_BAR; PG8_SCHED;
;             PG8_STAGE(PG8_SB(0, 1), b2 + hstep, voffB);
;             PG8_WAIT_V(6); PG8_BAR; PG8_MMA(1, 1, At, B1); PG8_BAR;
;             PG8_LDB(B0, 1, 0); PG8_SCHED; PG8_LDA(At, 1, 0); PG8_STAGE(PG8_SA(0, 1), a2 + hstep, voffA);
;             PG8_WAIT_L(8); PG8_BAR; PG8_WAIT_L(0); PG8_MMA(0, 0, At, B0); PG8_BAR; PG8_SCHED;
	s_add_i32 s26, s46, s3
	v_lshl_add_u64 v[214:215], v[214:215], 0, s[6:7]
	s_mov_b32 m0, s26
	ds_read_b128 v[182:185], v152 offset:49152
	ds_read_b128 v[186:189], v152 offset:50176
	ds_read_b128 v[190:193], v152 offset:51200
	ds_read_b128 v[194:197], v152 offset:52224
	ds_read_b128 v[198:201], v152 offset:53248
	ds_read_b128 v[202:205], v152 offset:54272
	ds_read_b128 v[206:209], v152 offset:55296
	ds_read_b128 v[210:213], v152 offset:56320
	global_load_lds_dwordx4 v[214:215], off
	s_add_i32 m0, s26, 0x2000
	s_add_u32 s24, s24, 0x80080
	v_lshl_add_u64 v[214:215], v[216:217], 0, s[6:7]
	s_addc_u32 s25, s25, 0
	s_add_i32 s26, s47, s3
	global_load_lds_dwordx4 v[214:215], off
	v_lshl_add_u64 v[214:215], s[24:25], 0, v[130:131]
	s_mov_b32 m0, s26
	s_nop 0
	global_load_lds_dwordx4 v[214:215], off
	v_lshl_add_u64 v[214:215], s[24:25], 0, v[134:135]
	s_add_i32 m0, s26, 0x2000
	s_nop 0
	global_load_lds_dwordx4 v[214:215], off
	v_lshl_add_u64 v[214:215], v[218:219], 0, s[6:7]
	s_mov_b32 m0, s36
	s_nop 0
	global_load_lds_dwordx4 v[214:215], off
	v_lshl_add_u64 v[214:215], v[220:221], 0, s[6:7]
	s_mov_b32 m0, s37
	s_nop 0
	global_load_lds_dwordx4 v[214:215], off
	s_waitcnt vmcnt(8)
	s_waitcnt lgkmcnt(0)
	s_barrier
	s_setprio 1
	s_waitcnt lgkmcnt(0)
	v_mfma_f32_16x16x32_bf16 v[62:65], v[144:147], v[182:185], v[62:65]
	v_mfma_f32_16x16x32_bf16 v[54:57], v[158:161], v[182:185], v[54:57]
	v_mfma_f32_16x16x32_bf16 v[46:49], v[144:147], v[190:193], v[46:49]
	v_mfma_f32_16x16x32_bf16 v[38:41], v[158:161], v[190:193], v[38:41]
	v_mfma_f32_16x16x32_bf16 v[30:33], v[144:147], v[198:201], v[30:33]
	v_mfma_f32_16x16x32_bf16 v[22:25], v[158:161], v[198:201], v[22:25]
	v_mfma_f32_16x16x32_bf16 v[14:17], v[144:147], v[206:209], v[14:17]
	v_mfma_f32_16x16x32_bf16 v[6:9], v[158:161], v[206:209], v[6:9]
	v_mfma_f32_16x16x32_bf16 v[62:65], v[154:157], v[186:189], v[62:65]
	v_mfma_f32_16x16x32_bf16 v[54:57], v[162:165], v[186:189], v[54:57]
	v_mfma_f32_16x16x32_bf16 v[46:49], v[154:157], v[194:197], v[46:49]
	v_mfma_f32_16x16x32_bf16 v[38:41], v[162:165], v[194:197], v[38:41]
	v_mfma_f32_16x16x32_bf16 v[30:33], v[154:157], v[202:205], v[30:33]
	v_mfma_f32_16x16x32_bf16 v[22:25], v[162:165], v[202:205], v[22:25]
	v_mfma_f32_16x16x32_bf16 v[14:17], v[154:157], v[210:213], v[14:17]
	v_mfma_f32_16x16x32_bf16 v[6:9], v[162:165], v[210:213], v[6:9]
	v_mfma_f32_16x16x32_bf16 v[58:61], v[166:169], v[182:185], v[58:61]
	v_mfma_f32_16x16x32_bf16 v[50:53], v[174:177], v[182:185], v[50:53]
	v_mfma_f32_16x16x32_bf16 v[42:45], v[166:169], v[190:193], v[42:45]
	v_mfma_f32_16x16x32_bf16 v[34:37], v[174:177], v[190:193], v[34:37]
	v_mfma_f32_16x16x32_bf16 v[26:29], v[166:169], v[198:201], v[26:29]
	v_mfma_f32_16x16x32_bf16 v[18:21], v[174:177], v[198:201], v[18:21]
	v_mfma_f32_16x16x32_bf16 v[10:13], v[166:169], v[206:209], v[10:13]
	v_mfma_f32_16x16x32_bf16 v[2:5], v[174:177], v[206:209], v[2:5]
	v_mfma_f32_16x16x32_bf16 v[58:61], v[170:173], v[186:189], v[58:61]
	v_mfma_f32_16x16x32_bf16 v[50:53], v[178:181], v[186:189], v[50:53]
	v_mfma_f32_16x16x32_bf16 v[42:45], v[170:173], v[194:197], v[42:45]
	v_mfma_f32_16x16x32_bf16 v[34:37], v[178:181], v[194:197], v[34:37]
	v_mfma_f32_16x16x32_bf16 v[26:29], v[170:173], v[202:205], v[26:29]
	v_mfma_f32_16x16x32_bf16 v[18:21], v[178:181], v[202:205], v[18:21]
	v_mfma_f32_16x16x32_bf16 v[10:13], v[170:173], v[210:213], v[10:13]
	v_mfma_f32_16x16x32_bf16 v[2:5], v[178:181], v[210:213], v[2:5]
	s_setprio 0
	s_barrier
	s_add_i32 s45, s45, 2
	s_add_u32 s22, s22, 0x100
	s_addc_u32 s23, s23, 0
	s_add_u32 s43, s43, 0x100
	s_addc_u32 s44, s44, 0
	s_cmp_gt_u32 s45, 29
	s_cbranch_scc0 .LBB0_2172
	s_and_b64 vcc, exec, s[8:9]
	s_cbranch_vccz .LBB0_2175
	s_barrier

; #define PG8_STAGE(bufoff, gbase, voff) do { _Pragma("unroll") for (int _i = 0; _i < 2; ++_i) \
;         __builtin_amdgcn_global_load_lds((const unsigned*)((const char*)(gbase) + (voff)[_i]), (PG8_LAS unsigned*)(lds + (bufoff) + ldsw + _i * 8192), 16, 0, 0); } while (0)
; #define PG8_LDA(dst, b, h) do { _Pragma("unroll") for (int m = 0; m < 4; ++m) _Pragma("unroll") for (int k = 0; k < 2; ++k) dst[m][k] = *(const PG8_LAS bf16x8*)(lds + PG8_SA(b, h) + aoff + m * 2048 + k * 1024); } while (0)
; #define PG8_LDB(dst, b, h) do { _Pragma("unroll") for (int n = 0; n < 2; ++n) _Pragma("unroll") for (int k = 0; k < 2; ++k) dst[n][k] = *(const PG8_LAS bf16x8*)(lds + PG8_SB(b, h) + boff + n * 2048 + k * 1024); } while (0)
; #define PG8_WAIT_V(n) asm volatile("s_waitcnt vmcnt(" #n ")" ::: "memory")
; #define PG8_WAIT_L(n) asm volatile("s_waitcnt lgkmcnt(" #n ")" ::: "memory")
; #define PG8_BAR __builtin_amdgcn_s_barrier()
; #define PG8_SCHED __builtin_amdgcn_sched_barrier(0)
; template <class Epi, class Sched, bool ALIGN_EPI = false, bool SP2 = false>
; __device__ __forceinline__ void gemm_phase(PG8_LAS unsigned char* lds, const Gemm g, const Sched& S, const Epi& E) {
;     ...
;         const char* nA = has_next ? (const char*)g.A + (size_t)nxt.pm * tstep + (size_t)nxt.k0 * 2 : cA; const char* nB = has_next ? (const char*)g.Bt + (size_t)nxt.pn * tstep + (size_t)nxt.k0 * 2 : cB;
;         for (int t = 0; t < nt; t += 2) {
;             const bool last = (t == nt - 2);
;             const char* a1 = cA + (size_t)(t + 1) * kstep;
;             const char* a2 = last ? nA : cA + (size_t)(t + 2) * kstep; const char* b2 = last ? nB : cB + (size_t)(t + 2) * kstep;
;             const char* a3 = a2 + kstep; const char* b3 = b2 + kstep;
;             if (last && has_next) S.a_ready(nxt);
;             if constexpr (SP2) {
;             PG8_LDB(B0, 0, 0); PG8_LDB(B1, 0, 1); PG8_SCHED; PG8_LDA(At, 0, 0); PG8_STAGE(PG8_SA(1, 1), a1 + hstep, voffA);
;             PG8_WAIT_V(8); PG8_WAIT_L(0); PG8_BAR; PG8_MMA(0, 0, At, B0); PG8_MMA(0, 1, At, B1); PG8_BAR; PG8_SCHED;
;             PG8_LDA(At, 0, 1); PG8_STAGE(PG8_SB(0, 0), b2, voffB); PG8_STAGE(PG8_SB(0, 1), b2 + hstep, voffB); PG8_STAGE(PG8_SA(0, 0), a2, voffA);
;             PG8_WAIT_V(8); PG8_WAIT_L(0); PG8_BAR; PG8_MMA(1, 0, At, B0); PG8_MMA(1, 1, At, B1); PG8_BAR; PG8_SCHED;
.LBB0_2253:
	ds_read_b128 v[150:153], v146
	ds_read_b128 v[154:157], v146 offset:1024
	ds_read_b128 v[158:161], v146 offset:2048
	ds_read_b128 v[162:165], v146 offset:3072
	ds_read_b128 v[166:169], v147
	ds_read_b128 v[170:173], v147 offset:1024
	ds_read_b128 v[174:177], v147 offset:2048
	ds_read_b128 v[178:181], v147 offset:3072
	s_add_u32 s38, s36, 0x100
	s_addc_u32 s39, s37, 0
	s_cmpk_eq_i32 s65, 0x6c
	s_cselect_b32 s43, s7, s39
	s_cselect_b32 s42, s6, s38
	s_cselect_b32 s41, s35, s64
	s_cselect_b32 s40, s34, s63
	v_lshl_add_u64 v[214:215], s[36:37], 0, v[138:139]
	s_add_i32 m0, s21, 0xc000
	ds_read_b128 v[182:185], v148
	ds_read_b128 v[186:189], v148 offset:1024
	ds_read_b128 v[190:193], v148 offset:2048
	ds_read_b128 v[194:197], v148 offset:3072
	ds_read_b128 v[198:201], v148 offset:4096
	ds_read_b128 v[202:205], v148 offset:5120
	ds_read_b128 v[206:209], v148 offset:6144
	ds_read_b128 v[210:213], v148 offset:7168
	global_load_lds_dwordx4 v[214:215], off
	v_lshl_add_u64 v[214:215], s[36:37], 0, v[140:141]
	s_add_i32 m0, s21, 0xe000
	s_nop 0
	global_load_lds_dwordx4 v[214:215], off
	s_waitcnt vmcnt(8)
	s_waitcnt lgkmcnt(0)
	s_barrier
	s_setprio 1
	s_waitcnt lgkmcnt(0)
	v_mfma_f32_16x16x32_bf16 v[126:129], v[150:153], v[182:185], v[126:129]
	v_mfma_f32_16x16x32_bf16 v[122:125], v[158:161], v[182:185], v[122:125]
	v_mfma_f32_16x16x32_bf16 v[118:121], v[150:153], v[190:193], v[118:121]
	v_mfma_f32_16x16x32_bf16 v[114:117], v[158:161], v[190:193], v[114:117]
	v_mfma_f32_16x16x32_bf16 v[102:105], v[150:153], v[198:201], v[102:105]
	v_mfma_f32_16x16x32_bf16 v[98:101], v[158:161], v[198:201], v[98:101]
	v_mfma_f32_16x16x32_bf16 v[86:89], v[150:153], v[206:209], v[86:89]
	v_mfma_f32_16x16x32_bf16 v[82:85], v[158:161], v[206:209], v[82:85]
	v_mfma_f32_16x16x32_bf16 v[126:129], v[154:157], v[186:189], v[126:129]
	v_mfma_f32_16x16x32_bf16 v[122:125], v[162:165], v[186:189], v[122:125]
	v_mfma_f32_16x16x32_bf16 v[118:121], v[154:157], v[194:197], v[118:121]
	v_mfma_f32_16x16x32_bf16 v[114:117], v[162:165], v[194:197], v[114:117]
	v_mfma_f32_16x16x32_bf16 v[102:105], v[154:157], v[202:205], v[102:105]
	v_mfma_f32_16x16x32_bf16 v[98:101], v[162:165], v[202:205], v[98:101]
	v_mfma_f32_16x16x32_bf16 v[86:89], v[154:157], v[210:213], v[86:89]
	v_mfma_f32_16x16x32_bf16 v[82:85], v[162:165], v[210:213], v[82:85]
	v_mfma_f32_16x16x32_bf16 v[110:113], v[166:169], v[182:185], v[110:113]
	v_mfma_f32_16x16x32_bf16 v[106:109], v[174:177], v[182:185], v[106:109]
	v_mfma_f32_16x16x32_bf16 v[94:97], v[166:169], v[190:193], v[94:97]
	v_mfma_f32_16x16x32_bf16 v[90:93], v[174:177], v[190:193], v[90:93]
	v_mfma_f32_16x16x32_bf16 v[78:81], v[166:169], v[198:201], v[78:81]
	v_mfma_f32_16x16x32_bf16 v[74:77], v[174:177], v[198:201], v[74:77]
	v_mfma_f32_16x16x32_bf16 v[70:73], v[166:169], v[206:209], v[70:73]
	v_mfma_f32_16x16x32_bf16 v[66:69], v[174:177], v[206:209], v[66:69]
	v_mfma_f32_16x16x32_bf16 v[110:113], v[170:173], v[186:189], v[110:113]
	v_mfma_f32_16x16x32_bf16 v[106:109], v[178:181], v[186:189], v[106:109]
	v_mfma_f32_16x16x32_bf16 v[94:97], v[170:173], v[194:197], v[94:97]
	v_mfma_f32_16x16x32_bf16 v[90:93], v[178:181], v[194:197], v[90:93]
	v_mfma_f32_16x16x32_bf16 v[78:81], v[170:173], v[202:205], v[78:81]
	v_mfma_f32_16x16x32_bf16 v[74:77], v[178:181], v[202:205], v[74:77]
	v_mfma_f32_16x16x32_bf16 v[70:73], v[170:173], v[210:213], v[70:73]
	v_mfma_f32_16x16x32_bf16 v[66:69], v[178:181], v[210:213], v[66:69]
	s_setprio 0
	s_barrier
	s_add_i32 s36, s11, s49
	v_lshl_add_u64 v[214:215], s[40:41], 0, v[130:131]
	s_mov_b32 m0, s36
	ds_read_b128 v[182:185], v148 offset:16384
	ds_read_b128 v[186:189], v148 offset:17408
	ds_read_b128 v[190:193], v148 offset:18432
	ds_read_b128 v[194:197], v148 offset:19456
	ds_read_b128 v[198:201], v148 offset:20480
	ds_read_b128 v[202:205], v148 offset:21504
	ds_read_b128 v[206:209], v148 offset:22528
	ds_read_b128 v[210:213], v148 offset:23552
	global_load_lds_dwordx4 v[214:215], off
	s_add_i32 m0, s36, 0x2000
	s_add_u32 s36, s40, 0x1c0000
	v_lshl_add_u64 v[216:217], s[40:41], 0, v[136:137]
	s_addc_u32 s37, s41, 0
	s_add_i32 s66, s57, s49
	global_load_lds_dwordx4 v[216:217], off
	v_lshl_add_u64 v[218:219], s[36:37], 0, v[130:131]
	s_mov_b32 m0, s66
	v_lshl_add_u64 v[220:221], s[42:43], 0, v[134:135]
	global_load_lds_dwordx4 v[218:219], off
	v_lshl_add_u64 v[218:219], s[36:37], 0, v[136:137]
	s_add_i32 m0, s66, 0x2000
	s_nop 0
	global_load_lds_dwordx4 v[218:219], off
	v_lshl_add_u64 v[218:219], s[42:43], 0, v[132:133]
	s_mov_b32 m0, s21
	s_nop 0
	global_load_lds_dwordx4 v[218:219], off
	s_mov_b32 m0, s51
	s_nop 0
	global_load_lds_dwordx4 v[220:221], off
	s_waitcnt vmcnt(8)
	s_waitcnt lgkmcnt(0)
	s_barrier
; #define PG8_STAGE(bufoff, gbase, voff) do { _Pragma("unroll") for (int _i = 0; _i < 2; ++_i) \
;         __builtin_amdgcn_global_load_lds((const unsigned*)((const char*)(gbase) + (voff)[_i]), (PG8_LAS unsigned*)(lds + (bufoff) + ldsw + _i * 8192), 16, 0, 0); } while (0)
; #define PG8_LDA(dst, b, h) do { _Pragma("unroll") for (int m = 0; m < 4; ++m) _Pragma("unroll") for (int k = 0; k < 2; ++k) dst[m][k] = *(const PG8_LAS bf16x8*)(lds + PG8_SA(b, h) + aoff + m * 2048 + k * 1024); } while (0)
; #define PG8_LDB(dst, b, h) do { _Pragma("unroll") for (int n = 0; n < 2; ++n) _Pragma("unroll") for (int k = 0; k < 2; ++k) dst[n][k] = *(const PG8_LAS bf16x8*)(lds + PG8_SB(b, h) + boff + n * 2048 + k * 1024); } while (0)
; #define PG8_MMA(ai, bj, At, Bt) do { __builtin_amdgcn_s_setprio(1); _Pragma("unroll") for (int m = 0; m < 4; ++m) _Pragma("unroll") for (int n = 0; n < 2; ++n) _Pragma("unroll") for (int k = 0; k < 2; ++k) \
;         acc[ai][bj][m][n] = __builtin_amdgcn_mfma_f32_16x16x32_bf16(Bt[n][k], At[m][k], acc[ai][bj][m][n], 0, 0, 0); __builtin_amdgcn_s_setprio(0); } while (0)
; #define PG8_WAIT_V(n) asm volatile("s_waitcnt vmcnt(" #n ")" ::: "memory")
; #define PG8_WAIT_L(n) asm volatile("s_waitcnt lgkmcnt(" #n ")" ::: "memory")
; #define PG8_BAR __builtin_amdgcn_s_barrier()
; #define PG8_SCHED __builtin_amdgcn_sched_barrier(0)
; template <class Epi, class Sched, bool ALIGN_EPI = false, bool SP2 = false>
; __device__ __forceinline__ void gemm_phase(PG8_LAS unsigned char* lds, const Gemm g, const Sched& S, const Epi& E) {
;     ...
;             PG8_WAIT_V(8); PG8_WAIT_L(0); PG8_BAR; PG8_MMA(0, 0, At, B0); PG8_MMA(0, 1, At, B1); PG8_BAR; PG8_SCHED;
;             PG8_LDA(At, 0, 1); PG8_STAGE(PG8_SB(0, 0), b2, voffB); PG8_STAGE(PG8_SB(0, 1), b2 + hstep, voffB); PG8_STAGE(PG8_SA(0, 0), a2, voffA);
;             PG8_WAIT_V(8); PG8_WAIT_L(0); PG8_BAR; PG8_MMA(1, 0, At, B0); PG8_MMA(1, 1, At, B1); PG8_BAR; PG8_SCHED;
;             PG8_LDB(B0, 1, 0); PG8_LDB(B1, 1, 1); PG8_SCHED; PG8_LDA(At, 1, 0); PG8_STAGE(PG8_SA(0, 1), a2 + hstep, voffA);
;             PG8_WAIT_V(8); PG8_WAIT_L(0); PG8_BAR; PG8_MMA(0, 0, At, B0); PG8_MMA(0, 1, At, B1); PG8_BAR; PG8_SCHED;
	s_setprio 1
	s_waitcnt lgkmcnt(0)
	v_mfma_f32_16x16x32_bf16 v[62:65], v[150:153], v[182:185], v[62:65]
	v_mfma_f32_16x16x32_bf16 v[58:61], v[158:161], v[182:185], v[58:61]
	v_mfma_f32_16x16x32_bf16 v[54:57], v[150:153], v[190:193], v[54:57]
	v_mfma_f32_16x16x32_bf16 v[50:53], v[158:161], v[190:193], v[50:53]
	v_mfma_f32_16x16x32_bf16 v[38:41], v[150:153], v[198:201], v[38:41]
	v_mfma_f32_16x16x32_bf16 v[34:37], v[158:161], v[198:201], v[34:37]
	v_mfma_f32_16x16x32_bf16 v[22:25], v[150:153], v[206:209], v[22:25]
	v_mfma_f32_16x16x32_bf16 v[18:21], v[158:161], v[206:209], v[18:21]
	v_mfma_f32_16x16x32_bf16 v[62:65], v[154:157], v[186:189], v[62:65]
	v_mfma_f32_16x16x32_bf16 v[58:61], v[162:165], v[186:189], v[58:61]
	v_mfma_f32_16x16x32_bf16 v[54:57], v[154:157], v[194:197], v[54:57]
	v_mfma_f32_16x16x32_bf16 v[50:53], v[162:165], v[194:197], v[50:53]
	v_mfma_f32_16x16x32_bf16 v[38:41], v[154:157], v[202:205], v[38:41]
	v_mfma_f32_16x16x32_bf16 v[34:37], v[162:165], v[202:205], v[34:37]
	v_mfma_f32_16x16x32_bf16 v[22:25], v[154:157], v[210:213], v[22:25]
	v_mfma_f32_16x16x32_bf16 v[18:21], v[162:165], v[210:213], v[18:21]
	v_mfma_f32_16x16x32_bf16 v[46:49], v[166:169], v[182:185], v[46:49]
	v_mfma_f32_16x16x32_bf16 v[42:45], v[174:177], v[182:185], v[42:45]
	v_mfma_f32_16x16x32_bf16 v[30:33], v[166:169], v[190:193], v[30:33]
	v_mfma_f32_16x16x32_bf16 v[26:29], v[174:177], v[190:193], v[26:29]
	v_mfma_f32_16x16x32_bf16 v[14:17], v[166:169], v[198:201], v[14:17]
	v_mfma_f32_16x16x32_bf16 v[10:13], v[174:177], v[198:201], v[10:13]
	v_mfma_f32_16x16x32_bf16 v[6:9], v[166:169], v[206:209], v[6:9]
	v_mfma_f32_16x16x32_bf16 v[2:5], v[174:177], v[206:209], v[2:5]
	v_mfma_f32_16x16x32_bf16 v[46:49], v[170:173], v[186:189], v[46:49]
	v_mfma_f32_16x16x32_bf16 v[42:45], v[178:181], v[186:189], v[42:45]
	v_mfma_f32_16x16x32_bf16 v[30:33], v[170:173], v[194:197], v[30:33]
	v_mfma_f32_16x16x32_bf16 v[26:29], v[178:181], v[194:197], v[26:29]
	v_mfma_f32_16x16x32_bf16 v[14:17], v[170:173], v[202:205], v[14:17]
	v_mfma_f32_16x16x32_bf16 v[10:13], v[178:181], v[202:205], v[10:13]
	v_mfma_f32_16x16x32_bf16 v[6:9], v[170:173], v[210:213], v[6:9]
	v_mfma_f32_16x16x32_bf16 v[2:5], v[178:181], v[210:213], v[2:5]
	s_setprio 0
	s_barrier
	s_add_i32 s66, 0, 0x18000
	v_add_u32_e32 v149, s66, v144
	s_add_i32 s67, 0, 0x1c000
	ds_read_b128 v[150:153], v149
	ds_read_b128 v[154:157], v149 offset:1024
	ds_read_b128 v[158:161], v149 offset:2048
	ds_read_b128 v[162:165], v149 offset:3072
	v_add_u32_e32 v149, s67, v144
	ds_read_b128 v[166:169], v149
	ds_read_b128 v[170:173], v149 offset:1024
	ds_read_b128 v[174:177], v149 offset:2048
	ds_read_b128 v[178:181], v149 offset:3072
	s_add_u32 s36, s42, 0x1c0000
	s_addc_u32 s37, s43, 0
	s_mov_b32 m0, s52
	v_lshl_add_u64 v[222:223], s[36:37], 0, v[132:133]
	ds_read_b128 v[182:185], v148 offset:32768
	ds_read_b128 v[186:189], v148 offset:33792
	ds_read_b128 v[190:193], v148 offset:34816
	ds_read_b128 v[194:197], v148 offset:35840
	ds_read_b128 v[198:201], v148 offset:36864
	ds_read_b128 v[202:205], v148 offset:37888
	ds_read_b128 v[206:209], v148 offset:38912
	ds_read_b128 v[210:213], v148 offset:39936
	global_load_lds_dwordx4 v[222:223], off
	v_lshl_add_u64 v[222:223], s[36:37], 0, v[134:135]
	s_mov_b32 m0, s53
	s_nop 0
	global_load_lds_dwordx4 v[222:223], off
	s_waitcnt vmcnt(8)
	s_waitcnt lgkmcnt(0)
	s_barrier
	s_setprio 1
	s_waitcnt lgkmcnt(0)
	v_mfma_f32_16x16x32_bf16 v[126:129], v[150:153], v[182:185], v[126:129]
	v_mfma_f32_16x16x32_bf16 v[122:125], v[158:161], v[182:185], v[122:125]
	v_mfma_f32_16x16x32_bf16 v[118:121], v[150:153], v[190:193], v[118:121]
	v_mfma_f32_16x16x32_bf16 v[114:117], v[158:161], v[190:193], v[114:117]
	v_mfma_f32_16x16x32_bf16 v[102:105], v[150:153], v[198:201], v[102:105]
	v_mfma_f32_16x16x32_bf16 v[98:101], v[158:161], v[198:201], v[98:101]
	v_mfma_f32_16x16x32_bf16 v[86:89], v[150:153], v[206:209], v[86:89]
	v_mfma_f32_16x16x32_bf16 v[82:85], v[158:161], v[206:209], v[82:85]
	v_mfma_f32_16x16x32_bf16 v[126:129], v[154:157], v[186:189], v[126:129]
	v_mfma_f32_16x16x32_bf16 v[122:125], v[162:165], v[186:189], v[122:125]
	v_mfma_f32_16x16x32_bf16 v[118:121], v[154:157], v[194:197], v[118:121]
	v_mfma_f32_16x16x32_bf16 v[114:117], v[162:165], v[194:197], v[114:117]
	v_mfma_f32_16x16x32_bf16 v[102:105], v[154:157], v[202:205], v[102:105]
	v_mfma_f32_16x16x32_bf16 v[98:101], v[162:165], v[202:205], v[98:101]
	v_mfma_f32_16x16x32_bf16 v[86:89], v[154:157], v[210:213], v[86:89]
	v_mfma_f32_16x16x32_bf16 v[82:85], v[162:165], v[210:213], v[82:85]
	v_mfma_f32_16x16x32_bf16 v[110:113], v[166:169], v[182:185], v[110:113]
	v_mfma_f32_16x16x32_bf16 v[106:109], v[174:177], v[182:185], v[106:109]
	v_mfma_f32_16x16x32_bf16 v[94:97], v[166:169], v[190:193], v[94:97]
	v_mfma_f32_16x16x32_bf16 v[90:93], v[174:177], v[190:193], v[90:93]
	v_mfma_f32_16x16x32_bf16 v[78:81], v[166:169], v[198:201], v[78:81]
	v_mfma_f32_16x16x32_bf16 v[74:77], v[174:177], v[198:201], v[74:77]
	v_mfma_f32_16x16x32_bf16 v[70:73], v[166:169], v[206:209], v[70:73]
	v_mfma_f32_16x16x32_bf16 v[66:69], v[174:177], v[206:209], v[66:69]
	v_mfma_f32_16x16x32_bf16 v[110:113], v[170:173], v[186:189], v[110:113]
	v_mfma_f32_16x16x32_bf16 v[106:109], v[178:181], v[186:189], v[106:109]
	v_mfma_f32_16x16x32_bf16 v[94:97], v[170:173], v[194:197], v[94:97]
	v_mfma_f32_16x16x32_bf16 v[90:93], v[178:181], v[194:197], v[90:93]
	v_mfma_f32_16x16x32_bf16 v[78:81], v[170:173], v[202:205], v[78:81]
	v_mfma_f32_16x16x32_bf16 v[74:77], v[178:181], v[202:205], v[74:77]
	v_mfma_f32_16x16x32_bf16 v[70:73], v[170:173], v[210:213], v[70:73]
	v_mfma_f32_16x16x32_bf16 v[66:69], v[178:181], v[210:213], v[66:69]
	s_setprio 0
	s_barrier
; #define PG8_STAGE(bufoff, gbase, voff) do { _Pragma("unroll") for (int _i = 0; _i < 2; ++_i) \
;         __builtin_amdgcn_global_load_lds((const unsigned*)((const char*)(gbase) + (voff)[_i]), (PG8_LAS unsigned*)(lds + (bufoff) + ldsw + _i * 8192), 16, 0, 0); } while (0)
; #define PG8_LDA(dst, b, h) do { _Pragma("unroll") for (int m = 0; m < 4; ++m) _Pragma("unroll") for (int k = 0; k < 2; ++k) dst[m][k] = *(const PG8_LAS bf16x8*)(lds + PG8_SA(b, h) + aoff + m * 2048 + k * 1024); } while (0)
; #define PG8_LDB(dst, b, h) do { _Pragma("unroll") for (int n = 0; n < 2; ++n) _Pragma("unroll") for (int k = 0; k < 2; ++k) dst[n][k] = *(const PG8_LAS bf16x8*)(lds + PG8_SB(b, h) + boff + n * 2048 + k * 1024); } while (0)
; #define PG8_WAIT_V(n) asm volatile("s_waitcnt vmcnt(" #n ")" ::: "memory")
; #define PG8_WAIT_L(n) asm volatile("s_waitcnt lgkmcnt(" #n ")" ::: "memory")
; #define PG8_BAR __builtin_amdgcn_s_barrier()
; #define PG8_SCHED __builtin_amdgcn_sched_barrier(0)
; template <class Epi, class Sched, bool ALIGN_EPI = false, bool SP2 = false>
; __device__ __forceinline__ void gemm_phase(PG8_LAS unsigned char* lds, const Gemm g, const Sched& S, const Epi& E) {
;     ...
;             PG8_LDA(At, 1, 1); PG8_STAGE(PG8_SB(1, 0), b3, voffB); PG8_STAGE(PG8_SB(1, 1), b3 + hstep, voffB); PG8_STAGE(PG8_SA(1, 0), a3, voffA);
;             PG8_WAIT_V(8); PG8_WAIT_L(0); PG8_BAR; PG8_MMA(1, 0, At, B0); PG8_MMA(1, 1, At, B1); PG8_BAR; PG8_SCHED;
;             } else {
;             PG8_LDB(B0, 0, 0); PG8_SCHED; PG8_LDA(At, 0, 0); PG8_STAGE(PG8_SA(1, 1), a1 + hstep, voffA);
;             PG8_WAIT_L(8); PG8_BAR; PG8_WAIT_L(0); PG8_MMA(0, 0, At, B0); PG8_BAR; PG8_SCHED;
;             PG8_LDB(B1, 0, 1); PG8_STAGE(PG8_SB(0, 0), b2, voffB);
;             PG8_BAR; PG8_WAIT_L(0); PG8_MMA(0, 1, At, B1); PG8_BAR;
;             PG8_LDA(At, 0, 1); PG8_STAGE(PG8_SA(0, 0), a2, voffA);
;             PG8_BAR; PG8_WAIT_L(0); PG8_MMA(1, 0, At, B0); PG8_BAR; PG8_SCHED;
;             PG8_STAGE(PG8_SB(0, 1), b2 + hstep, voffB);
;             PG8_WAIT_V(6); PG8_BAR; PG8_MMA(1, 1, At, B1); PG8_BAR;
;             PG8_LDB(B0, 1, 0); PG8_SCHED; PG8_LDA(At, 1, 0); PG8_STAGE(PG8_SA(0, 1), a2 + hstep, voffA);
;             PG8_WAIT_L(8); PG8_BAR; PG8_WAIT_L(0); PG8_MMA(0, 0, At, B0); PG8_BAR; PG8_SCHED;
	s_add_i32 s36, s66, s49
	v_lshl_add_u64 v[214:215], v[214:215], 0, s[18:19]
	s_mov_b32 m0, s36
	ds_read_b128 v[182:185], v148 offset:49152
	ds_read_b128 v[186:189], v148 offset:50176
	ds_read_b128 v[190:193], v148 offset:51200
	ds_read_b128 v[194:197], v148 offset:52224
	ds_read_b128 v[198:201], v148 offset:53248
	ds_read_b128 v[202:205], v148 offset:54272
	ds_read_b128 v[206:209], v148 offset:55296
	ds_read_b128 v[210:213], v148 offset:56320
	global_load_lds_dwordx4 v[214:215], off
	s_add_i32 m0, s36, 0x2000
	s_add_u32 s36, s40, 0x1c0080
	v_lshl_add_u64 v[214:215], v[216:217], 0, s[18:19]
	s_addc_u32 s37, s41, 0
	s_add_i32 s40, s67, s49
	global_load_lds_dwordx4 v[214:215], off
	v_lshl_add_u64 v[214:215], s[36:37], 0, v[130:131]
	s_mov_b32 m0, s40
	s_nop 0
	global_load_lds_dwordx4 v[214:215], off
	v_lshl_add_u64 v[214:215], s[36:37], 0, v[136:137]
	s_add_i32 m0, s40, 0x2000
	s_nop 0
	global_load_lds_dwordx4 v[214:215], off
	v_lshl_add_u64 v[214:215], v[218:219], 0, s[18:19]
	s_mov_b32 m0, s55
	s_nop 0
	global_load_lds_dwordx4 v[214:215], off
	v_lshl_add_u64 v[214:215], v[220:221], 0, s[18:19]
	s_mov_b32 m0, s56
	s_nop 0
	global_load_lds_dwordx4 v[214:215], off
	s_waitcnt vmcnt(8)
	s_waitcnt lgkmcnt(0)
	s_barrier
	s_setprio 1
	s_waitcnt lgkmcnt(0)
	v_mfma_f32_16x16x32_bf16 v[62:65], v[150:153], v[182:185], v[62:65]
	v_mfma_f32_16x16x32_bf16 v[58:61], v[158:161], v[182:185], v[58:61]
	v_mfma_f32_16x16x32_bf16 v[54:57], v[150:153], v[190:193], v[54:57]
	v_mfma_f32_16x16x32_bf16 v[50:53], v[158:161], v[190:193], v[50:53]
	v_mfma_f32_16x16x32_bf16 v[38:41], v[150:153], v[198:201], v[38:41]
	v_mfma_f32_16x16x32_bf16 v[34:37], v[158:161], v[198:201], v[34:37]
	v_mfma_f32_16x16x32_bf16 v[22:25], v[150:153], v[206:209], v[22:25]
	v_mfma_f32_16x16x32_bf16 v[18:21], v[158:161], v[206:209], v[18:21]
	v_mfma_f32_16x16x32_bf16 v[62:65], v[154:157], v[186:189], v[62:65]
	v_mfma_f32_16x16x32_bf16 v[58:61], v[162:165], v[186:189], v[58:61]
	v_mfma_f32_16x16x32_bf16 v[54:57], v[154:157], v[194:197], v[54:57]
	v_mfma_f32_16x16x32_bf16 v[50:53], v[162:165], v[194:197], v[50:53]
	v_mfma_f32_16x16x32_bf16 v[38:41], v[154:157], v[202:205], v[38:41]
	v_mfma_f32_16x16x32_bf16 v[34:37], v[162:165], v[202:205], v[34:37]
	v_mfma_f32_16x16x32_bf16 v[22:25], v[154:157], v[210:213], v[22:25]
	v_mfma_f32_16x16x32_bf16 v[18:21], v[162:165], v[210:213], v[18:21]
	v_mfma_f32_16x16x32_bf16 v[46:49], v[166:169], v[182:185], v[46:49]
	v_mfma_f32_16x16x32_bf16 v[42:45], v[174:177], v[182:185], v[42:45]
	v_mfma_f32_16x16x32_bf16 v[30:33], v[166:169], v[190:193], v[30:33]
	v_mfma_f32_16x16x32_bf16 v[26:29], v[174:177], v[190:193], v[26:29]
	v_mfma_f32_16x16x32_bf16 v[14:17], v[166:169], v[198:201], v[14:17]
	v_mfma_f32_16x16x32_bf16 v[10:13], v[174:177], v[198:201], v[10:13]
	v_mfma_f32_16x16x32_bf16 v[6:9], v[166:169], v[206:209], v[6:9]
	v_mfma_f32_16x16x32_bf16 v[2:5], v[174:177], v[206:209], v[2:5]
	v_mfma_f32_16x16x32_bf16 v[46:49], v[170:173], v[186:189], v[46:49]
	v_mfma_f32_16x16x32_bf16 v[42:45], v[178:181], v[186:189], v[42:45]
	v_mfma_f32_16x16x32_bf16 v[30:33], v[170:173], v[194:197], v[30:33]
	v_mfma_f32_16x16x32_bf16 v[26:29], v[178:181], v[194:197], v[26:29]
	v_mfma_f32_16x16x32_bf16 v[14:17], v[170:173], v[202:205], v[14:17]
	v_mfma_f32_16x16x32_bf16 v[10:13], v[178:181], v[202:205], v[10:13]
	v_mfma_f32_16x16x32_bf16 v[6:9], v[170:173], v[210:213], v[6:9]
	v_mfma_f32_16x16x32_bf16 v[2:5], v[178:181], v[210:213], v[2:5]
	s_setprio 0
	s_barrier
	s_add_i32 s65, s65, 2
	s_add_u32 s63, s63, 0x100
	s_addc_u32 s64, s64, 0
	s_cmpk_gt_u32 s65, 0x6d
	s_mov_b64 s[36:37], s[38:39]
	s_cbranch_scc0 .LBB0_2253
	s_and_b64 vcc, exec, s[22:23]
	s_cbranch_vccz .LBB0_2256
	s_barrier

; #define PG8_STAGE(bufoff, gbase, voff) do { _Pragma("unroll") for (int _i = 0; _i < 2; ++_i) \
;         __builtin_amdgcn_global_load_lds((const unsigned*)((const char*)(gbase) + (voff)[_i]), (PG8_LAS unsigned*)(lds + (bufoff) + ldsw + _i * 8192), 16, 0, 0); } while (0)
; #define PG8_LDA(dst, b, h) do { _Pragma("unroll") for (int m = 0; m < 4; ++m) _Pragma("unroll") for (int k = 0; k < 2; ++k) dst[m][k] = *(const PG8_LAS bf16x8*)(lds + PG8_SA(b, h) + aoff + m * 2048 + k * 1024); } while (0)
; #define PG8_LDB(dst, b, h) do { _Pragma("unroll") for (int n = 0; n < 2; ++n) _Pragma("unroll") for (int k = 0; k < 2; ++k) dst[n][k] = *(const PG8_LAS bf16x8*)(lds + PG8_SB(b, h) + boff + n * 2048 + k * 1024); } while (0)
; #define PG8_WAIT_V(n) asm volatile("s_waitcnt vmcnt(" #n ")" ::: "memory")
; #define PG8_WAIT_L(n) asm volatile("s_waitcnt lgkmcnt(" #n ")" ::: "memory")
; #define PG8_BAR __builtin_amdgcn_s_barrier()
; #define PG8_SCHED __builtin_amdgcn_sched_barrier(0)
; template <class Epi, class Sched, bool ALIGN_EPI = false, bool SP2 = false>
; __device__ __forceinline__ void gemm_phase(PG8_LAS unsigned char* lds, const Gemm g, const Sched& S, const Epi& E) {
;     ...
;         const char* nA = has_next ? (const char*)g.A + (size_t)nxt.pm * tstep + (size_t)nxt.k0 * 2 : cA; const char* nB = has_next ? (const char*)g.Bt + (size_t)nxt.pn * tstep + (size_t)nxt.k0 * 2 : cB;
;         for (int t = 0; t < nt; t += 2) {
;             const bool last = (t == nt - 2);
;             const char* a1 = cA + (size_t)(t + 1) * kstep;
;             const char* a2 = last ? nA : cA + (size_t)(t + 2) * kstep; const char* b2 = last ? nB : cB + (size_t)(t + 2) * kstep;
;             const char* a3 = a2 + kstep; const char* b3 = b2 + kstep;
;             if (last && has_next) S.a_ready(nxt);
;             if constexpr (SP2) {
;             PG8_LDB(B0, 0, 0); PG8_LDB(B1, 0, 1); PG8_SCHED; PG8_LDA(At, 0, 0); PG8_STAGE(PG8_SA(1, 1), a1 + hstep, voffA);
;             PG8_WAIT_V(8); PG8_WAIT_L(0); PG8_BAR; PG8_MMA(0, 0, At, B0); PG8_MMA(0, 1, At, B1); PG8_BAR; PG8_SCHED;
;             PG8_LDA(At, 0, 1); PG8_STAGE(PG8_SB(0, 0), b2, voffB); PG8_STAGE(PG8_SB(0, 1), b2 + hstep, voffB); PG8_STAGE(PG8_SA(0, 0), a2, voffA);
;             PG8_WAIT_V(8); PG8_WAIT_L(0); PG8_BAR; PG8_MMA(1, 0, At, B0); PG8_MMA(1, 1, At, B1); PG8_BAR; PG8_SCHED;
.LBB0_2279:
	ds_read_b128 v[146:149], v142
	ds_read_b128 v[150:153], v142 offset:1024
	ds_read_b128 v[154:157], v142 offset:2048
	ds_read_b128 v[158:161], v142 offset:3072
	ds_read_b128 v[162:165], v143
	ds_read_b128 v[166:169], v143 offset:1024
	ds_read_b128 v[170:173], v143 offset:2048
	ds_read_b128 v[174:177], v143 offset:3072
	s_add_i32 s60, s27, 2
	s_add_u32 s34, s30, 0x100
	s_addc_u32 s35, s31, 0
	s_cmp_eq_u32 s52, s27
	s_cselect_b32 s39, s5, s35
	s_cselect_b32 s38, s4, s34
	s_cselect_b32 s37, s29, s25
	s_cselect_b32 s36, s28, s23
	v_lshl_add_u64 v[210:211], s[30:31], 0, v[138:139]
	s_add_i32 m0, s7, 0xc000
	ds_read_b128 v[178:181], v144
	ds_read_b128 v[182:185], v144 offset:1024
	ds_read_b128 v[186:189], v144 offset:2048
	ds_read_b128 v[190:193], v144 offset:3072
	ds_read_b128 v[194:197], v144 offset:4096
	ds_read_b128 v[198:201], v144 offset:5120
	ds_read_b128 v[202:205], v144 offset:6144
	ds_read_b128 v[206:209], v144 offset:7168
	global_load_lds_dwordx4 v[210:211], off
	v_lshl_add_u64 v[210:211], s[30:31], 0, v[140:141]
	s_add_i32 m0, s7, 0xe000
	s_nop 0
	global_load_lds_dwordx4 v[210:211], off
	s_waitcnt vmcnt(8)
	s_waitcnt lgkmcnt(0)
	s_barrier
	s_setprio 1
	s_waitcnt lgkmcnt(0)
	v_mfma_f32_16x16x32_bf16 v[126:129], v[146:149], v[178:181], v[126:129]
	v_mfma_f32_16x16x32_bf16 v[122:125], v[154:157], v[178:181], v[122:125]
	v_mfma_f32_16x16x32_bf16 v[118:121], v[146:149], v[186:189], v[118:121]
	v_mfma_f32_16x16x32_bf16 v[114:117], v[154:157], v[186:189], v[114:117]
	v_mfma_f32_16x16x32_bf16 v[110:113], v[146:149], v[194:197], v[110:113]
	v_mfma_f32_16x16x32_bf16 v[102:105], v[154:157], v[194:197], v[102:105]
	v_mfma_f32_16x16x32_bf16 v[94:97], v[146:149], v[202:205], v[94:97]
	v_mfma_f32_16x16x32_bf16 v[86:89], v[154:157], v[202:205], v[86:89]
	v_mfma_f32_16x16x32_bf16 v[126:129], v[150:153], v[182:185], v[126:129]
	v_mfma_f32_16x16x32_bf16 v[122:125], v[158:161], v[182:185], v[122:125]
	v_mfma_f32_16x16x32_bf16 v[118:121], v[150:153], v[190:193], v[118:121]
	v_mfma_f32_16x16x32_bf16 v[114:117], v[158:161], v[190:193], v[114:117]
	v_mfma_f32_16x16x32_bf16 v[110:113], v[150:153], v[198:201], v[110:113]
	v_mfma_f32_16x16x32_bf16 v[102:105], v[158:161], v[198:201], v[102:105]
	v_mfma_f32_16x16x32_bf16 v[94:97], v[150:153], v[206:209], v[94:97]
	v_mfma_f32_16x16x32_bf16 v[86:89], v[158:161], v[206:209], v[86:89]
	v_mfma_f32_16x16x32_bf16 v[106:109], v[162:165], v[178:181], v[106:109]
	v_mfma_f32_16x16x32_bf16 v[98:101], v[170:173], v[178:181], v[98:101]
	v_mfma_f32_16x16x32_bf16 v[90:93], v[162:165], v[186:189], v[90:93]
	v_mfma_f32_16x16x32_bf16 v[82:85], v[170:173], v[186:189], v[82:85]
	v_mfma_f32_16x16x32_bf16 v[78:81], v[162:165], v[194:197], v[78:81]
	v_mfma_f32_16x16x32_bf16 v[74:77], v[170:173], v[194:197], v[74:77]
	v_mfma_f32_16x16x32_bf16 v[70:73], v[162:165], v[202:205], v[70:73]
	v_mfma_f32_16x16x32_bf16 v[66:69], v[170:173], v[202:205], v[66:69]
	v_mfma_f32_16x16x32_bf16 v[106:109], v[166:169], v[182:185], v[106:109]
	v_mfma_f32_16x16x32_bf16 v[98:101], v[174:177], v[182:185], v[98:101]
	v_mfma_f32_16x16x32_bf16 v[90:93], v[166:169], v[190:193], v[90:93]
	v_mfma_f32_16x16x32_bf16 v[82:85], v[174:177], v[190:193], v[82:85]
	v_mfma_f32_16x16x32_bf16 v[78:81], v[166:169], v[198:201], v[78:81]
	v_mfma_f32_16x16x32_bf16 v[74:77], v[174:177], v[198:201], v[74:77]
	v_mfma_f32_16x16x32_bf16 v[70:73], v[166:169], v[206:209], v[70:73]
	v_mfma_f32_16x16x32_bf16 v[66:69], v[174:177], v[206:209], v[66:69]
	s_setprio 0
	s_barrier
	s_add_i32 s27, s54, s41
	v_lshl_add_u64 v[210:211], s[36:37], 0, v[132:133]
	s_mov_b32 m0, s27
	ds_read_b128 v[178:181], v144 offset:16384
	ds_read_b128 v[182:185], v144 offset:17408
	ds_read_b128 v[186:189], v144 offset:18432
	ds_read_b128 v[190:193], v144 offset:19456
	ds_read_b128 v[194:197], v144 offset:20480
	ds_read_b128 v[198:201], v144 offset:21504
	ds_read_b128 v[202:205], v144 offset:22528
	ds_read_b128 v[206:209], v144 offset:23552
	global_load_lds_dwordx4 v[210:211], off
	s_add_i32 m0, s27, 0x2000
	s_add_u32 s30, s36, 0x1c0000
	v_lshl_add_u64 v[212:213], s[36:37], 0, v[134:135]
	s_addc_u32 s31, s37, 0
	s_add_i32 s27, s55, s41
	global_load_lds_dwordx4 v[212:213], off
	v_lshl_add_u64 v[214:215], s[30:31], 0, v[132:133]
	s_mov_b32 m0, s27
	v_lshl_add_u64 v[216:217], s[38:39], 0, v[134:135]
	global_load_lds_dwordx4 v[214:215], off
	v_lshl_add_u64 v[214:215], s[30:31], 0, v[134:135]
	s_add_i32 m0, s27, 0x2000
	s_nop 0
	global_load_lds_dwordx4 v[214:215], off
	v_lshl_add_u64 v[214:215], s[38:39], 0, v[132:133]
	s_mov_b32 m0, s7
	s_nop 0
	global_load_lds_dwordx4 v[214:215], off
	s_mov_b32 m0, s17
	s_nop 0
	global_load_lds_dwordx4 v[216:217], off
	s_waitcnt vmcnt(8)
	s_waitcnt lgkmcnt(0)
	s_barrier
; #define PG8_STAGE(bufoff, gbase, voff) do { _Pragma("unroll") for (int _i = 0; _i < 2; ++_i) \
;         __builtin_amdgcn_global_load_lds((const unsigned*)((const char*)(gbase) + (voff)[_i]), (PG8_LAS unsigned*)(lds + (bufoff) + ldsw + _i * 8192), 16, 0, 0); } while (0)
; #define PG8_LDA(dst, b, h) do { _Pragma("unroll") for (int m = 0; m < 4; ++m) _Pragma("unroll") for (int k = 0; k < 2; ++k) dst[m][k] = *(const PG8_LAS bf16x8*)(lds + PG8_SA(b, h) + aoff + m * 2048 + k * 1024); } while (0)
; #define PG8_LDB(dst, b, h) do { _Pragma("unroll") for (int n = 0; n < 2; ++n) _Pragma("unroll") for (int k = 0; k < 2; ++k) dst[n][k] = *(const PG8_LAS bf16x8*)(lds + PG8_SB(b, h) + boff + n * 2048 + k * 1024); } while (0)
; #define PG8_MMA(ai, bj, At, Bt) do { __builtin_amdgcn_s_setprio(1); _Pragma("unroll") for (int m = 0; m < 4; ++m) _Pragma("unroll") for (int n = 0; n < 2; ++n) _Pragma("unroll") for (int k = 0; k < 2; ++k) \
;         acc[ai][bj][m][n] = __builtin_amdgcn_mfma_f32_16x16x32_bf16(Bt[n][k], At[m][k], acc[ai][bj][m][n], 0, 0, 0); __builtin_amdgcn_s_setprio(0); } while (0)
; #define PG8_WAIT_V(n) asm volatile("s_waitcnt vmcnt(" #n ")" ::: "memory")
; #define PG8_WAIT_L(n) asm volatile("s_waitcnt lgkmcnt(" #n ")" ::: "memory")
; #define PG8_BAR __builtin_amdgcn_s_barrier()
; #define PG8_SCHED __builtin_amdgcn_sched_barrier(0)
; template <class Epi, class Sched, bool ALIGN_EPI = false, bool SP2 = false>
; __device__ __forceinline__ void gemm_phase(PG8_LAS unsigned char* lds, const Gemm g, const Sched& S, const Epi& E) {
;     ...
;             PG8_WAIT_V(8); PG8_WAIT_L(0); PG8_BAR; PG8_MMA(1, 0, At, B0); PG8_MMA(1, 1, At, B1); PG8_BAR; PG8_SCHED;
;             PG8_LDB(B0, 1, 0); PG8_LDB(B1, 1, 1); PG8_SCHED; PG8_LDA(At, 1, 0); PG8_STAGE(PG8_SA(0, 1), a2 + hstep, voffA);
;             PG8_WAIT_V(8); PG8_WAIT_L(0); PG8_BAR; PG8_MMA(0, 0, At, B0); PG8_MMA(0, 1, At, B1); PG8_BAR; PG8_SCHED;
	s_setprio 1
	s_waitcnt lgkmcnt(0)
	v_mfma_f32_16x16x32_bf16 v[62:65], v[146:149], v[178:181], v[62:65]
	v_mfma_f32_16x16x32_bf16 v[58:61], v[154:157], v[178:181], v[58:61]
	v_mfma_f32_16x16x32_bf16 v[54:57], v[146:149], v[186:189], v[54:57]
	v_mfma_f32_16x16x32_bf16 v[50:53], v[154:157], v[186:189], v[50:53]
	v_mfma_f32_16x16x32_bf16 v[46:49], v[146:149], v[194:197], v[46:49]
	v_mfma_f32_16x16x32_bf16 v[38:41], v[154:157], v[194:197], v[38:41]
	v_mfma_f32_16x16x32_bf16 v[30:33], v[146:149], v[202:205], v[30:33]
	v_mfma_f32_16x16x32_bf16 v[22:25], v[154:157], v[202:205], v[22:25]
	v_mfma_f32_16x16x32_bf16 v[62:65], v[150:153], v[182:185], v[62:65]
	v_mfma_f32_16x16x32_bf16 v[58:61], v[158:161], v[182:185], v[58:61]
	v_mfma_f32_16x16x32_bf16 v[54:57], v[150:153], v[190:193], v[54:57]
	v_mfma_f32_16x16x32_bf16 v[50:53], v[158:161], v[190:193], v[50:53]
	v_mfma_f32_16x16x32_bf16 v[46:49], v[150:153], v[198:201], v[46:49]
	v_mfma_f32_16x16x32_bf16 v[38:41], v[158:161], v[198:201], v[38:41]
	v_mfma_f32_16x16x32_bf16 v[30:33], v[150:153], v[206:209], v[30:33]
	v_mfma_f32_16x16x32_bf16 v[22:25], v[158:161], v[206:209], v[22:25]
	v_mfma_f32_16x16x32_bf16 v[42:45], v[162:165], v[178:181], v[42:45]
	v_mfma_f32_16x16x32_bf16 v[34:37], v[170:173], v[178:181], v[34:37]
	v_mfma_f32_16x16x32_bf16 v[26:29], v[162:165], v[186:189], v[26:29]
	v_mfma_f32_16x16x32_bf16 v[18:21], v[170:173], v[186:189], v[18:21]
	v_mfma_f32_16x16x32_bf16 v[14:17], v[162:165], v[194:197], v[14:17]
	v_mfma_f32_16x16x32_bf16 v[10:13], v[170:173], v[194:197], v[10:13]
	v_mfma_f32_16x16x32_bf16 v[6:9], v[162:165], v[202:205], v[6:9]
	v_mfma_f32_16x16x32_bf16 v[2:5], v[170:173], v[202:205], v[2:5]
	v_mfma_f32_16x16x32_bf16 v[42:45], v[166:169], v[182:185], v[42:45]
	v_mfma_f32_16x16x32_bf16 v[34:37], v[174:177], v[182:185], v[34:37]
	v_mfma_f32_16x16x32_bf16 v[26:29], v[166:169], v[190:193], v[26:29]
	v_mfma_f32_16x16x32_bf16 v[18:21], v[174:177], v[190:193], v[18:21]
	v_mfma_f32_16x16x32_bf16 v[14:17], v[166:169], v[198:201], v[14:17]
	v_mfma_f32_16x16x32_bf16 v[10:13], v[174:177], v[198:201], v[10:13]
	v_mfma_f32_16x16x32_bf16 v[6:9], v[166:169], v[206:209], v[6:9]
	v_mfma_f32_16x16x32_bf16 v[2:5], v[174:177], v[206:209], v[2:5]
	s_setprio 0
	s_barrier
	s_add_i32 s27, 0, 0x18000
	s_add_i32 s61, 0, 0x1c000
	v_add_u32_e32 v158, s27, v1
	v_add_u32_e32 v174, s61, v1
	ds_read_b128 v[146:149], v158
	ds_read_b128 v[150:153], v158 offset:1024
	ds_read_b128 v[154:157], v158 offset:2048
	ds_read_b128 v[158:161], v158 offset:3072
	ds_read_b128 v[162:165], v174
	ds_read_b128 v[166:169], v174 offset:1024
	ds_read_b128 v[170:173], v174 offset:2048
	ds_read_b128 v[174:177], v174 offset:3072
	s_add_u32 s30, s38, 0x1c0000
	s_addc_u32 s31, s39, 0
	s_mov_b32 m0, s44
	v_lshl_add_u64 v[218:219], s[30:31], 0, v[132:133]
	ds_read_b128 v[178:181], v144 offset:32768
	ds_read_b128 v[182:185], v144 offset:33792
	ds_read_b128 v[186:189], v144 offset:34816
	ds_read_b128 v[190:193], v144 offset:35840
	ds_read_b128 v[194:197], v144 offset:36864
	ds_read_b128 v[198:201], v144 offset:37888
	ds_read_b128 v[202:205], v144 offset:38912
	ds_read_b128 v[206:209], v144 offset:39936
	global_load_lds_dwordx4 v[218:219], off
	v_lshl_add_u64 v[218:219], s[30:31], 0, v[134:135]
	s_mov_b32 m0, s45
	s_nop 0
	global_load_lds_dwordx4 v[218:219], off
	s_waitcnt vmcnt(8)
	s_waitcnt lgkmcnt(0)
	s_barrier
	s_setprio 1
	s_waitcnt lgkmcnt(0)
	v_mfma_f32_16x16x32_bf16 v[126:129], v[146:149], v[178:181], v[126:129]
	v_mfma_f32_16x16x32_bf16 v[122:125], v[154:157], v[178:181], v[122:125]
	v_mfma_f32_16x16x32_bf16 v[118:121], v[146:149], v[186:189], v[118:121]
	v_mfma_f32_16x16x32_bf16 v[114:117], v[154:157], v[186:189], v[114:117]
	v_mfma_f32_16x16x32_bf16 v[110:113], v[146:149], v[194:197], v[110:113]
	v_mfma_f32_16x16x32_bf16 v[102:105], v[154:157], v[194:197], v[102:105]
	v_mfma_f32_16x16x32_bf16 v[94:97], v[146:149], v[202:205], v[94:97]
	v_mfma_f32_16x16x32_bf16 v[86:89], v[154:157], v[202:205], v[86:89]
	v_mfma_f32_16x16x32_bf16 v[126:129], v[150:153], v[182:185], v[126:129]
	v_mfma_f32_16x16x32_bf16 v[122:125], v[158:161], v[182:185], v[122:125]
	v_mfma_f32_16x16x32_bf16 v[118:121], v[150:153], v[190:193], v[118:121]
	v_mfma_f32_16x16x32_bf16 v[114:117], v[158:161], v[190:193], v[114:117]
	v_mfma_f32_16x16x32_bf16 v[110:113], v[150:153], v[198:201], v[110:113]
	v_mfma_f32_16x16x32_bf16 v[102:105], v[158:161], v[198:201], v[102:105]
	v_mfma_f32_16x16x32_bf16 v[94:97], v[150:153], v[206:209], v[94:97]
	v_mfma_f32_16x16x32_bf16 v[86:89], v[158:161], v[206:209], v[86:89]
	v_mfma_f32_16x16x32_bf16 v[106:109], v[162:165], v[178:181], v[106:109]
	v_mfma_f32_16x16x32_bf16 v[98:101], v[170:173], v[178:181], v[98:101]
	v_mfma_f32_16x16x32_bf16 v[90:93], v[162:165], v[186:189], v[90:93]
	v_mfma_f32_16x16x32_bf16 v[82:85], v[170:173], v[186:189], v[82:85]
	v_mfma_f32_16x16x32_bf16 v[78:81], v[162:165], v[194:197], v[78:81]
	v_mfma_f32_16x16x32_bf16 v[74:77], v[170:173], v[194:197], v[74:77]
	v_mfma_f32_16x16x32_bf16 v[70:73], v[162:165], v[202:205], v[70:73]
	v_mfma_f32_16x16x32_bf16 v[66:69], v[170:173], v[202:205], v[66:69]
	v_mfma_f32_16x16x32_bf16 v[106:109], v[166:169], v[182:185], v[106:109]
	v_mfma_f32_16x16x32_bf16 v[98:101], v[174:177], v[182:185], v[98:101]
	v_mfma_f32_16x16x32_bf16 v[90:93], v[166:169], v[190:193], v[90:93]
	v_mfma_f32_16x16x32_bf16 v[82:85], v[174:177], v[190:193], v[82:85]
	v_mfma_f32_16x16x32_bf16 v[78:81], v[166:169], v[198:201], v[78:81]
	v_mfma_f32_16x16x32_bf16 v[74:77], v[174:177], v[198:201], v[74:77]
	v_mfma_f32_16x16x32_bf16 v[70:73], v[166:169], v[206:209], v[70:73]
	v_mfma_f32_16x16x32_bf16 v[66:69], v[174:177], v[206:209], v[66:69]
	s_setprio 0
	s_barrier
; #define PG8_STAGE(bufoff, gbase, voff) do { _Pragma("unroll") for (int _i = 0; _i < 2; ++_i) \
;         __builtin_amdgcn_global_load_lds((const unsigned*)((const char*)(gbase) + (voff)[_i]), (PG8_LAS unsigned*)(lds + (bufoff) + ldsw + _i * 8192), 16, 0, 0); } while (0)
; #define PG8_LDA(dst, b, h) do { _Pragma("unroll") for (int m = 0; m < 4; ++m) _Pragma("unroll") for (int k = 0; k < 2; ++k) dst[m][k] = *(const PG8_LAS bf16x8*)(lds + PG8_SA(b, h) + aoff + m * 2048 + k * 1024); } while (0)
; #define PG8_MMA(ai, bj, At, Bt) do { __builtin_amdgcn_s_setprio(1); _Pragma("unroll") for (int m = 0; m < 4; ++m) _Pragma("unroll") for (int n = 0; n < 2; ++n) _Pragma("unroll") for (int k = 0; k < 2; ++k) \
;         acc[ai][bj][m][n] = __builtin_amdgcn_mfma_f32_16x16x32_bf16(Bt[n][k], At[m][k], acc[ai][bj][m][n], 0, 0, 0); __builtin_amdgcn_s_setprio(0); } while (0)
; #define PG8_WAIT_V(n) asm volatile("s_waitcnt vmcnt(" #n ")" ::: "memory")
; #define PG8_WAIT_L(n) asm volatile("s_waitcnt lgkmcnt(" #n ")" ::: "memory")
; #define PG8_BAR __builtin_amdgcn_s_barrier()
; #define PG8_SCHED __builtin_amdgcn_sched_barrier(0)
; template <class Epi, class Sched, bool ALIGN_EPI = false, bool SP2 = false>
; __device__ __forceinline__ void gemm_phase(PG8_LAS unsigned char* lds, const Gemm g, const Sched& S, const Epi& E) {
;     ...
;             PG8_LDA(At, 1, 1); PG8_STAGE(PG8_SB(1, 0), b3, voffB); PG8_STAGE(PG8_SB(1, 1), b3 + hstep, voffB); PG8_STAGE(PG8_SA(1, 0), a3, voffA);
;             PG8_WAIT_V(8); PG8_WAIT_L(0); PG8_BAR; PG8_MMA(1, 0, At, B0); PG8_MMA(1, 1, At, B1); PG8_BAR; PG8_SCHED;
;     ...
;         if constexpr (ALIGN_EPI) { if (wr == 0) PG8_BAR; }
	s_add_i32 s27, s27, s41
	v_lshl_add_u64 v[210:211], v[210:211], 0, s[18:19]
	s_mov_b32 m0, s27
	ds_read_b128 v[178:181], v144 offset:49152
	ds_read_b128 v[182:185], v144 offset:50176
	ds_read_b128 v[186:189], v144 offset:51200
	ds_read_b128 v[190:193], v144 offset:52224
	ds_read_b128 v[194:197], v144 offset:53248
	ds_read_b128 v[198:201], v144 offset:54272
	ds_read_b128 v[202:205], v144 offset:55296
	ds_read_b128 v[206:209], v144 offset:56320
	global_load_lds_dwordx4 v[210:211], off
	s_add_i32 m0, s27, 0x2000
	s_add_u32 s30, s36, 0x1c0080
	v_lshl_add_u64 v[210:211], v[212:213], 0, s[18:19]
	s_addc_u32 s31, s37, 0
	s_add_i32 s27, s61, s41
	global_load_lds_dwordx4 v[210:211], off
	v_lshl_add_u64 v[210:211], s[30:31], 0, v[132:133]
	s_mov_b32 m0, s27
	s_nop 0
	global_load_lds_dwordx4 v[210:211], off
	v_lshl_add_u64 v[210:211], s[30:31], 0, v[134:135]
	s_add_i32 m0, s27, 0x2000
	s_nop 0
	global_load_lds_dwordx4 v[210:211], off
	v_lshl_add_u64 v[210:211], v[214:215], 0, s[18:19]
	s_mov_b32 m0, s48
	s_nop 0
	global_load_lds_dwordx4 v[210:211], off
	v_lshl_add_u64 v[210:211], v[216:217], 0, s[18:19]
	s_mov_b32 m0, s49
	s_nop 0
	global_load_lds_dwordx4 v[210:211], off
	s_waitcnt vmcnt(8)
	s_waitcnt lgkmcnt(0)
	s_barrier
	s_setprio 1
	s_waitcnt lgkmcnt(0)
	v_mfma_f32_16x16x32_bf16 v[62:65], v[146:149], v[178:181], v[62:65]
	v_mfma_f32_16x16x32_bf16 v[58:61], v[154:157], v[178:181], v[58:61]
	v_mfma_f32_16x16x32_bf16 v[54:57], v[146:149], v[186:189], v[54:57]
	v_mfma_f32_16x16x32_bf16 v[50:53], v[154:157], v[186:189], v[50:53]
	v_mfma_f32_16x16x32_bf16 v[46:49], v[146:149], v[194:197], v[46:49]
	v_mfma_f32_16x16x32_bf16 v[38:41], v[154:157], v[194:197], v[38:41]
	v_mfma_f32_16x16x32_bf16 v[30:33], v[146:149], v[202:205], v[30:33]
	v_mfma_f32_16x16x32_bf16 v[22:25], v[154:157], v[202:205], v[22:25]
	v_mfma_f32_16x16x32_bf16 v[62:65], v[150:153], v[182:185], v[62:65]
	v_mfma_f32_16x16x32_bf16 v[58:61], v[158:161], v[182:185], v[58:61]
	v_mfma_f32_16x16x32_bf16 v[54:57], v[150:153], v[190:193], v[54:57]
	v_mfma_f32_16x16x32_bf16 v[50:53], v[158:161], v[190:193], v[50:53]
	v_mfma_f32_16x16x32_bf16 v[46:49], v[150:153], v[198:201], v[46:49]
	v_mfma_f32_16x16x32_bf16 v[38:41], v[158:161], v[198:201], v[38:41]
	v_mfma_f32_16x16x32_bf16 v[30:33], v[150:153], v[206:209], v[30:33]
	v_mfma_f32_16x16x32_bf16 v[22:25], v[158:161], v[206:209], v[22:25]
	v_mfma_f32_16x16x32_bf16 v[42:45], v[162:165], v[178:181], v[42:45]
	v_mfma_f32_16x16x32_bf16 v[34:37], v[170:173], v[178:181], v[34:37]
	v_mfma_f32_16x16x32_bf16 v[26:29], v[162:165], v[186:189], v[26:29]
	v_mfma_f32_16x16x32_bf16 v[18:21], v[170:173], v[186:189], v[18:21]
	v_mfma_f32_16x16x32_bf16 v[14:17], v[162:165], v[194:197], v[14:17]
	v_mfma_f32_16x16x32_bf16 v[10:13], v[170:173], v[194:197], v[10:13]
	v_mfma_f32_16x16x32_bf16 v[6:9], v[162:165], v[202:205], v[6:9]
	v_mfma_f32_16x16x32_bf16 v[2:5], v[170:173], v[202:205], v[2:5]
	v_mfma_f32_16x16x32_bf16 v[42:45], v[166:169], v[182:185], v[42:45]
	v_mfma_f32_16x16x32_bf16 v[34:37], v[174:177], v[182:185], v[34:37]
	v_mfma_f32_16x16x32_bf16 v[26:29], v[166:169], v[190:193], v[26:29]
	v_mfma_f32_16x16x32_bf16 v[18:21], v[174:177], v[190:193], v[18:21]
	v_mfma_f32_16x16x32_bf16 v[14:17], v[166:169], v[198:201], v[14:17]
	v_mfma_f32_16x16x32_bf16 v[10:13], v[174:177], v[198:201], v[10:13]
	v_mfma_f32_16x16x32_bf16 v[6:9], v[166:169], v[206:209], v[6:9]
	v_mfma_f32_16x16x32_bf16 v[2:5], v[174:177], v[206:209], v[2:5]
	s_setprio 0
	s_barrier
	s_add_u32 s23, s23, 0x100
	s_addc_u32 s25, s25, 0
	s_cmp_ge_u32 s60, s47
	s_mov_b64 s[30:31], s[34:35]
	s_mov_b32 s27, s60
	s_cbranch_scc0 .LBB0_2279
	s_and_b64 vcc, exec, s[20:21]
	s_cbranch_vccz .LBB0_2282
	s_barrier
